# removed no-op lgkmcnt waits and mid-section setprio toggles inside MFMA sections of all 14 GEMM K-loops
# speedup vs baseline: 1.0017x; 1.0017x over previous
; #define PG8_STAGE(bufoff, gbase, voff) do { _Pragma("unroll") for (int _i = 0; _i < 2; ++_i) { unsigned keep_; \
;         asm volatile("s_mov_b32 %0, m0\n\ts_mov_b32 m0, %3\n\ts_nop 0\n\tglobal_load_lds_dwordx4 %1, %2\n\ts_mov_b32 m0, %0" : "=&s"(keep_) : "v"((voff)[_i]), "s"((const char*)(gbase)), "s"(ldsbase + (unsigned)((bufoff) + _i * 8192)) : "memory"); } } while (0)
; #define PG8_WAIT_V(n) asm volatile("s_waitcnt vmcnt(" #n ")" ::: "memory")
; #define PG8_WAIT_L(n) asm volatile("s_waitcnt lgkmcnt(" #n ")" ::: "memory")
; #define PG8_BAR __builtin_amdgcn_s_barrier()
; #define PG8_SCHED __builtin_amdgcn_sched_barrier(0)
;     DI int nt(const Unit& u) const { return (u.aux & 8) ? PLED / 64 : ((u.aux & 4) ? (D_ / 2) / 64 : D_ / 64); }
; template <class Epi, class Sched, bool ALIGN_EPI, bool FP8 = false>
; DI void gemm_phase(LAS unsigned char* lds, const Gemm g, const Sched& S, const Epi& E) {
;     ...
;             const bool last = (t == nt - 2);
;             const char* a1 = cA + (size_t)(t + 1) * kstep;
;             const char* a2 = last ? nA : cA + (size_t)(t + 2) * kstep; const char* b2 = last ? nB : cB + (size_t)(t + 2) * kstep;
;             const char* a3 = a2 + kstep; const char* b3 = b2 + kstep;
;             PG8_LDB(B0, 0, 0); PG8_LDB(B1, 0, 1); PG8_SCHED; PG8_LDA(At, 0, 0); PG8_STAGE(PG8_SA(1, 1), a1 + hstepA, voffA);
;             PG8_WAIT_V(8); PG8_WAIT_L(0); PG8_BAR; PG8_MMA(0, 0, At, B0); PG8_MMA(0, 1, At, B1); PG8_BAR; PG8_SCHED;
;             PG8_LDA(At, 0, 1); PG8_STAGE(PG8_SB(0, 0), b2, voffB); PG8_STAGE(PG8_SB(0, 1), b2 + hstepB, voffB); PG8_STAGE(PG8_SA(0, 0), a2, voffA);
;             PG8_WAIT_V(8); PG8_WAIT_L(0); PG8_BAR; PG8_MMA(1, 0, At, B0); PG8_MMA(1, 1, At, B1); PG8_BAR; PG8_SCHED;
.LBB0_255:
	s_add_i32 s53, s51, 2
	s_add_u32 s42, s18, s56
	s_addc_u32 s43, s19, s57
	s_add_u32 s58, s42, 0x100
	v_add_u32_e32 v130, 0x10000, v157
	s_addc_u32 s59, s43, 0
	ds_read_b128 v[146:149], v130
	ds_read_b128 v[150:153], v130 offset:1024
	ds_read_b128 v[160:163], v130 offset:2048
	ds_read_b128 v[164:167], v130 offset:3072
	v_add_u32_e32 v130, 0x14000, v157
	s_add_u32 s60, s22, s56
	ds_read_b128 v[168:171], v130
	ds_read_b128 v[172:175], v130 offset:1024
	ds_read_b128 v[176:179], v130 offset:2048
	ds_read_b128 v[180:183], v130 offset:3072
	s_addc_u32 s61, s23, s57
	s_add_u32 s60, s60, 0x100
	s_addc_u32 s61, s61, 0
	s_cmp_eq_u32 s20, s51
	s_cselect_b32 s62, s8, s58
	s_cselect_b32 s63, s9, s59
	s_cselect_b32 s60, s54, s60
	s_cselect_b32 s61, s55, s61
	s_add_u32 s58, s62, 0x80
	s_addc_u32 s59, s63, 0
	ds_read_b128 v[184:187], v158
	ds_read_b128 v[188:191], v158 offset:1024
	ds_read_b128 v[192:195], v158 offset:2048
	ds_read_b128 v[196:199], v158 offset:3072
	ds_read_b128 v[200:203], v158 offset:4096
	ds_read_b128 v[204:207], v158 offset:5120
	ds_read_b128 v[208:211], v158 offset:6144
	ds_read_b128 v[212:215], v158 offset:7168
	s_add_u32 s42, s42, 0x80080
	s_addc_u32 s43, s43, 0
	s_mov_b32 s51, m0
	s_mov_b32 m0, s89
	s_nop 0
	global_load_lds_dwordx4 v129, s[42:43]
	s_mov_b32 m0, s51
	s_nop 0
	s_mov_b32 s51, m0
	s_mov_b32 m0, s90
	s_nop 0
	global_load_lds_dwordx4 v154, s[42:43]
	s_mov_b32 m0, s51
	s_waitcnt vmcnt(8)
	s_waitcnt lgkmcnt(0)
	s_barrier
	s_setprio 1
	v_mfma_f32_16x16x32_bf16 v[124:127], v[146:149], v[184:187], v[124:127]
	v_mfma_f32_16x16x32_bf16 v[120:123], v[160:163], v[184:187], v[120:123]
	v_mfma_f32_16x16x32_bf16 v[116:119], v[146:149], v[192:195], v[116:119]
	v_mfma_f32_16x16x32_bf16 v[112:115], v[160:163], v[192:195], v[112:115]
	v_mfma_f32_16x16x32_bf16 v[108:111], v[146:149], v[200:203], v[108:111]
	v_mfma_f32_16x16x32_bf16 v[104:107], v[160:163], v[200:203], v[104:107]
	v_mfma_f32_16x16x32_bf16 v[100:103], v[146:149], v[208:211], v[100:103]
	v_mfma_f32_16x16x32_bf16 v[96:99], v[160:163], v[208:211], v[96:99]
	v_mfma_f32_16x16x32_bf16 v[124:127], v[150:153], v[188:191], v[124:127]
	v_mfma_f32_16x16x32_bf16 v[120:123], v[164:167], v[188:191], v[120:123]
	v_mfma_f32_16x16x32_bf16 v[116:119], v[150:153], v[196:199], v[116:119]
	v_mfma_f32_16x16x32_bf16 v[112:115], v[164:167], v[196:199], v[112:115]
	v_mfma_f32_16x16x32_bf16 v[108:111], v[150:153], v[204:207], v[108:111]
	v_mfma_f32_16x16x32_bf16 v[104:107], v[164:167], v[204:207], v[104:107]
	v_mfma_f32_16x16x32_bf16 v[100:103], v[150:153], v[212:215], v[100:103]
	v_mfma_f32_16x16x32_bf16 v[96:99], v[164:167], v[212:215], v[96:99]
	v_mfma_f32_16x16x32_bf16 v[92:95], v[168:171], v[184:187], v[92:95]
	v_mfma_f32_16x16x32_bf16 v[88:91], v[176:179], v[184:187], v[88:91]
	v_mfma_f32_16x16x32_bf16 v[84:87], v[168:171], v[192:195], v[84:87]
	v_mfma_f32_16x16x32_bf16 v[80:83], v[176:179], v[192:195], v[80:83]
	v_mfma_f32_16x16x32_bf16 v[76:79], v[168:171], v[200:203], v[76:79]
	v_mfma_f32_16x16x32_bf16 v[72:75], v[176:179], v[200:203], v[72:75]
	v_mfma_f32_16x16x32_bf16 v[68:71], v[168:171], v[208:211], v[68:71]
	v_mfma_f32_16x16x32_bf16 v[64:67], v[176:179], v[208:211], v[64:67]
	v_mfma_f32_16x16x32_bf16 v[92:95], v[172:175], v[188:191], v[92:95]
	v_mfma_f32_16x16x32_bf16 v[88:91], v[180:183], v[188:191], v[88:91]
	v_mfma_f32_16x16x32_bf16 v[84:87], v[172:175], v[196:199], v[84:87]
	v_mfma_f32_16x16x32_bf16 v[80:83], v[180:183], v[196:199], v[80:83]
	v_mfma_f32_16x16x32_bf16 v[76:79], v[172:175], v[204:207], v[76:79]
	v_mfma_f32_16x16x32_bf16 v[72:75], v[180:183], v[204:207], v[72:75]
	v_mfma_f32_16x16x32_bf16 v[68:71], v[172:175], v[212:215], v[68:71]
	v_mfma_f32_16x16x32_bf16 v[64:67], v[180:183], v[212:215], v[64:67]
	s_setprio 0
	s_barrier
	ds_read_b128 v[184:187], v158 offset:16384
	ds_read_b128 v[188:191], v158 offset:17408
	ds_read_b128 v[192:195], v158 offset:18432
	ds_read_b128 v[196:199], v158 offset:19456
	ds_read_b128 v[200:203], v158 offset:20480
	ds_read_b128 v[204:207], v158 offset:21504
	ds_read_b128 v[208:211], v158 offset:22528
	ds_read_b128 v[212:215], v158 offset:23552
	s_mov_b32 s42, m0
	s_mov_b32 m0, s17
	s_nop 0
	global_load_lds_dwordx4 v145, s[60:61]
	s_mov_b32 m0, s42
	s_nop 0
	s_mov_b32 s42, m0
	s_mov_b32 m0, s68
	s_nop 0
	global_load_lds_dwordx4 v155, s[60:61]
	s_mov_b32 m0, s42
	s_add_u32 s42, s60, 0x80000
	s_addc_u32 s43, s61, 0
	s_mov_b32 s51, m0
	s_mov_b32 m0, s69
	s_nop 0
	global_load_lds_dwordx4 v145, s[42:43]
	s_mov_b32 m0, s51
	s_nop 0
	s_mov_b32 s51, m0
	s_mov_b32 m0, s70
	s_nop 0
	global_load_lds_dwordx4 v155, s[42:43]
	s_mov_b32 m0, s51
	s_mov_b32 s42, m0
	s_mov_b32 m0, s15
	s_nop 0
	global_load_lds_dwordx4 v129, s[62:63]
	s_mov_b32 m0, s42
	s_nop 0
	s_mov_b32 s42, m0
	s_mov_b32 m0, s71
	s_nop 0
	global_load_lds_dwordx4 v154, s[62:63]
	s_mov_b32 m0, s42
	s_waitcnt vmcnt(8)
	s_waitcnt lgkmcnt(0)
	s_barrier
; #define PG8_STAGE(bufoff, gbase, voff) do { _Pragma("unroll") for (int _i = 0; _i < 2; ++_i) { unsigned keep_; \
;         asm volatile("s_mov_b32 %0, m0\n\ts_mov_b32 m0, %3\n\ts_nop 0\n\tglobal_load_lds_dwordx4 %1, %2\n\ts_mov_b32 m0, %0" : "=&s"(keep_) : "v"((voff)[_i]), "s"((const char*)(gbase)), "s"(ldsbase + (unsigned)((bufoff) + _i * 8192)) : "memory"); } } while (0)
; #define PG8_WAIT_V(n) asm volatile("s_waitcnt vmcnt(" #n ")" ::: "memory")
; #define PG8_WAIT_L(n) asm volatile("s_waitcnt lgkmcnt(" #n ")" ::: "memory")
; #define PG8_BAR __builtin_amdgcn_s_barrier()
; #define PG8_SCHED __builtin_amdgcn_sched_barrier(0)
; template <class Epi, class Sched, bool ALIGN_EPI, bool FP8 = false>
; DI void gemm_phase(LAS unsigned char* lds, const Gemm g, const Sched& S, const Epi& E) {
;     ...
;             PG8_WAIT_V(8); PG8_WAIT_L(0); PG8_BAR; PG8_MMA(1, 0, At, B0); PG8_MMA(1, 1, At, B1); PG8_BAR; PG8_SCHED;
;             PG8_LDB(B0, 1, 0); PG8_LDB(B1, 1, 1); PG8_SCHED; PG8_LDA(At, 1, 0); PG8_STAGE(PG8_SA(0, 1), a2 + hstepA, voffA);
;             PG8_WAIT_V(8); PG8_WAIT_L(0); PG8_BAR; PG8_MMA(0, 0, At, B0); PG8_MMA(0, 1, At, B1); PG8_BAR; PG8_SCHED;
	s_setprio 1
	v_mfma_f32_16x16x32_bf16 v[60:63], v[146:149], v[184:187], v[60:63]
	v_mfma_f32_16x16x32_bf16 v[56:59], v[160:163], v[184:187], v[56:59]
	v_mfma_f32_16x16x32_bf16 v[52:55], v[146:149], v[192:195], v[52:55]
	v_mfma_f32_16x16x32_bf16 v[48:51], v[160:163], v[192:195], v[48:51]
	v_mfma_f32_16x16x32_bf16 v[44:47], v[146:149], v[200:203], v[44:47]
	v_mfma_f32_16x16x32_bf16 v[40:43], v[160:163], v[200:203], v[40:43]
	v_mfma_f32_16x16x32_bf16 v[36:39], v[146:149], v[208:211], v[36:39]
	v_mfma_f32_16x16x32_bf16 v[32:35], v[160:163], v[208:211], v[32:35]
	v_mfma_f32_16x16x32_bf16 v[60:63], v[150:153], v[188:191], v[60:63]
	v_mfma_f32_16x16x32_bf16 v[56:59], v[164:167], v[188:191], v[56:59]
	v_mfma_f32_16x16x32_bf16 v[52:55], v[150:153], v[196:199], v[52:55]
	v_mfma_f32_16x16x32_bf16 v[48:51], v[164:167], v[196:199], v[48:51]
	v_mfma_f32_16x16x32_bf16 v[44:47], v[150:153], v[204:207], v[44:47]
	v_mfma_f32_16x16x32_bf16 v[40:43], v[164:167], v[204:207], v[40:43]
	v_mfma_f32_16x16x32_bf16 v[36:39], v[150:153], v[212:215], v[36:39]
	v_mfma_f32_16x16x32_bf16 v[32:35], v[164:167], v[212:215], v[32:35]
	v_mfma_f32_16x16x32_bf16 v[28:31], v[168:171], v[184:187], v[28:31]
	v_mfma_f32_16x16x32_bf16 v[24:27], v[176:179], v[184:187], v[24:27]
	v_mfma_f32_16x16x32_bf16 v[20:23], v[168:171], v[192:195], v[20:23]
	v_mfma_f32_16x16x32_bf16 v[16:19], v[176:179], v[192:195], v[16:19]
	v_mfma_f32_16x16x32_bf16 v[12:15], v[168:171], v[200:203], v[12:15]
	v_mfma_f32_16x16x32_bf16 v[8:11], v[176:179], v[200:203], v[8:11]
	v_mfma_f32_16x16x32_bf16 v[4:7], v[168:171], v[208:211], v[4:7]
	v_mfma_f32_16x16x32_bf16 v[0:3], v[176:179], v[208:211], v[0:3]
	v_mfma_f32_16x16x32_bf16 v[28:31], v[172:175], v[188:191], v[28:31]
	v_mfma_f32_16x16x32_bf16 v[24:27], v[180:183], v[188:191], v[24:27]
	v_mfma_f32_16x16x32_bf16 v[20:23], v[172:175], v[196:199], v[20:23]
	v_mfma_f32_16x16x32_bf16 v[16:19], v[180:183], v[196:199], v[16:19]
	v_mfma_f32_16x16x32_bf16 v[12:15], v[172:175], v[204:207], v[12:15]
	v_mfma_f32_16x16x32_bf16 v[8:11], v[180:183], v[204:207], v[8:11]
	v_mfma_f32_16x16x32_bf16 v[4:7], v[172:175], v[212:215], v[4:7]
	v_mfma_f32_16x16x32_bf16 v[0:3], v[180:183], v[212:215], v[0:3]
	s_setprio 0
	s_barrier
	v_add_u32_e32 v130, 0x18000, v157
	ds_read_b128 v[146:149], v130
	ds_read_b128 v[150:153], v130 offset:1024
	ds_read_b128 v[160:163], v130 offset:2048
	ds_read_b128 v[164:167], v130 offset:3072
	v_add_u32_e32 v130, 0x1c000, v157
	ds_read_b128 v[168:171], v130
	ds_read_b128 v[172:175], v130 offset:1024
	ds_read_b128 v[176:179], v130 offset:2048
	ds_read_b128 v[180:183], v130 offset:3072
	ds_read_b128 v[184:187], v158 offset:32768
	ds_read_b128 v[188:191], v158 offset:33792
	ds_read_b128 v[192:195], v158 offset:34816
	ds_read_b128 v[196:199], v158 offset:35840
	ds_read_b128 v[200:203], v158 offset:36864
	ds_read_b128 v[204:207], v158 offset:37888
	ds_read_b128 v[208:211], v158 offset:38912
	ds_read_b128 v[212:215], v158 offset:39936
	s_add_u32 s42, s62, 0x80000
	s_addc_u32 s43, s63, 0
	s_mov_b32 s51, m0
	s_mov_b32 m0, s72
	s_nop 0
	global_load_lds_dwordx4 v129, s[42:43]
	s_mov_b32 m0, s51
	s_nop 0
	s_mov_b32 s51, m0
	s_mov_b32 m0, s73
	s_nop 0
	global_load_lds_dwordx4 v154, s[42:43]
	s_mov_b32 m0, s51
	s_waitcnt vmcnt(8)
	s_waitcnt lgkmcnt(0)
	s_barrier
	s_setprio 1
	v_mfma_f32_16x16x32_bf16 v[124:127], v[146:149], v[184:187], v[124:127]
	v_mfma_f32_16x16x32_bf16 v[120:123], v[160:163], v[184:187], v[120:123]
	v_mfma_f32_16x16x32_bf16 v[116:119], v[146:149], v[192:195], v[116:119]
	v_mfma_f32_16x16x32_bf16 v[112:115], v[160:163], v[192:195], v[112:115]
	v_mfma_f32_16x16x32_bf16 v[108:111], v[146:149], v[200:203], v[108:111]
	v_mfma_f32_16x16x32_bf16 v[104:107], v[160:163], v[200:203], v[104:107]
	v_mfma_f32_16x16x32_bf16 v[100:103], v[146:149], v[208:211], v[100:103]
	v_mfma_f32_16x16x32_bf16 v[96:99], v[160:163], v[208:211], v[96:99]
	v_mfma_f32_16x16x32_bf16 v[124:127], v[150:153], v[188:191], v[124:127]
	v_mfma_f32_16x16x32_bf16 v[120:123], v[164:167], v[188:191], v[120:123]
	v_mfma_f32_16x16x32_bf16 v[116:119], v[150:153], v[196:199], v[116:119]
	v_mfma_f32_16x16x32_bf16 v[112:115], v[164:167], v[196:199], v[112:115]
	v_mfma_f32_16x16x32_bf16 v[108:111], v[150:153], v[204:207], v[108:111]
	v_mfma_f32_16x16x32_bf16 v[104:107], v[164:167], v[204:207], v[104:107]
	v_mfma_f32_16x16x32_bf16 v[100:103], v[150:153], v[212:215], v[100:103]
	v_mfma_f32_16x16x32_bf16 v[96:99], v[164:167], v[212:215], v[96:99]
	v_mfma_f32_16x16x32_bf16 v[92:95], v[168:171], v[184:187], v[92:95]
	v_mfma_f32_16x16x32_bf16 v[88:91], v[176:179], v[184:187], v[88:91]
	v_mfma_f32_16x16x32_bf16 v[84:87], v[168:171], v[192:195], v[84:87]
	v_mfma_f32_16x16x32_bf16 v[80:83], v[176:179], v[192:195], v[80:83]
	v_mfma_f32_16x16x32_bf16 v[76:79], v[168:171], v[200:203], v[76:79]
	v_mfma_f32_16x16x32_bf16 v[72:75], v[176:179], v[200:203], v[72:75]
	v_mfma_f32_16x16x32_bf16 v[68:71], v[168:171], v[208:211], v[68:71]
	v_mfma_f32_16x16x32_bf16 v[64:67], v[176:179], v[208:211], v[64:67]
	v_mfma_f32_16x16x32_bf16 v[92:95], v[172:175], v[188:191], v[92:95]
	v_mfma_f32_16x16x32_bf16 v[88:91], v[180:183], v[188:191], v[88:91]
	v_mfma_f32_16x16x32_bf16 v[84:87], v[172:175], v[196:199], v[84:87]
	v_mfma_f32_16x16x32_bf16 v[80:83], v[180:183], v[196:199], v[80:83]
	v_mfma_f32_16x16x32_bf16 v[76:79], v[172:175], v[204:207], v[76:79]
	v_mfma_f32_16x16x32_bf16 v[72:75], v[180:183], v[204:207], v[72:75]
	v_mfma_f32_16x16x32_bf16 v[68:71], v[172:175], v[212:215], v[68:71]
	v_mfma_f32_16x16x32_bf16 v[64:67], v[180:183], v[212:215], v[64:67]
	s_setprio 0
	s_barrier
; #define PG8_STAGE(bufoff, gbase, voff) do { _Pragma("unroll") for (int _i = 0; _i < 2; ++_i) { unsigned keep_; \
;         asm volatile("s_mov_b32 %0, m0\n\ts_mov_b32 m0, %3\n\ts_nop 0\n\tglobal_load_lds_dwordx4 %1, %2\n\ts_mov_b32 m0, %0" : "=&s"(keep_) : "v"((voff)[_i]), "s"((const char*)(gbase)), "s"(ldsbase + (unsigned)((bufoff) + _i * 8192)) : "memory"); } } while (0)
; #define PG8_WAIT_V(n) asm volatile("s_waitcnt vmcnt(" #n ")" ::: "memory")
; #define PG8_WAIT_L(n) asm volatile("s_waitcnt lgkmcnt(" #n ")" ::: "memory")
; #define PG8_BAR __builtin_amdgcn_s_barrier()
; #define PG8_SCHED __builtin_amdgcn_sched_barrier(0)
; template <class Epi, class Sched, bool ALIGN_EPI, bool FP8 = false>
; DI void gemm_phase(LAS unsigned char* lds, const Gemm g, const Sched& S, const Epi& E) {
;     ...
;             PG8_LDA(At, 1, 1); PG8_STAGE(PG8_SB(1, 0), b3, voffB); PG8_STAGE(PG8_SB(1, 1), b3 + hstepB, voffB); PG8_STAGE(PG8_SA(1, 0), a3, voffA);
;             PG8_WAIT_V(8); PG8_WAIT_L(0); PG8_BAR; PG8_MMA(1, 0, At, B0); PG8_MMA(1, 1, At, B1); PG8_BAR; PG8_SCHED;
;         }
;         if constexpr (ALIGN_EPI) { if (wr == 0) PG8_BAR; }
;         E(acc, cur, wr, wc, fr, fq);
;         if (!has_next) break;
	ds_read_b128 v[184:187], v158 offset:49152
	ds_read_b128 v[188:191], v158 offset:50176
	ds_read_b128 v[192:195], v158 offset:51200
	ds_read_b128 v[196:199], v158 offset:52224
	ds_read_b128 v[200:203], v158 offset:53248
	ds_read_b128 v[204:207], v158 offset:54272
	ds_read_b128 v[208:211], v158 offset:55296
	ds_read_b128 v[212:215], v158 offset:56320
	s_add_u32 s42, s60, 0x80
	s_addc_u32 s43, s61, 0
	s_mov_b32 s51, m0
	s_mov_b32 m0, s83
	s_nop 0
	global_load_lds_dwordx4 v145, s[42:43]
	s_mov_b32 m0, s51
	s_nop 0
	s_mov_b32 s51, m0
	s_mov_b32 m0, s84
	s_nop 0
	global_load_lds_dwordx4 v155, s[42:43]
	s_mov_b32 m0, s51
	s_add_u32 s42, s60, 0x80080
	s_addc_u32 s43, s61, 0
	s_mov_b32 s51, m0
	s_mov_b32 m0, s87
	s_nop 0
	global_load_lds_dwordx4 v145, s[42:43]
	s_mov_b32 m0, s51
	s_nop 0
	s_mov_b32 s51, m0
	s_mov_b32 m0, s88
	s_nop 0
	global_load_lds_dwordx4 v155, s[42:43]
	s_mov_b32 m0, s51
	s_mov_b32 s42, m0
	s_mov_b32 m0, s85
	s_nop 0
	global_load_lds_dwordx4 v129, s[58:59]
	s_mov_b32 m0, s42
	s_nop 0
	s_mov_b32 s42, m0
	s_mov_b32 m0, s86
	s_nop 0
	global_load_lds_dwordx4 v154, s[58:59]
	s_mov_b32 m0, s42
	s_waitcnt vmcnt(8)
	s_waitcnt lgkmcnt(0)
	s_barrier
	s_setprio 1
	v_mfma_f32_16x16x32_bf16 v[60:63], v[146:149], v[184:187], v[60:63]
	v_mfma_f32_16x16x32_bf16 v[56:59], v[160:163], v[184:187], v[56:59]
	v_mfma_f32_16x16x32_bf16 v[52:55], v[146:149], v[192:195], v[52:55]
	v_mfma_f32_16x16x32_bf16 v[48:51], v[160:163], v[192:195], v[48:51]
	v_mfma_f32_16x16x32_bf16 v[44:47], v[146:149], v[200:203], v[44:47]
	v_mfma_f32_16x16x32_bf16 v[40:43], v[160:163], v[200:203], v[40:43]
	v_mfma_f32_16x16x32_bf16 v[36:39], v[146:149], v[208:211], v[36:39]
	v_mfma_f32_16x16x32_bf16 v[32:35], v[160:163], v[208:211], v[32:35]
	v_mfma_f32_16x16x32_bf16 v[60:63], v[150:153], v[188:191], v[60:63]
	v_mfma_f32_16x16x32_bf16 v[56:59], v[164:167], v[188:191], v[56:59]
	v_mfma_f32_16x16x32_bf16 v[52:55], v[150:153], v[196:199], v[52:55]
	v_mfma_f32_16x16x32_bf16 v[48:51], v[164:167], v[196:199], v[48:51]
	v_mfma_f32_16x16x32_bf16 v[44:47], v[150:153], v[204:207], v[44:47]
	v_mfma_f32_16x16x32_bf16 v[40:43], v[164:167], v[204:207], v[40:43]
	v_mfma_f32_16x16x32_bf16 v[36:39], v[150:153], v[212:215], v[36:39]
	v_mfma_f32_16x16x32_bf16 v[32:35], v[164:167], v[212:215], v[32:35]
	v_mfma_f32_16x16x32_bf16 v[28:31], v[168:171], v[184:187], v[28:31]
	v_mfma_f32_16x16x32_bf16 v[24:27], v[176:179], v[184:187], v[24:27]
	v_mfma_f32_16x16x32_bf16 v[20:23], v[168:171], v[192:195], v[20:23]
	v_mfma_f32_16x16x32_bf16 v[16:19], v[176:179], v[192:195], v[16:19]
	v_mfma_f32_16x16x32_bf16 v[12:15], v[168:171], v[200:203], v[12:15]
	v_mfma_f32_16x16x32_bf16 v[8:11], v[176:179], v[200:203], v[8:11]
	v_mfma_f32_16x16x32_bf16 v[4:7], v[168:171], v[208:211], v[4:7]
	v_mfma_f32_16x16x32_bf16 v[0:3], v[176:179], v[208:211], v[0:3]
	v_mfma_f32_16x16x32_bf16 v[28:31], v[172:175], v[188:191], v[28:31]
	v_mfma_f32_16x16x32_bf16 v[24:27], v[180:183], v[188:191], v[24:27]
	v_mfma_f32_16x16x32_bf16 v[20:23], v[172:175], v[196:199], v[20:23]
	v_mfma_f32_16x16x32_bf16 v[16:19], v[180:183], v[196:199], v[16:19]
	v_mfma_f32_16x16x32_bf16 v[12:15], v[172:175], v[204:207], v[12:15]
	v_mfma_f32_16x16x32_bf16 v[8:11], v[180:183], v[204:207], v[8:11]
	v_mfma_f32_16x16x32_bf16 v[4:7], v[172:175], v[212:215], v[4:7]
	v_mfma_f32_16x16x32_bf16 v[0:3], v[180:183], v[212:215], v[0:3]
	s_setprio 0
	s_barrier
	s_add_u32 s56, s56, 0x100
	s_addc_u32 s57, s57, 0
	s_cmp_ge_u32 s53, s81
	s_mov_b32 s51, s53
	s_cbranch_scc0 .LBB0_255
	s_and_b64 vcc, exec, s[26:27]
	s_cbranch_vccnz .LBB0_265
	s_bitcmp0_b32 s77, 1
	s_mov_b64 s[56:57], -1
	v_lshl_add_u32 v142, s14, 8, v156
	s_cbranch_scc0 .LBB0_266

; #define PG8_STAGE(bufoff, gbase, voff) do { _Pragma("unroll") for (int _i = 0; _i < 2; ++_i) { unsigned keep_; \
;         asm volatile("s_mov_b32 %0, m0\n\ts_mov_b32 m0, %3\n\ts_nop 0\n\tglobal_load_lds_dwordx4 %1, %2\n\ts_mov_b32 m0, %0" : "=&s"(keep_) : "v"((voff)[_i]), "s"((const char*)(gbase)), "s"(ldsbase + (unsigned)((bufoff) + _i * 8192)) : "memory"); } } while (0)
; #define PG8_WAIT_V(n) asm volatile("s_waitcnt vmcnt(" #n ")" ::: "memory")
; #define PG8_WAIT_L(n) asm volatile("s_waitcnt lgkmcnt(" #n ")" ::: "memory")
; #define PG8_BAR __builtin_amdgcn_s_barrier()
; #define PG8_SCHED __builtin_amdgcn_sched_barrier(0)
; template <class Epi, class Sched, bool ALIGN_EPI, bool FP8 = false>
; DI void gemm_phase(LAS unsigned char* lds, const Gemm g, const Sched& S, const Epi& E) {
;     ...
;             PG8_LDB(B0, 0, 0); PG8_LDB(B1, 0, 1); PG8_SCHED; PG8_LDA(At, 0, 0); PG8_STAGE(PG8_SA(1, 1), a1 + hstepA, voffA);
;             PG8_WAIT_V(8); PG8_WAIT_L(0); PG8_BAR; PG8_MMA(0, 0, At, B0); PG8_MMA(0, 1, At, B1); PG8_BAR; PG8_SCHED;
;             PG8_LDA(At, 0, 1); PG8_STAGE(PG8_SB(0, 0), b2, voffB); PG8_STAGE(PG8_SB(0, 1), b2 + hstepB, voffB); PG8_STAGE(PG8_SA(0, 0), a2, voffA);
;             PG8_WAIT_V(8); PG8_WAIT_L(0); PG8_BAR; PG8_MMA(1, 0, At, B0); PG8_MMA(1, 1, At, B1); PG8_BAR; PG8_SCHED;
.LBB0_298:
	ds_read_b128 v[104:107], v151
	s_waitcnt vmcnt(8)
	ds_read_b128 v[108:111], v151 offset:16
	ds_read_b128 v[112:115], v151 offset:2048
	ds_read_b128 v[116:119], v151 offset:2064
	ds_read_b128 v[160:163], v151 offset:16384
	ds_read_b128 v[164:167], v151 offset:16400
	ds_read_b128 v[168:171], v151 offset:18432
	ds_read_b128 v[172:175], v151 offset:18448
	s_add_u32 s52, s50, 0x100
	s_addc_u32 s53, s51, 0
	s_cmp_eq_u32 s91, 12
	s_cselect_b32 s58, s87, s52
	s_cselect_b32 s59, s43, s53
	s_cselect_b32 s56, s88, s89
	s_cselect_b32 s57, s41, s90
	s_add_u32 s54, s58, 0x80
	s_addc_u32 s55, s59, 0
	ds_read_b128 v[176:179], v150
	ds_read_b128 v[180:183], v150 offset:16
	ds_read_b128 v[184:187], v150 offset:2048
	ds_read_b128 v[188:191], v150 offset:2064
	ds_read_b128 v[192:195], v150 offset:4096
	ds_read_b128 v[196:199], v150 offset:4112
	ds_read_b128 v[200:203], v150 offset:6144
	ds_read_b128 v[204:207], v150 offset:6160
	s_add_u32 s50, s50, 0x40080
	s_addc_u32 s51, s51, 0
	s_mov_b32 s92, m0
	s_mov_b32 m0, s75
	s_nop 0
	global_load_lds_dwordx4 v152, s[50:51]
	s_mov_b32 m0, s92
	s_nop 0
	s_mov_b32 s92, m0
	s_mov_b32 m0, s77
	s_nop 0
	global_load_lds_dwordx4 v154, s[50:51]
	s_mov_b32 m0, s92
	s_waitcnt vmcnt(8)
	s_waitcnt lgkmcnt(0)
	s_barrier
	s_setprio 1
	v_mfma_scale_f32_16x16x128_f8f6f4 v[140:143], v[104:111], v[176:183], v[140:143], v158, v158 op_sel_hi:[0,0,0]
	v_mfma_scale_f32_16x16x128_f8f6f4 v[136:139], v[112:119], v[176:183], v[136:139], v158, v158 op_sel_hi:[0,0,0]
	v_mfma_scale_f32_16x16x128_f8f6f4 v[124:127], v[104:111], v[184:191], v[124:127], v158, v158 op_sel_hi:[0,0,0]
	v_mfma_scale_f32_16x16x128_f8f6f4 v[120:123], v[112:119], v[184:191], v[120:123], v158, v158 op_sel_hi:[0,0,0]
	v_mfma_scale_f32_16x16x128_f8f6f4 v[208:211], v[104:111], v[192:199], v[92:95], v158, v158 op_sel_hi:[0,0,0]
	v_mfma_scale_f32_16x16x128_f8f6f4 v[212:215], v[112:119], v[192:199], v[88:91], v158, v158 op_sel_hi:[0,0,0]
	v_mfma_scale_f32_16x16x128_f8f6f4 v[216:219], v[104:111], v[200:207], v[76:79], v158, v158 op_sel_hi:[0,0,0]
	v_mfma_scale_f32_16x16x128_f8f6f4 v[220:223], v[112:119], v[200:207], v[72:75], v158, v158 op_sel_hi:[0,0,0]
	v_mfma_scale_f32_16x16x128_f8f6f4 v[132:135], v[160:167], v[176:183], v[132:135], v158, v158 op_sel_hi:[0,0,0]
	v_mfma_scale_f32_16x16x128_f8f6f4 v[128:131], v[168:175], v[176:183], v[128:131], v158, v158 op_sel_hi:[0,0,0]
	v_mfma_scale_f32_16x16x128_f8f6f4 v[100:103], v[160:167], v[184:191], v[100:103], v158, v158 op_sel_hi:[0,0,0]
	v_mfma_scale_f32_16x16x128_f8f6f4 v[96:99], v[168:175], v[184:191], v[96:99], v158, v158 op_sel_hi:[0,0,0]
	v_mfma_scale_f32_16x16x128_f8f6f4 v[176:179], v[160:167], v[192:199], v[84:87], v158, v158 op_sel_hi:[0,0,0]
	v_mfma_scale_f32_16x16x128_f8f6f4 v[180:183], v[168:175], v[192:199], v[80:83], v158, v158 op_sel_hi:[0,0,0]
	v_mfma_scale_f32_16x16x128_f8f6f4 v[184:187], v[160:167], v[200:207], v[68:71], v158, v158 op_sel_hi:[0,0,0]
	v_mfma_scale_f32_16x16x128_f8f6f4 v[188:191], v[168:175], v[200:207], v[64:67], v158, v158 op_sel_hi:[0,0,0]
	s_setprio 0
	s_barrier
	s_nop 4
	ds_read_b128 v[64:67], v150 offset:16384
	ds_read_b128 v[68:71], v150 offset:16400
	ds_read_b128 v[72:75], v150 offset:18432
	ds_read_b128 v[76:79], v150 offset:18448
	ds_read_b128 v[80:83], v150 offset:20480
	ds_read_b128 v[84:87], v150 offset:20496
	ds_read_b128 v[88:91], v150 offset:22528
	ds_read_b128 v[92:95], v150 offset:22544
	s_mov_b32 s50, m0
	s_mov_b32 m0, s49
	s_nop 0
	global_load_lds_dwordx4 v153, s[56:57]
	s_mov_b32 m0, s50
	s_nop 0
	s_mov_b32 s50, m0
	s_mov_b32 m0, s63
	s_nop 0
	global_load_lds_dwordx4 v155, s[56:57]
	s_mov_b32 m0, s50
	s_add_u32 s50, s56, 0x40000
	s_addc_u32 s51, s57, 0
	s_mov_b32 s92, m0
	s_mov_b32 m0, s64
	s_nop 0
	global_load_lds_dwordx4 v153, s[50:51]
	s_mov_b32 m0, s92
	s_nop 0
	s_mov_b32 s92, m0
	s_mov_b32 m0, s65
	s_nop 0
	global_load_lds_dwordx4 v155, s[50:51]
	s_mov_b32 m0, s92
	s_mov_b32 s50, m0
	s_mov_b32 m0, s62
	s_nop 0
	global_load_lds_dwordx4 v152, s[58:59]
	s_mov_b32 m0, s50
	s_nop 0
	s_mov_b32 s50, m0
	s_mov_b32 m0, s66
	s_nop 0
	global_load_lds_dwordx4 v154, s[58:59]
	s_mov_b32 m0, s50
	s_waitcnt vmcnt(8)
	s_waitcnt lgkmcnt(0)
	s_barrier
	s_setprio 1
	v_mfma_scale_f32_16x16x128_f8f6f4 v[60:63], v[104:111], v[64:71], v[60:63], v158, v158 op_sel_hi:[0,0,0]
	v_mfma_scale_f32_16x16x128_f8f6f4 v[56:59], v[112:119], v[64:71], v[56:59], v158, v158 op_sel_hi:[0,0,0]
	v_mfma_scale_f32_16x16x128_f8f6f4 v[192:195], v[104:111], v[72:79], v[44:47], v158, v158 op_sel_hi:[0,0,0]
	v_mfma_scale_f32_16x16x128_f8f6f4 v[196:199], v[112:119], v[72:79], v[40:43], v158, v158 op_sel_hi:[0,0,0]
	v_mfma_scale_f32_16x16x128_f8f6f4 v[200:203], v[104:111], v[80:87], v[28:31], v158, v158 op_sel_hi:[0,0,0]
	v_mfma_scale_f32_16x16x128_f8f6f4 v[204:207], v[112:119], v[80:87], v[24:27], v158, v158 op_sel_hi:[0,0,0]
	v_mfma_scale_f32_16x16x128_f8f6f4 v[224:227], v[104:111], v[88:95], v[12:15], v158, v158 op_sel_hi:[0,0,0]
	v_mfma_scale_f32_16x16x128_f8f6f4 v[228:231], v[112:119], v[88:95], v[8:11], v158, v158 op_sel_hi:[0,0,0]
	v_mfma_scale_f32_16x16x128_f8f6f4 v[52:55], v[160:167], v[64:71], v[52:55], v158, v158 op_sel_hi:[0,0,0]
	v_mfma_scale_f32_16x16x128_f8f6f4 v[48:51], v[168:175], v[64:71], v[48:51], v158, v158 op_sel_hi:[0,0,0]
	v_mfma_scale_f32_16x16x128_f8f6f4 v[232:235], v[160:167], v[72:79], v[36:39], v158, v158 op_sel_hi:[0,0,0]
	v_mfma_scale_f32_16x16x128_f8f6f4 v[236:239], v[168:175], v[72:79], v[32:35], v158, v158 op_sel_hi:[0,0,0]
	v_mfma_scale_f32_16x16x128_f8f6f4 v[240:243], v[160:167], v[80:87], v[20:23], v158, v158 op_sel_hi:[0,0,0]
	v_mfma_scale_f32_16x16x128_f8f6f4 v[244:247], v[168:175], v[80:87], v[16:19], v158, v158 op_sel_hi:[0,0,0]
	v_mfma_scale_f32_16x16x128_f8f6f4 v[248:251], v[160:167], v[88:95], v[4:7], v158, v158 op_sel_hi:[0,0,0]
	v_mfma_scale_f32_16x16x128_f8f6f4 v[144:147], v[168:175], v[88:95], v[0:3], v158, v158 op_sel_hi:[0,0,0]
	s_setprio 0
	s_barrier
; #define PG8_STAGE(bufoff, gbase, voff) do { _Pragma("unroll") for (int _i = 0; _i < 2; ++_i) { unsigned keep_; \
;         asm volatile("s_mov_b32 %0, m0\n\ts_mov_b32 m0, %3\n\ts_nop 0\n\tglobal_load_lds_dwordx4 %1, %2\n\ts_mov_b32 m0, %0" : "=&s"(keep_) : "v"((voff)[_i]), "s"((const char*)(gbase)), "s"(ldsbase + (unsigned)((bufoff) + _i * 8192)) : "memory"); } } while (0)
; #define PG8_WAIT_V(n) asm volatile("s_waitcnt vmcnt(" #n ")" ::: "memory")
; #define PG8_WAIT_L(n) asm volatile("s_waitcnt lgkmcnt(" #n ")" ::: "memory")
; #define PG8_BAR __builtin_amdgcn_s_barrier()
; #define PG8_SCHED __builtin_amdgcn_sched_barrier(0)
; template <class Epi, class Sched, bool ALIGN_EPI, bool FP8 = false>
; DI void gemm_phase(LAS unsigned char* lds, const Gemm g, const Sched& S, const Epi& E) {
;     ...
;             PG8_LDB(B0, 1, 0); PG8_LDB(B1, 1, 1); PG8_SCHED; PG8_LDA(At, 1, 0); PG8_STAGE(PG8_SA(0, 1), a2 + hstepA, voffA);
;             PG8_WAIT_V(8); PG8_WAIT_L(0); PG8_BAR; PG8_MMA(0, 0, At, B0); PG8_MMA(0, 1, At, B1); PG8_BAR; PG8_SCHED;
;             PG8_LDA(At, 1, 1); PG8_STAGE(PG8_SB(1, 0), b3, voffB); PG8_STAGE(PG8_SB(1, 1), b3 + hstepB, voffB); PG8_STAGE(PG8_SA(1, 0), a3, voffA);
;             PG8_WAIT_V(8); PG8_WAIT_L(0); PG8_BAR; PG8_MMA(1, 0, At, B0); PG8_MMA(1, 1, At, B1); PG8_BAR; PG8_SCHED;
;         }
;         if constexpr (ALIGN_EPI) { if (wr == 0) PG8_BAR; }
;         E(acc, cur, wr, wc, fr, fq);
;         if (!has_next) break;
	s_nop 4
	ds_read_b128 v[0:3], v151 offset:32768
	ds_read_b128 v[4:7], v151 offset:32784
	ds_read_b128 v[16:19], v151 offset:34816
	ds_read_b128 v[20:23], v151 offset:34832
	ds_read_b128 v[104:107], v151 offset:49152
	ds_read_b128 v[108:111], v151 offset:49168
	ds_read_b128 v[112:115], v151 offset:51200
	ds_read_b128 v[116:119], v151 offset:51216
	ds_read_b128 v[8:11], v150 offset:32768
	ds_read_b128 v[12:15], v150 offset:32784
	ds_read_b128 v[24:27], v150 offset:34816
	ds_read_b128 v[28:31], v150 offset:34832
	ds_read_b128 v[32:35], v150 offset:36864
	ds_read_b128 v[36:39], v150 offset:36880
	ds_read_b128 v[40:43], v150 offset:38912
	ds_read_b128 v[44:47], v150 offset:38928
	s_add_u32 s50, s58, 0x40000
	s_addc_u32 s51, s59, 0
	s_mov_b32 s58, m0
	s_mov_b32 m0, s67
	s_nop 0
	global_load_lds_dwordx4 v152, s[50:51]
	s_mov_b32 m0, s58
	s_nop 0
	s_mov_b32 s58, m0
	s_mov_b32 m0, s68
	s_nop 0
	global_load_lds_dwordx4 v154, s[50:51]
	s_mov_b32 m0, s58
	s_waitcnt vmcnt(8)
	s_waitcnt lgkmcnt(0)
	s_barrier
	s_setprio 1
	v_mfma_scale_f32_16x16x128_f8f6f4 v[140:143], v[0:7], v[8:15], v[140:143], v158, v158 op_sel_hi:[0,0,0]
	v_mfma_scale_f32_16x16x128_f8f6f4 v[136:139], v[16:23], v[8:15], v[136:139], v158, v158 op_sel_hi:[0,0,0]
	v_mfma_scale_f32_16x16x128_f8f6f4 v[124:127], v[0:7], v[24:31], v[124:127], v158, v158 op_sel_hi:[0,0,0]
	v_mfma_scale_f32_16x16x128_f8f6f4 v[120:123], v[16:23], v[24:31], v[120:123], v158, v158 op_sel_hi:[0,0,0]
	v_mfma_scale_f32_16x16x128_f8f6f4 v[92:95], v[0:7], v[32:39], v[208:211], v158, v158 op_sel_hi:[0,0,0]
	v_mfma_scale_f32_16x16x128_f8f6f4 v[88:91], v[16:23], v[32:39], v[212:215], v158, v158 op_sel_hi:[0,0,0]
	v_mfma_scale_f32_16x16x128_f8f6f4 v[76:79], v[0:7], v[40:47], v[216:219], v158, v158 op_sel_hi:[0,0,0]
	v_mfma_scale_f32_16x16x128_f8f6f4 v[72:75], v[16:23], v[40:47], v[220:223], v158, v158 op_sel_hi:[0,0,0]
	v_mfma_scale_f32_16x16x128_f8f6f4 v[132:135], v[104:111], v[8:15], v[132:135], v158, v158 op_sel_hi:[0,0,0]
	v_mfma_scale_f32_16x16x128_f8f6f4 v[128:131], v[112:119], v[8:15], v[128:131], v158, v158 op_sel_hi:[0,0,0]
	v_mfma_scale_f32_16x16x128_f8f6f4 v[100:103], v[104:111], v[24:31], v[100:103], v158, v158 op_sel_hi:[0,0,0]
	v_mfma_scale_f32_16x16x128_f8f6f4 v[96:99], v[112:119], v[24:31], v[96:99], v158, v158 op_sel_hi:[0,0,0]
	v_mfma_scale_f32_16x16x128_f8f6f4 v[84:87], v[104:111], v[32:39], v[176:179], v158, v158 op_sel_hi:[0,0,0]
	v_mfma_scale_f32_16x16x128_f8f6f4 v[80:83], v[112:119], v[32:39], v[180:183], v158, v158 op_sel_hi:[0,0,0]
	v_mfma_scale_f32_16x16x128_f8f6f4 v[68:71], v[104:111], v[40:47], v[184:187], v158, v158 op_sel_hi:[0,0,0]
	v_mfma_scale_f32_16x16x128_f8f6f4 v[64:67], v[112:119], v[40:47], v[188:191], v158, v158 op_sel_hi:[0,0,0]
	s_setprio 0
	s_barrier
	ds_read_b128 v[32:35], v150 offset:49152
	ds_read_b128 v[36:39], v150 offset:49168
	ds_read_b128 v[160:163], v150 offset:51200
	ds_read_b128 v[164:167], v150 offset:51216
	ds_read_b128 v[168:171], v150 offset:53248
	ds_read_b128 v[172:175], v150 offset:53264
	ds_read_b128 v[176:179], v150 offset:55296
	ds_read_b128 v[180:183], v150 offset:55312
	s_add_u32 s50, s56, 0x80
	s_addc_u32 s51, s57, 0
	s_mov_b32 s58, m0
	s_mov_b32 m0, s69
	s_nop 0
	global_load_lds_dwordx4 v153, s[50:51]
	s_mov_b32 m0, s58
	s_nop 0
	s_mov_b32 s58, m0
	s_mov_b32 m0, s70
	s_nop 0
	global_load_lds_dwordx4 v155, s[50:51]
	s_mov_b32 m0, s58
	s_add_u32 s50, s56, 0x40080
	s_addc_u32 s51, s57, 0
	s_mov_b32 s56, m0
	s_mov_b32 m0, s73
	s_nop 0
	global_load_lds_dwordx4 v153, s[50:51]
	s_mov_b32 m0, s56
	s_nop 0
	s_mov_b32 s56, m0
	s_mov_b32 m0, s74
	s_nop 0
	global_load_lds_dwordx4 v155, s[50:51]
	s_mov_b32 m0, s56
	s_mov_b32 s50, m0
	s_mov_b32 m0, s71
	s_nop 0
	global_load_lds_dwordx4 v152, s[54:55]
	s_mov_b32 m0, s50
	s_nop 0
	s_mov_b32 s50, m0
	s_mov_b32 m0, s72
	s_nop 0
	global_load_lds_dwordx4 v154, s[54:55]
	s_mov_b32 m0, s50
	s_waitcnt vmcnt(8)
	s_waitcnt lgkmcnt(0)
	s_barrier
	s_setprio 1
	v_mfma_scale_f32_16x16x128_f8f6f4 v[60:63], v[0:7], v[32:39], v[60:63], v158, v158 op_sel_hi:[0,0,0]
	v_mfma_scale_f32_16x16x128_f8f6f4 v[56:59], v[16:23], v[32:39], v[56:59], v158, v158 op_sel_hi:[0,0,0]
	v_mfma_scale_f32_16x16x128_f8f6f4 v[44:47], v[0:7], v[160:167], v[192:195], v158, v158 op_sel_hi:[0,0,0]
	v_mfma_scale_f32_16x16x128_f8f6f4 v[40:43], v[16:23], v[160:167], v[196:199], v158, v158 op_sel_hi:[0,0,0]
	v_mfma_scale_f32_16x16x128_f8f6f4 v[28:31], v[0:7], v[168:175], v[200:203], v158, v158 op_sel_hi:[0,0,0]
	v_mfma_scale_f32_16x16x128_f8f6f4 v[24:27], v[16:23], v[168:175], v[204:207], v158, v158 op_sel_hi:[0,0,0]
	v_mfma_scale_f32_16x16x128_f8f6f4 v[12:15], v[0:7], v[176:183], v[224:227], v158, v158 op_sel_hi:[0,0,0]
	v_mfma_scale_f32_16x16x128_f8f6f4 v[8:11], v[16:23], v[176:183], v[228:231], v158, v158 op_sel_hi:[0,0,0]
	v_mfma_scale_f32_16x16x128_f8f6f4 v[52:55], v[104:111], v[32:39], v[52:55], v158, v158 op_sel_hi:[0,0,0]
	v_mfma_scale_f32_16x16x128_f8f6f4 v[48:51], v[112:119], v[32:39], v[48:51], v158, v158 op_sel_hi:[0,0,0]
	v_mfma_scale_f32_16x16x128_f8f6f4 v[36:39], v[104:111], v[160:167], v[232:235], v158, v158 op_sel_hi:[0,0,0]
	v_mfma_scale_f32_16x16x128_f8f6f4 v[32:35], v[112:119], v[160:167], v[236:239], v158, v158 op_sel_hi:[0,0,0]
	v_mfma_scale_f32_16x16x128_f8f6f4 v[20:23], v[104:111], v[168:175], v[240:243], v158, v158 op_sel_hi:[0,0,0]
	v_mfma_scale_f32_16x16x128_f8f6f4 v[16:19], v[112:119], v[168:175], v[244:247], v158, v158 op_sel_hi:[0,0,0]
	v_mfma_scale_f32_16x16x128_f8f6f4 v[4:7], v[104:111], v[176:183], v[248:251], v158, v158 op_sel_hi:[0,0,0]
	v_mfma_scale_f32_16x16x128_f8f6f4 v[0:3], v[112:119], v[176:183], v[144:147], v158, v158 op_sel_hi:[0,0,0]
	s_setprio 0
	s_barrier
	s_add_i32 s91, s91, 2
	s_add_u32 s89, s89, 0x100
	s_addc_u32 s90, s90, 0
	s_cmp_gt_u32 s91, 13
	s_mov_b64 s[50:51], s[52:53]
	s_cbranch_scc0 .LBB0_298
	s_and_b64 vcc, exec, s[16:17]
	s_cbranch_vccz .LBB0_301
	s_barrier

; #define PG8_STAGE(bufoff, gbase, voff) do { _Pragma("unroll") for (int _i = 0; _i < 2; ++_i) { unsigned keep_; \
;         asm volatile("s_mov_b32 %0, m0\n\ts_mov_b32 m0, %3\n\ts_nop 0\n\tglobal_load_lds_dwordx4 %1, %2\n\ts_mov_b32 m0, %0" : "=&s"(keep_) : "v"((voff)[_i]), "s"((const char*)(gbase)), "s"(ldsbase + (unsigned)((bufoff) + _i * 8192)) : "memory"); } } while (0)
; #define PG8_WAIT_V(n) asm volatile("s_waitcnt vmcnt(" #n ")" ::: "memory")
; #define PG8_WAIT_L(n) asm volatile("s_waitcnt lgkmcnt(" #n ")" ::: "memory")
; #define PG8_BAR __builtin_amdgcn_s_barrier()
; #define PG8_SCHED __builtin_amdgcn_sched_barrier(0)
; template <class Epi, class Sched, bool ALIGN_EPI, bool FP8 = false>
; DI void gemm_phase(LAS unsigned char* lds, const Gemm g, const Sched& S, const Epi& E) {
;     ...
;             PG8_LDB(B0, 0, 0); PG8_LDB(B1, 0, 1); PG8_SCHED; PG8_LDA(At, 0, 0); PG8_STAGE(PG8_SA(1, 1), a1 + hstepA, voffA);
;             PG8_WAIT_V(8); PG8_WAIT_L(0); PG8_BAR; PG8_MMA(0, 0, At, B0); PG8_MMA(0, 1, At, B1); PG8_BAR; PG8_SCHED;
;             PG8_LDA(At, 0, 1); PG8_STAGE(PG8_SB(0, 0), b2, voffB); PG8_STAGE(PG8_SB(0, 1), b2 + hstepB, voffB); PG8_STAGE(PG8_SA(0, 0), a2, voffA);
;             PG8_WAIT_V(8); PG8_WAIT_L(0); PG8_BAR; PG8_MMA(1, 0, At, B0); PG8_MMA(1, 1, At, B1); PG8_BAR; PG8_SCHED;
.LBB0_489:
	v_add_u32_e32 v1, 0x10000, v160
	ds_read_b128 v[132:135], v1
	ds_read_b128 v[136:139], v1 offset:1024
	ds_read_b128 v[140:143], v1 offset:2048
	ds_read_b128 v[162:165], v1 offset:3072
	v_add_u32_e32 v1, 0x14000, v160
	ds_read_b128 v[166:169], v1
	ds_read_b128 v[170:173], v1 offset:1024
	ds_read_b128 v[174:177], v1 offset:2048
	ds_read_b128 v[178:181], v1 offset:3072
	s_add_u32 s28, s26, 0x100
	s_addc_u32 s29, s27, 0
	s_cmp_eq_u32 s69, 28
	s_cselect_b32 s44, s65, s28
	s_cselect_b32 s45, s21, s29
	s_cselect_b32 s42, s66, s67
	s_cselect_b32 s43, s19, s68
	s_add_u32 s40, s44, 0x80
	s_addc_u32 s41, s45, 0
	ds_read_b128 v[182:185], v161
	ds_read_b128 v[186:189], v161 offset:1024
	ds_read_b128 v[190:193], v161 offset:2048
	ds_read_b128 v[194:197], v161 offset:3072
	ds_read_b128 v[198:201], v161 offset:4096
	ds_read_b128 v[202:205], v161 offset:5120
	ds_read_b128 v[206:209], v161 offset:6144
	ds_read_b128 v[210:213], v161 offset:7168
	s_add_u32 s26, s26, 0x80080
	s_addc_u32 s27, s27, 0
	s_mov_b32 s70, m0
	s_mov_b32 m0, s61
	s_nop 0
	global_load_lds_dwordx4 v154, s[26:27]
	s_mov_b32 m0, s70
	s_nop 0
	s_mov_b32 s70, m0
	s_mov_b32 m0, s62
	s_nop 0
	global_load_lds_dwordx4 v156, s[26:27]
	s_mov_b32 m0, s70
	s_waitcnt vmcnt(8)
	s_waitcnt lgkmcnt(0)
	s_barrier
	s_setprio 1
	v_mfma_f32_16x16x32_bf16 v[128:131], v[132:135], v[182:185], v[128:131]
	v_mfma_f32_16x16x32_bf16 v[124:127], v[140:143], v[182:185], v[124:127]
	v_mfma_f32_16x16x32_bf16 v[112:115], v[132:135], v[190:193], v[112:115]
	v_mfma_f32_16x16x32_bf16 v[108:111], v[140:143], v[190:193], v[108:111]
	v_mfma_f32_16x16x32_bf16 v[96:99], v[132:135], v[198:201], v[96:99]
	v_mfma_f32_16x16x32_bf16 v[92:95], v[140:143], v[198:201], v[92:95]
	v_mfma_f32_16x16x32_bf16 v[80:83], v[132:135], v[206:209], v[80:83]
	v_mfma_f32_16x16x32_bf16 v[76:79], v[140:143], v[206:209], v[76:79]
	v_mfma_f32_16x16x32_bf16 v[128:131], v[136:139], v[186:189], v[128:131]
	v_mfma_f32_16x16x32_bf16 v[124:127], v[162:165], v[186:189], v[124:127]
	v_mfma_f32_16x16x32_bf16 v[112:115], v[136:139], v[194:197], v[112:115]
	v_mfma_f32_16x16x32_bf16 v[108:111], v[162:165], v[194:197], v[108:111]
	v_mfma_f32_16x16x32_bf16 v[96:99], v[136:139], v[202:205], v[96:99]
	v_mfma_f32_16x16x32_bf16 v[92:95], v[162:165], v[202:205], v[92:95]
	v_mfma_f32_16x16x32_bf16 v[80:83], v[136:139], v[210:213], v[80:83]
	v_mfma_f32_16x16x32_bf16 v[76:79], v[162:165], v[210:213], v[76:79]
	v_mfma_f32_16x16x32_bf16 v[120:123], v[166:169], v[182:185], v[120:123]
	v_mfma_f32_16x16x32_bf16 v[116:119], v[174:177], v[182:185], v[116:119]
	v_mfma_f32_16x16x32_bf16 v[104:107], v[166:169], v[190:193], v[104:107]
	v_mfma_f32_16x16x32_bf16 v[100:103], v[174:177], v[190:193], v[100:103]
	v_mfma_f32_16x16x32_bf16 v[88:91], v[166:169], v[198:201], v[88:91]
	v_mfma_f32_16x16x32_bf16 v[84:87], v[174:177], v[198:201], v[84:87]
	v_mfma_f32_16x16x32_bf16 v[72:75], v[166:169], v[206:209], v[72:75]
	v_mfma_f32_16x16x32_bf16 v[68:71], v[174:177], v[206:209], v[68:71]
	v_mfma_f32_16x16x32_bf16 v[120:123], v[170:173], v[186:189], v[120:123]
	v_mfma_f32_16x16x32_bf16 v[116:119], v[178:181], v[186:189], v[116:119]
	v_mfma_f32_16x16x32_bf16 v[104:107], v[170:173], v[194:197], v[104:107]
	v_mfma_f32_16x16x32_bf16 v[100:103], v[178:181], v[194:197], v[100:103]
	v_mfma_f32_16x16x32_bf16 v[88:91], v[170:173], v[202:205], v[88:91]
	v_mfma_f32_16x16x32_bf16 v[84:87], v[178:181], v[202:205], v[84:87]
	v_mfma_f32_16x16x32_bf16 v[72:75], v[170:173], v[210:213], v[72:75]
	v_mfma_f32_16x16x32_bf16 v[68:71], v[178:181], v[210:213], v[68:71]
	s_setprio 0
	s_barrier
	ds_read_b128 v[182:185], v161 offset:16384
	ds_read_b128 v[186:189], v161 offset:17408
	ds_read_b128 v[190:193], v161 offset:18432
	ds_read_b128 v[194:197], v161 offset:19456
	ds_read_b128 v[198:201], v161 offset:20480
	ds_read_b128 v[202:205], v161 offset:21504
	ds_read_b128 v[206:209], v161 offset:22528
	ds_read_b128 v[210:213], v161 offset:23552
	s_mov_b32 s26, m0
	s_mov_b32 m0, s48
	s_nop 0
	global_load_lds_dwordx4 v155, s[42:43]
	s_mov_b32 m0, s26
	s_nop 0
	s_mov_b32 s26, m0
	s_mov_b32 m0, s49
	s_nop 0
	global_load_lds_dwordx4 v157, s[42:43]
	s_mov_b32 m0, s26
	s_add_u32 s26, s42, 0x80000
	s_addc_u32 s27, s43, 0
	s_mov_b32 s70, m0
	s_mov_b32 m0, s50
	s_nop 0
	global_load_lds_dwordx4 v155, s[26:27]
	s_mov_b32 m0, s70
	s_nop 0
	s_mov_b32 s70, m0
	s_mov_b32 m0, s51
	s_nop 0
	global_load_lds_dwordx4 v157, s[26:27]
	s_mov_b32 m0, s70
	s_mov_b32 s26, m0
	s_mov_b32 m0, s47
	s_nop 0
	global_load_lds_dwordx4 v154, s[44:45]
	s_mov_b32 m0, s26
	s_nop 0
	s_mov_b32 s26, m0
	s_mov_b32 m0, s52
	s_nop 0
	global_load_lds_dwordx4 v156, s[44:45]
	s_mov_b32 m0, s26
	s_waitcnt vmcnt(8)
	s_waitcnt lgkmcnt(0)
	s_barrier
; #define PG8_STAGE(bufoff, gbase, voff) do { _Pragma("unroll") for (int _i = 0; _i < 2; ++_i) { unsigned keep_; \
;         asm volatile("s_mov_b32 %0, m0\n\ts_mov_b32 m0, %3\n\ts_nop 0\n\tglobal_load_lds_dwordx4 %1, %2\n\ts_mov_b32 m0, %0" : "=&s"(keep_) : "v"((voff)[_i]), "s"((const char*)(gbase)), "s"(ldsbase + (unsigned)((bufoff) + _i * 8192)) : "memory"); } } while (0)
; #define PG8_WAIT_V(n) asm volatile("s_waitcnt vmcnt(" #n ")" ::: "memory")
; #define PG8_WAIT_L(n) asm volatile("s_waitcnt lgkmcnt(" #n ")" ::: "memory")
; #define PG8_BAR __builtin_amdgcn_s_barrier()
; #define PG8_SCHED __builtin_amdgcn_sched_barrier(0)
; template <class Epi, class Sched, bool ALIGN_EPI, bool FP8 = false>
; DI void gemm_phase(LAS unsigned char* lds, const Gemm g, const Sched& S, const Epi& E) {
;     ...
;             PG8_WAIT_V(8); PG8_WAIT_L(0); PG8_BAR; PG8_MMA(1, 0, At, B0); PG8_MMA(1, 1, At, B1); PG8_BAR; PG8_SCHED;
;             PG8_LDB(B0, 1, 0); PG8_LDB(B1, 1, 1); PG8_SCHED; PG8_LDA(At, 1, 0); PG8_STAGE(PG8_SA(0, 1), a2 + hstepA, voffA);
;             PG8_WAIT_V(8); PG8_WAIT_L(0); PG8_BAR; PG8_MMA(0, 0, At, B0); PG8_MMA(0, 1, At, B1); PG8_BAR; PG8_SCHED;
	s_setprio 1
	v_mfma_f32_16x16x32_bf16 v[64:67], v[132:135], v[182:185], v[64:67]
	v_mfma_f32_16x16x32_bf16 v[60:63], v[140:143], v[182:185], v[60:63]
	v_mfma_f32_16x16x32_bf16 v[48:51], v[132:135], v[190:193], v[48:51]
	v_mfma_f32_16x16x32_bf16 v[44:47], v[140:143], v[190:193], v[44:47]
	v_mfma_f32_16x16x32_bf16 v[32:35], v[132:135], v[198:201], v[32:35]
	v_mfma_f32_16x16x32_bf16 v[28:31], v[140:143], v[198:201], v[28:31]
	v_mfma_f32_16x16x32_bf16 v[16:19], v[132:135], v[206:209], v[16:19]
	v_mfma_f32_16x16x32_bf16 v[12:15], v[140:143], v[206:209], v[12:15]
	v_mfma_f32_16x16x32_bf16 v[64:67], v[136:139], v[186:189], v[64:67]
	v_mfma_f32_16x16x32_bf16 v[60:63], v[162:165], v[186:189], v[60:63]
	v_mfma_f32_16x16x32_bf16 v[48:51], v[136:139], v[194:197], v[48:51]
	v_mfma_f32_16x16x32_bf16 v[44:47], v[162:165], v[194:197], v[44:47]
	v_mfma_f32_16x16x32_bf16 v[32:35], v[136:139], v[202:205], v[32:35]
	v_mfma_f32_16x16x32_bf16 v[28:31], v[162:165], v[202:205], v[28:31]
	v_mfma_f32_16x16x32_bf16 v[16:19], v[136:139], v[210:213], v[16:19]
	v_mfma_f32_16x16x32_bf16 v[12:15], v[162:165], v[210:213], v[12:15]
	v_mfma_f32_16x16x32_bf16 v[56:59], v[166:169], v[182:185], v[56:59]
	v_mfma_f32_16x16x32_bf16 v[52:55], v[174:177], v[182:185], v[52:55]
	v_mfma_f32_16x16x32_bf16 v[40:43], v[166:169], v[190:193], v[40:43]
	v_mfma_f32_16x16x32_bf16 v[36:39], v[174:177], v[190:193], v[36:39]
	v_mfma_f32_16x16x32_bf16 v[24:27], v[166:169], v[198:201], v[24:27]
	v_mfma_f32_16x16x32_bf16 v[20:23], v[174:177], v[198:201], v[20:23]
	v_mfma_f32_16x16x32_bf16 v[8:11], v[166:169], v[206:209], v[8:11]
	v_mfma_f32_16x16x32_bf16 v[2:5], v[174:177], v[206:209], v[4:7]
	v_mfma_f32_16x16x32_bf16 v[56:59], v[170:173], v[186:189], v[56:59]
	v_mfma_f32_16x16x32_bf16 v[52:55], v[178:181], v[186:189], v[52:55]
	v_mfma_f32_16x16x32_bf16 v[40:43], v[170:173], v[194:197], v[40:43]
	v_mfma_f32_16x16x32_bf16 v[36:39], v[178:181], v[194:197], v[36:39]
	v_mfma_f32_16x16x32_bf16 v[24:27], v[170:173], v[202:205], v[24:27]
	v_mfma_f32_16x16x32_bf16 v[20:23], v[178:181], v[202:205], v[20:23]
	v_mfma_f32_16x16x32_bf16 v[8:11], v[170:173], v[210:213], v[8:11]
	v_mfma_f32_16x16x32_bf16 v[2:5], v[178:181], v[210:213], v[2:5]
	s_setprio 0
	s_barrier
	v_add_u32_e32 v1, 0x18000, v160
	ds_read_b128 v[132:135], v1
	ds_read_b128 v[136:139], v1 offset:1024
	ds_read_b128 v[140:143], v1 offset:2048
	ds_read_b128 v[162:165], v1 offset:3072
	v_add_u32_e32 v1, 0x1c000, v160
	ds_read_b128 v[166:169], v1
	ds_read_b128 v[170:173], v1 offset:1024
	ds_read_b128 v[174:177], v1 offset:2048
	ds_read_b128 v[178:181], v1 offset:3072
	ds_read_b128 v[182:185], v161 offset:32768
	ds_read_b128 v[186:189], v161 offset:33792
	ds_read_b128 v[190:193], v161 offset:34816
	ds_read_b128 v[194:197], v161 offset:35840
	ds_read_b128 v[198:201], v161 offset:36864
	ds_read_b128 v[202:205], v161 offset:37888
	ds_read_b128 v[206:209], v161 offset:38912
	ds_read_b128 v[210:213], v161 offset:39936
	s_add_u32 s26, s44, 0x80000
	s_addc_u32 s27, s45, 0
	s_mov_b32 s44, m0
	s_mov_b32 m0, s53
	s_nop 0
	global_load_lds_dwordx4 v154, s[26:27]
	s_mov_b32 m0, s44
	s_nop 0
	s_mov_b32 s44, m0
	s_mov_b32 m0, s54
	s_nop 0
	global_load_lds_dwordx4 v156, s[26:27]
	s_mov_b32 m0, s44
	s_waitcnt vmcnt(8)
	s_waitcnt lgkmcnt(0)
	s_barrier
	s_setprio 1
	v_mfma_f32_16x16x32_bf16 v[128:131], v[132:135], v[182:185], v[128:131]
	v_mfma_f32_16x16x32_bf16 v[124:127], v[140:143], v[182:185], v[124:127]
	v_mfma_f32_16x16x32_bf16 v[112:115], v[132:135], v[190:193], v[112:115]
	v_mfma_f32_16x16x32_bf16 v[108:111], v[140:143], v[190:193], v[108:111]
	v_mfma_f32_16x16x32_bf16 v[96:99], v[132:135], v[198:201], v[96:99]
	v_mfma_f32_16x16x32_bf16 v[92:95], v[140:143], v[198:201], v[92:95]
	v_mfma_f32_16x16x32_bf16 v[80:83], v[132:135], v[206:209], v[80:83]
	v_mfma_f32_16x16x32_bf16 v[76:79], v[140:143], v[206:209], v[76:79]
	v_mfma_f32_16x16x32_bf16 v[128:131], v[136:139], v[186:189], v[128:131]
	v_mfma_f32_16x16x32_bf16 v[124:127], v[162:165], v[186:189], v[124:127]
	v_mfma_f32_16x16x32_bf16 v[112:115], v[136:139], v[194:197], v[112:115]
	v_mfma_f32_16x16x32_bf16 v[108:111], v[162:165], v[194:197], v[108:111]
	v_mfma_f32_16x16x32_bf16 v[96:99], v[136:139], v[202:205], v[96:99]
	v_mfma_f32_16x16x32_bf16 v[92:95], v[162:165], v[202:205], v[92:95]
	v_mfma_f32_16x16x32_bf16 v[80:83], v[136:139], v[210:213], v[80:83]
	v_mfma_f32_16x16x32_bf16 v[76:79], v[162:165], v[210:213], v[76:79]
	v_mfma_f32_16x16x32_bf16 v[120:123], v[166:169], v[182:185], v[120:123]
	v_mfma_f32_16x16x32_bf16 v[116:119], v[174:177], v[182:185], v[116:119]
	v_mfma_f32_16x16x32_bf16 v[104:107], v[166:169], v[190:193], v[104:107]
	v_mfma_f32_16x16x32_bf16 v[100:103], v[174:177], v[190:193], v[100:103]
	v_mfma_f32_16x16x32_bf16 v[88:91], v[166:169], v[198:201], v[88:91]
	v_mfma_f32_16x16x32_bf16 v[84:87], v[174:177], v[198:201], v[84:87]
	v_mfma_f32_16x16x32_bf16 v[72:75], v[166:169], v[206:209], v[72:75]
	v_mfma_f32_16x16x32_bf16 v[68:71], v[174:177], v[206:209], v[68:71]
	v_mfma_f32_16x16x32_bf16 v[120:123], v[170:173], v[186:189], v[120:123]
	v_mfma_f32_16x16x32_bf16 v[116:119], v[178:181], v[186:189], v[116:119]
	v_mfma_f32_16x16x32_bf16 v[104:107], v[170:173], v[194:197], v[104:107]
	v_mfma_f32_16x16x32_bf16 v[100:103], v[178:181], v[194:197], v[100:103]
	v_mfma_f32_16x16x32_bf16 v[88:91], v[170:173], v[202:205], v[88:91]
	v_mfma_f32_16x16x32_bf16 v[84:87], v[178:181], v[202:205], v[84:87]
	v_mfma_f32_16x16x32_bf16 v[72:75], v[170:173], v[210:213], v[72:75]
	v_mfma_f32_16x16x32_bf16 v[68:71], v[178:181], v[210:213], v[68:71]
	s_setprio 0
	s_barrier
; #define PG8_STAGE(bufoff, gbase, voff) do { _Pragma("unroll") for (int _i = 0; _i < 2; ++_i) { unsigned keep_; \
;         asm volatile("s_mov_b32 %0, m0\n\ts_mov_b32 m0, %3\n\ts_nop 0\n\tglobal_load_lds_dwordx4 %1, %2\n\ts_mov_b32 m0, %0" : "=&s"(keep_) : "v"((voff)[_i]), "s"((const char*)(gbase)), "s"(ldsbase + (unsigned)((bufoff) + _i * 8192)) : "memory"); } } while (0)
; #define PG8_WAIT_V(n) asm volatile("s_waitcnt vmcnt(" #n ")" ::: "memory")
; #define PG8_WAIT_L(n) asm volatile("s_waitcnt lgkmcnt(" #n ")" ::: "memory")
; #define PG8_BAR __builtin_amdgcn_s_barrier()
; #define PG8_SCHED __builtin_amdgcn_sched_barrier(0)
;     DI int nt(const Unit& u) const { return (u.aux & 8) ? PLED / 64 : ((u.aux & 4) ? (D_ / 2) / 64 : D_ / 64); }
; template <class Epi, class Sched, bool ALIGN_EPI, bool FP8 = false>
; DI void gemm_phase(LAS unsigned char* lds, const Gemm g, const Sched& S, const Epi& E) {
;     ...
;         for (int t = 0; t < nt; t += 2) {
;             if constexpr (Epi::MID) { if (t == (nt >> 1)) E.mid(acc, cur, wr, wc, fr, fq); }
;             const bool last = (t == nt - 2);
;             const char* a1 = cA + (size_t)(t + 1) * kstep;
;             const char* a2 = last ? nA : cA + (size_t)(t + 2) * kstep; const char* b2 = last ? nB : cB + (size_t)(t + 2) * kstep;
;             const char* a3 = a2 + kstep; const char* b3 = b2 + kstep;
;             PG8_LDB(B0, 0, 0); PG8_LDB(B1, 0, 1); PG8_SCHED; PG8_LDA(At, 0, 0); PG8_STAGE(PG8_SA(1, 1), a1 + hstepA, voffA);
;             PG8_WAIT_V(8); PG8_WAIT_L(0); PG8_BAR; PG8_MMA(0, 0, At, B0); PG8_MMA(0, 1, At, B1); PG8_BAR; PG8_SCHED;
;             PG8_LDA(At, 0, 1); PG8_STAGE(PG8_SB(0, 0), b2, voffB); PG8_STAGE(PG8_SB(0, 1), b2 + hstepB, voffB); PG8_STAGE(PG8_SA(0, 0), a2, voffA);
;             PG8_WAIT_V(8); PG8_WAIT_L(0); PG8_BAR; PG8_MMA(1, 0, At, B0); PG8_MMA(1, 1, At, B1); PG8_BAR; PG8_SCHED;
;             PG8_LDB(B0, 1, 0); PG8_LDB(B1, 1, 1); PG8_SCHED; PG8_LDA(At, 1, 0); PG8_STAGE(PG8_SA(0, 1), a2 + hstepA, voffA);
;             PG8_WAIT_V(8); PG8_WAIT_L(0); PG8_BAR; PG8_MMA(0, 0, At, B0); PG8_MMA(0, 1, At, B1); PG8_BAR; PG8_SCHED;
;             PG8_LDA(At, 1, 1); PG8_STAGE(PG8_SB(1, 0), b3, voffB); PG8_STAGE(PG8_SB(1, 1), b3 + hstepB, voffB); PG8_STAGE(PG8_SA(1, 0), a3, voffA);
;             PG8_WAIT_V(8); PG8_WAIT_L(0); PG8_BAR; PG8_MMA(1, 0, At, B0); PG8_MMA(1, 1, At, B1); PG8_BAR; PG8_SCHED;
	ds_read_b128 v[182:185], v161 offset:49152
	ds_read_b128 v[186:189], v161 offset:50176
	ds_read_b128 v[190:193], v161 offset:51200
	ds_read_b128 v[194:197], v161 offset:52224
	ds_read_b128 v[198:201], v161 offset:53248
	ds_read_b128 v[202:205], v161 offset:54272
	ds_read_b128 v[206:209], v161 offset:55296
	ds_read_b128 v[210:213], v161 offset:56320
	s_add_u32 s26, s42, 0x80
	s_addc_u32 s27, s43, 0
	s_mov_b32 s44, m0
	s_mov_b32 m0, s55
	s_nop 0
	global_load_lds_dwordx4 v155, s[26:27]
	s_mov_b32 m0, s44
	s_nop 0
	s_mov_b32 s44, m0
	s_mov_b32 m0, s56
	s_nop 0
	global_load_lds_dwordx4 v157, s[26:27]
	s_mov_b32 m0, s44
	s_add_u32 s26, s42, 0x80080
	s_addc_u32 s27, s43, 0
	s_mov_b32 s42, m0
	s_mov_b32 m0, s59
	s_nop 0
	global_load_lds_dwordx4 v155, s[26:27]
	s_mov_b32 m0, s42
	s_nop 0
	s_mov_b32 s42, m0
	s_mov_b32 m0, s60
	s_nop 0
	global_load_lds_dwordx4 v157, s[26:27]
	s_mov_b32 m0, s42
	s_mov_b32 s26, m0
	s_mov_b32 m0, s57
	s_nop 0
	global_load_lds_dwordx4 v154, s[40:41]
	s_mov_b32 m0, s26
	s_nop 0
	s_mov_b32 s26, m0
	s_mov_b32 m0, s58
	s_nop 0
	global_load_lds_dwordx4 v156, s[40:41]
	s_mov_b32 m0, s26
	s_waitcnt vmcnt(8)
	s_waitcnt lgkmcnt(0)
	s_barrier
	s_setprio 1
	v_mfma_f32_16x16x32_bf16 v[64:67], v[132:135], v[182:185], v[64:67]
	v_mfma_f32_16x16x32_bf16 v[60:63], v[140:143], v[182:185], v[60:63]
	v_mfma_f32_16x16x32_bf16 v[48:51], v[132:135], v[190:193], v[48:51]
	v_mfma_f32_16x16x32_bf16 v[44:47], v[140:143], v[190:193], v[44:47]
	v_mfma_f32_16x16x32_bf16 v[32:35], v[132:135], v[198:201], v[32:35]
	v_mfma_f32_16x16x32_bf16 v[28:31], v[140:143], v[198:201], v[28:31]
	v_mfma_f32_16x16x32_bf16 v[16:19], v[132:135], v[206:209], v[16:19]
	v_mfma_f32_16x16x32_bf16 v[12:15], v[140:143], v[206:209], v[12:15]
	v_mfma_f32_16x16x32_bf16 v[64:67], v[136:139], v[186:189], v[64:67]
	v_mfma_f32_16x16x32_bf16 v[60:63], v[162:165], v[186:189], v[60:63]
	v_mfma_f32_16x16x32_bf16 v[48:51], v[136:139], v[194:197], v[48:51]
	v_mfma_f32_16x16x32_bf16 v[44:47], v[162:165], v[194:197], v[44:47]
	v_mfma_f32_16x16x32_bf16 v[32:35], v[136:139], v[202:205], v[32:35]
	v_mfma_f32_16x16x32_bf16 v[28:31], v[162:165], v[202:205], v[28:31]
	v_mfma_f32_16x16x32_bf16 v[16:19], v[136:139], v[210:213], v[16:19]
	v_mfma_f32_16x16x32_bf16 v[12:15], v[162:165], v[210:213], v[12:15]
	v_mfma_f32_16x16x32_bf16 v[56:59], v[166:169], v[182:185], v[56:59]
	v_mfma_f32_16x16x32_bf16 v[52:55], v[174:177], v[182:185], v[52:55]
	v_mfma_f32_16x16x32_bf16 v[40:43], v[166:169], v[190:193], v[40:43]
	v_mfma_f32_16x16x32_bf16 v[36:39], v[174:177], v[190:193], v[36:39]
	v_mfma_f32_16x16x32_bf16 v[24:27], v[166:169], v[198:201], v[24:27]
	v_mfma_f32_16x16x32_bf16 v[20:23], v[174:177], v[198:201], v[20:23]
	v_mfma_f32_16x16x32_bf16 v[6:9], v[166:169], v[206:209], v[8:11]
	v_mfma_f32_16x16x32_bf16 v[2:5], v[174:177], v[206:209], v[2:5]
	v_mfma_f32_16x16x32_bf16 v[56:59], v[170:173], v[186:189], v[56:59]
	v_mfma_f32_16x16x32_bf16 v[52:55], v[178:181], v[186:189], v[52:55]
	v_mfma_f32_16x16x32_bf16 v[40:43], v[170:173], v[194:197], v[40:43]
	v_mfma_f32_16x16x32_bf16 v[36:39], v[178:181], v[194:197], v[36:39]
	v_mfma_f32_16x16x32_bf16 v[24:27], v[170:173], v[202:205], v[24:27]
	v_mfma_f32_16x16x32_bf16 v[20:23], v[178:181], v[202:205], v[20:23]
	v_mfma_f32_16x16x32_bf16 v[8:11], v[170:173], v[210:213], v[6:9]
	v_mfma_f32_16x16x32_bf16 v[4:7], v[178:181], v[210:213], v[2:5]
	s_setprio 0
	s_barrier
	s_add_i32 s69, s69, 2
	s_add_u32 s67, s67, 0x100
	s_addc_u32 s68, s68, 0
	s_cmp_gt_u32 s69, 29
	s_cbranch_scc1 .LBB0_491
	s_mov_b64 s[26:27], s[28:29]
	s_cmp_lg_u32 s69, 14
	s_cbranch_scc0 .LBB0_488
	s_branch .LBB0_489

; #define PG8_STAGE(bufoff, gbase, voff) do { _Pragma("unroll") for (int _i = 0; _i < 2; ++_i) { unsigned keep_; \
;         asm volatile("s_mov_b32 %0, m0\n\ts_mov_b32 m0, %3\n\ts_nop 0\n\tglobal_load_lds_dwordx4 %1, %2\n\ts_mov_b32 m0, %0" : "=&s"(keep_) : "v"((voff)[_i]), "s"((const char*)(gbase)), "s"(ldsbase + (unsigned)((bufoff) + _i * 8192)) : "memory"); } } while (0)
; #define PG8_WAIT_V(n) asm volatile("s_waitcnt vmcnt(" #n ")" ::: "memory")
; #define PG8_WAIT_L(n) asm volatile("s_waitcnt lgkmcnt(" #n ")" ::: "memory")
; #define PG8_BAR __builtin_amdgcn_s_barrier()
; #define PG8_SCHED __builtin_amdgcn_sched_barrier(0)
; template <class Epi, class Sched, bool ALIGN_EPI, bool FP8 = false>
; DI void gemm_phase(LAS unsigned char* lds, const Gemm g, const Sched& S, const Epi& E) {
;     ...
;             PG8_LDB(B0, 0, 0); PG8_LDB(B1, 0, 1); PG8_SCHED; PG8_LDA(At, 0, 0); PG8_STAGE(PG8_SA(1, 1), a1 + hstepA, voffA);
;             PG8_WAIT_V(8); PG8_WAIT_L(0); PG8_BAR; PG8_MMA(0, 0, At, B0); PG8_MMA(0, 1, At, B1); PG8_BAR; PG8_SCHED;
;             PG8_LDA(At, 0, 1); PG8_STAGE(PG8_SB(0, 0), b2, voffB); PG8_STAGE(PG8_SB(0, 1), b2 + hstepB, voffB); PG8_STAGE(PG8_SA(0, 0), a2, voffA);
;             PG8_WAIT_V(8); PG8_WAIT_L(0); PG8_BAR; PG8_MMA(1, 0, At, B0); PG8_MMA(1, 1, At, B1); PG8_BAR; PG8_SCHED;
.LBB0_569:
	ds_read_b128 v[146:149], v140
	ds_read_b128 v[150:153], v140 offset:1024
	ds_read_b128 v[154:157], v140 offset:2048
	ds_read_b128 v[158:161], v140 offset:3072
	ds_read_b128 v[162:165], v141
	ds_read_b128 v[166:169], v141 offset:1024
	ds_read_b128 v[170:173], v141 offset:2048
	ds_read_b128 v[174:177], v141 offset:3072
	s_add_u32 s66, s64, 0x100
	s_addc_u32 s67, s65, 0
	s_cmp_eq_u32 s97, 28
	s_cselect_b32 s72, s93, s66
	s_cselect_b32 s73, s57, s67
	s_cselect_b32 s70, s94, s95
	s_cselect_b32 s71, s55, s96
	s_add_u32 s68, s72, 0x80
	s_addc_u32 s69, s73, 0
	ds_read_b128 v[178:181], v142
	ds_read_b128 v[182:185], v142 offset:1024
	ds_read_b128 v[186:189], v142 offset:2048
	ds_read_b128 v[190:193], v142 offset:3072
	ds_read_b128 v[194:197], v142 offset:4096
	ds_read_b128 v[198:201], v142 offset:5120
	ds_read_b128 v[202:205], v142 offset:6144
	ds_read_b128 v[206:209], v142 offset:7168
	s_add_u32 s64, s64, 0x80080
	s_addc_u32 s65, s65, 0
	s_mov_b32 vcc_lo, m0
	s_mov_b32 m0, s89
	s_nop 0
	global_load_lds_dwordx4 v134, s[64:65]
	s_mov_b32 m0, vcc_lo
	s_nop 0
	s_mov_b32 vcc_lo, m0
	s_mov_b32 m0, s90
	s_nop 0
	global_load_lds_dwordx4 v136, s[64:65]
	s_mov_b32 m0, vcc_lo
	s_waitcnt vmcnt(8)
	s_waitcnt lgkmcnt(0)
	s_barrier
	s_setprio 1
	v_mfma_f32_16x16x32_bf16 v[124:127], v[146:149], v[178:181], v[124:127]
	v_mfma_f32_16x16x32_bf16 v[120:123], v[154:157], v[178:181], v[120:123]
	v_mfma_f32_16x16x32_bf16 v[108:111], v[146:149], v[186:189], v[108:111]
	v_mfma_f32_16x16x32_bf16 v[104:107], v[154:157], v[186:189], v[104:107]
	v_mfma_f32_16x16x32_bf16 v[92:95], v[146:149], v[194:197], v[92:95]
	v_mfma_f32_16x16x32_bf16 v[88:91], v[154:157], v[194:197], v[88:91]
	v_mfma_f32_16x16x32_bf16 v[76:79], v[146:149], v[202:205], v[76:79]
	v_mfma_f32_16x16x32_bf16 v[72:75], v[154:157], v[202:205], v[72:75]
	v_mfma_f32_16x16x32_bf16 v[124:127], v[150:153], v[182:185], v[124:127]
	v_mfma_f32_16x16x32_bf16 v[120:123], v[158:161], v[182:185], v[120:123]
	v_mfma_f32_16x16x32_bf16 v[108:111], v[150:153], v[190:193], v[108:111]
	v_mfma_f32_16x16x32_bf16 v[104:107], v[158:161], v[190:193], v[104:107]
	v_mfma_f32_16x16x32_bf16 v[92:95], v[150:153], v[198:201], v[92:95]
	v_mfma_f32_16x16x32_bf16 v[88:91], v[158:161], v[198:201], v[88:91]
	v_mfma_f32_16x16x32_bf16 v[76:79], v[150:153], v[206:209], v[76:79]
	v_mfma_f32_16x16x32_bf16 v[72:75], v[158:161], v[206:209], v[72:75]
	v_mfma_f32_16x16x32_bf16 v[116:119], v[162:165], v[178:181], v[116:119]
	v_mfma_f32_16x16x32_bf16 v[112:115], v[170:173], v[178:181], v[112:115]
	v_mfma_f32_16x16x32_bf16 v[100:103], v[162:165], v[186:189], v[100:103]
	v_mfma_f32_16x16x32_bf16 v[96:99], v[170:173], v[186:189], v[96:99]
	v_mfma_f32_16x16x32_bf16 v[84:87], v[162:165], v[194:197], v[84:87]
	v_mfma_f32_16x16x32_bf16 v[80:83], v[170:173], v[194:197], v[80:83]
	v_mfma_f32_16x16x32_bf16 v[68:71], v[162:165], v[202:205], v[68:71]
	v_mfma_f32_16x16x32_bf16 v[64:67], v[170:173], v[202:205], v[64:67]
	v_mfma_f32_16x16x32_bf16 v[116:119], v[166:169], v[182:185], v[116:119]
	v_mfma_f32_16x16x32_bf16 v[112:115], v[174:177], v[182:185], v[112:115]
	v_mfma_f32_16x16x32_bf16 v[100:103], v[166:169], v[190:193], v[100:103]
	v_mfma_f32_16x16x32_bf16 v[96:99], v[174:177], v[190:193], v[96:99]
	v_mfma_f32_16x16x32_bf16 v[84:87], v[166:169], v[198:201], v[84:87]
	v_mfma_f32_16x16x32_bf16 v[80:83], v[174:177], v[198:201], v[80:83]
	v_mfma_f32_16x16x32_bf16 v[68:71], v[166:169], v[206:209], v[68:71]
	v_mfma_f32_16x16x32_bf16 v[64:67], v[174:177], v[206:209], v[64:67]
	s_setprio 0
	s_barrier
	ds_read_b128 v[178:181], v142 offset:16384
	ds_read_b128 v[182:185], v142 offset:17408
	ds_read_b128 v[186:189], v142 offset:18432
	ds_read_b128 v[190:193], v142 offset:19456
	ds_read_b128 v[194:197], v142 offset:20480
	ds_read_b128 v[198:201], v142 offset:21504
	ds_read_b128 v[202:205], v142 offset:22528
	ds_read_b128 v[206:209], v142 offset:23552
	s_mov_b32 s64, m0
	s_mov_b32 m0, s63
	s_nop 0
	global_load_lds_dwordx4 v135, s[70:71]
	s_mov_b32 m0, s64
	s_nop 0
	s_mov_b32 s64, m0
	s_mov_b32 m0, s75
	s_nop 0
	global_load_lds_dwordx4 v137, s[70:71]
	s_mov_b32 m0, s64
	s_add_u32 s64, s70, 0x80000
	s_addc_u32 s65, s71, 0
	s_mov_b32 vcc_lo, m0
	s_mov_b32 m0, s77
	s_nop 0
	global_load_lds_dwordx4 v135, s[64:65]
	s_mov_b32 m0, vcc_lo
	s_nop 0
	s_mov_b32 vcc_lo, m0
	s_mov_b32 m0, s79
	s_nop 0
	global_load_lds_dwordx4 v137, s[64:65]
	s_mov_b32 m0, vcc_lo
	s_mov_b32 s64, m0
	s_mov_b32 m0, s74
	s_nop 0
	global_load_lds_dwordx4 v134, s[72:73]
	s_mov_b32 m0, s64
	s_nop 0
	s_mov_b32 s64, m0
	s_mov_b32 m0, s80
	s_nop 0
	global_load_lds_dwordx4 v136, s[72:73]
	s_mov_b32 m0, s64
	s_waitcnt vmcnt(8)
	s_waitcnt lgkmcnt(0)
	s_barrier
; #define PG8_STAGE(bufoff, gbase, voff) do { _Pragma("unroll") for (int _i = 0; _i < 2; ++_i) { unsigned keep_; \
;         asm volatile("s_mov_b32 %0, m0\n\ts_mov_b32 m0, %3\n\ts_nop 0\n\tglobal_load_lds_dwordx4 %1, %2\n\ts_mov_b32 m0, %0" : "=&s"(keep_) : "v"((voff)[_i]), "s"((const char*)(gbase)), "s"(ldsbase + (unsigned)((bufoff) + _i * 8192)) : "memory"); } } while (0)
; #define PG8_WAIT_V(n) asm volatile("s_waitcnt vmcnt(" #n ")" ::: "memory")
; #define PG8_WAIT_L(n) asm volatile("s_waitcnt lgkmcnt(" #n ")" ::: "memory")
; #define PG8_BAR __builtin_amdgcn_s_barrier()
; #define PG8_SCHED __builtin_amdgcn_sched_barrier(0)
; template <class Epi, class Sched, bool ALIGN_EPI, bool FP8 = false>
; DI void gemm_phase(LAS unsigned char* lds, const Gemm g, const Sched& S, const Epi& E) {
;     ...
;             PG8_WAIT_V(8); PG8_WAIT_L(0); PG8_BAR; PG8_MMA(1, 0, At, B0); PG8_MMA(1, 1, At, B1); PG8_BAR; PG8_SCHED;
;             PG8_LDB(B0, 1, 0); PG8_LDB(B1, 1, 1); PG8_SCHED; PG8_LDA(At, 1, 0); PG8_STAGE(PG8_SA(0, 1), a2 + hstepA, voffA);
;             PG8_WAIT_V(8); PG8_WAIT_L(0); PG8_BAR; PG8_MMA(0, 0, At, B0); PG8_MMA(0, 1, At, B1); PG8_BAR; PG8_SCHED;
	s_setprio 1
	v_mfma_f32_16x16x32_bf16 v[60:63], v[146:149], v[178:181], v[60:63]
	v_mfma_f32_16x16x32_bf16 v[56:59], v[154:157], v[178:181], v[56:59]
	v_mfma_f32_16x16x32_bf16 v[44:47], v[146:149], v[186:189], v[44:47]
	v_mfma_f32_16x16x32_bf16 v[40:43], v[154:157], v[186:189], v[40:43]
	v_mfma_f32_16x16x32_bf16 v[28:31], v[146:149], v[194:197], v[28:31]
	v_mfma_f32_16x16x32_bf16 v[24:27], v[154:157], v[194:197], v[24:27]
	v_mfma_f32_16x16x32_bf16 v[12:15], v[146:149], v[202:205], v[12:15]
	v_mfma_f32_16x16x32_bf16 v[8:11], v[154:157], v[202:205], v[8:11]
	v_mfma_f32_16x16x32_bf16 v[60:63], v[150:153], v[182:185], v[60:63]
	v_mfma_f32_16x16x32_bf16 v[56:59], v[158:161], v[182:185], v[56:59]
	v_mfma_f32_16x16x32_bf16 v[44:47], v[150:153], v[190:193], v[44:47]
	v_mfma_f32_16x16x32_bf16 v[40:43], v[158:161], v[190:193], v[40:43]
	v_mfma_f32_16x16x32_bf16 v[28:31], v[150:153], v[198:201], v[28:31]
	v_mfma_f32_16x16x32_bf16 v[24:27], v[158:161], v[198:201], v[24:27]
	v_mfma_f32_16x16x32_bf16 v[12:15], v[150:153], v[206:209], v[12:15]
	v_mfma_f32_16x16x32_bf16 v[8:11], v[158:161], v[206:209], v[8:11]
	v_mfma_f32_16x16x32_bf16 v[52:55], v[162:165], v[178:181], v[52:55]
	v_mfma_f32_16x16x32_bf16 v[48:51], v[170:173], v[178:181], v[48:51]
	v_mfma_f32_16x16x32_bf16 v[36:39], v[162:165], v[186:189], v[36:39]
	v_mfma_f32_16x16x32_bf16 v[32:35], v[170:173], v[186:189], v[32:35]
	v_mfma_f32_16x16x32_bf16 v[20:23], v[162:165], v[194:197], v[20:23]
	v_mfma_f32_16x16x32_bf16 v[16:19], v[170:173], v[194:197], v[16:19]
	v_mfma_f32_16x16x32_bf16 v[4:7], v[162:165], v[202:205], v[4:7]
	v_mfma_f32_16x16x32_bf16 v[0:3], v[170:173], v[202:205], v[0:3]
	v_mfma_f32_16x16x32_bf16 v[52:55], v[166:169], v[182:185], v[52:55]
	v_mfma_f32_16x16x32_bf16 v[48:51], v[174:177], v[182:185], v[48:51]
	v_mfma_f32_16x16x32_bf16 v[36:39], v[166:169], v[190:193], v[36:39]
	v_mfma_f32_16x16x32_bf16 v[32:35], v[174:177], v[190:193], v[32:35]
	v_mfma_f32_16x16x32_bf16 v[20:23], v[166:169], v[198:201], v[20:23]
	v_mfma_f32_16x16x32_bf16 v[16:19], v[174:177], v[198:201], v[16:19]
	v_mfma_f32_16x16x32_bf16 v[4:7], v[166:169], v[206:209], v[4:7]
	v_mfma_f32_16x16x32_bf16 v[0:3], v[174:177], v[206:209], v[0:3]
	s_setprio 0
	s_barrier
	ds_read_b128 v[146:149], v143
	ds_read_b128 v[150:153], v143 offset:1024
	ds_read_b128 v[154:157], v143 offset:2048
	ds_read_b128 v[158:161], v143 offset:3072
	ds_read_b128 v[162:165], v144
	ds_read_b128 v[166:169], v144 offset:1024
	ds_read_b128 v[170:173], v144 offset:2048
	ds_read_b128 v[174:177], v144 offset:3072
	ds_read_b128 v[178:181], v142 offset:32768
	ds_read_b128 v[182:185], v142 offset:33792
	ds_read_b128 v[186:189], v142 offset:34816
	ds_read_b128 v[190:193], v142 offset:35840
	ds_read_b128 v[194:197], v142 offset:36864
	ds_read_b128 v[198:201], v142 offset:37888
	ds_read_b128 v[202:205], v142 offset:38912
	ds_read_b128 v[206:209], v142 offset:39936
	s_add_u32 s64, s72, 0x80000
	s_addc_u32 s65, s73, 0
	s_mov_b32 s72, m0
	s_mov_b32 m0, s81
	s_nop 0
	global_load_lds_dwordx4 v134, s[64:65]
	s_mov_b32 m0, s72
	s_nop 0
	s_mov_b32 s72, m0
	s_mov_b32 m0, s82
	s_nop 0
	global_load_lds_dwordx4 v136, s[64:65]
	s_mov_b32 m0, s72
	s_waitcnt vmcnt(8)
	s_waitcnt lgkmcnt(0)
	s_barrier
	s_setprio 1
	v_mfma_f32_16x16x32_bf16 v[124:127], v[146:149], v[178:181], v[124:127]
	v_mfma_f32_16x16x32_bf16 v[120:123], v[154:157], v[178:181], v[120:123]
	v_mfma_f32_16x16x32_bf16 v[108:111], v[146:149], v[186:189], v[108:111]
	v_mfma_f32_16x16x32_bf16 v[104:107], v[154:157], v[186:189], v[104:107]
	v_mfma_f32_16x16x32_bf16 v[92:95], v[146:149], v[194:197], v[92:95]
	v_mfma_f32_16x16x32_bf16 v[88:91], v[154:157], v[194:197], v[88:91]
	v_mfma_f32_16x16x32_bf16 v[76:79], v[146:149], v[202:205], v[76:79]
	v_mfma_f32_16x16x32_bf16 v[72:75], v[154:157], v[202:205], v[72:75]
	v_mfma_f32_16x16x32_bf16 v[124:127], v[150:153], v[182:185], v[124:127]
	v_mfma_f32_16x16x32_bf16 v[120:123], v[158:161], v[182:185], v[120:123]
	v_mfma_f32_16x16x32_bf16 v[108:111], v[150:153], v[190:193], v[108:111]
	v_mfma_f32_16x16x32_bf16 v[104:107], v[158:161], v[190:193], v[104:107]
	v_mfma_f32_16x16x32_bf16 v[92:95], v[150:153], v[198:201], v[92:95]
	v_mfma_f32_16x16x32_bf16 v[88:91], v[158:161], v[198:201], v[88:91]
	v_mfma_f32_16x16x32_bf16 v[76:79], v[150:153], v[206:209], v[76:79]
	v_mfma_f32_16x16x32_bf16 v[72:75], v[158:161], v[206:209], v[72:75]
	v_mfma_f32_16x16x32_bf16 v[116:119], v[162:165], v[178:181], v[116:119]
	v_mfma_f32_16x16x32_bf16 v[112:115], v[170:173], v[178:181], v[112:115]
	v_mfma_f32_16x16x32_bf16 v[100:103], v[162:165], v[186:189], v[100:103]
	v_mfma_f32_16x16x32_bf16 v[96:99], v[170:173], v[186:189], v[96:99]
	v_mfma_f32_16x16x32_bf16 v[84:87], v[162:165], v[194:197], v[84:87]
	v_mfma_f32_16x16x32_bf16 v[80:83], v[170:173], v[194:197], v[80:83]
	v_mfma_f32_16x16x32_bf16 v[68:71], v[162:165], v[202:205], v[68:71]
	v_mfma_f32_16x16x32_bf16 v[64:67], v[170:173], v[202:205], v[64:67]
	v_mfma_f32_16x16x32_bf16 v[116:119], v[166:169], v[182:185], v[116:119]
	v_mfma_f32_16x16x32_bf16 v[112:115], v[174:177], v[182:185], v[112:115]
	v_mfma_f32_16x16x32_bf16 v[100:103], v[166:169], v[190:193], v[100:103]
	v_mfma_f32_16x16x32_bf16 v[96:99], v[174:177], v[190:193], v[96:99]
	v_mfma_f32_16x16x32_bf16 v[84:87], v[166:169], v[198:201], v[84:87]
	v_mfma_f32_16x16x32_bf16 v[80:83], v[174:177], v[198:201], v[80:83]
	v_mfma_f32_16x16x32_bf16 v[68:71], v[166:169], v[206:209], v[68:71]
	v_mfma_f32_16x16x32_bf16 v[64:67], v[174:177], v[206:209], v[64:67]
	s_setprio 0
	s_barrier
; #define PG8_STAGE(bufoff, gbase, voff) do { _Pragma("unroll") for (int _i = 0; _i < 2; ++_i) { unsigned keep_; \
;         asm volatile("s_mov_b32 %0, m0\n\ts_mov_b32 m0, %3\n\ts_nop 0\n\tglobal_load_lds_dwordx4 %1, %2\n\ts_mov_b32 m0, %0" : "=&s"(keep_) : "v"((voff)[_i]), "s"((const char*)(gbase)), "s"(ldsbase + (unsigned)((bufoff) + _i * 8192)) : "memory"); } } while (0)
; #define PG8_WAIT_V(n) asm volatile("s_waitcnt vmcnt(" #n ")" ::: "memory")
; #define PG8_WAIT_L(n) asm volatile("s_waitcnt lgkmcnt(" #n ")" ::: "memory")
; #define PG8_BAR __builtin_amdgcn_s_barrier()
; #define PG8_SCHED __builtin_amdgcn_sched_barrier(0)
; template <class Epi, class Sched, bool ALIGN_EPI, bool FP8 = false>
; DI void gemm_phase(LAS unsigned char* lds, const Gemm g, const Sched& S, const Epi& E) {
;     ...
;             PG8_LDA(At, 1, 1); PG8_STAGE(PG8_SB(1, 0), b3, voffB); PG8_STAGE(PG8_SB(1, 1), b3 + hstepB, voffB); PG8_STAGE(PG8_SA(1, 0), a3, voffA);
;             PG8_WAIT_V(8); PG8_WAIT_L(0); PG8_BAR; PG8_MMA(1, 0, At, B0); PG8_MMA(1, 1, At, B1); PG8_BAR; PG8_SCHED;
;         }
;         if constexpr (ALIGN_EPI) { if (wr == 0) PG8_BAR; }
;         E(acc, cur, wr, wc, fr, fq);
;         if (!has_next) break;
	ds_read_b128 v[178:181], v142 offset:49152
	ds_read_b128 v[182:185], v142 offset:50176
	ds_read_b128 v[186:189], v142 offset:51200
	ds_read_b128 v[190:193], v142 offset:52224
	ds_read_b128 v[194:197], v142 offset:53248
	ds_read_b128 v[198:201], v142 offset:54272
	ds_read_b128 v[202:205], v142 offset:55296
	ds_read_b128 v[206:209], v142 offset:56320
	s_add_u32 s64, s70, 0x80
	s_addc_u32 s65, s71, 0
	s_mov_b32 s72, m0
	s_mov_b32 m0, s83
	s_nop 0
	global_load_lds_dwordx4 v135, s[64:65]
	s_mov_b32 m0, s72
	s_nop 0
	s_mov_b32 s72, m0
	s_mov_b32 m0, s84
	s_nop 0
	global_load_lds_dwordx4 v137, s[64:65]
	s_mov_b32 m0, s72
	s_add_u32 s64, s70, 0x80080
	s_addc_u32 s65, s71, 0
	s_mov_b32 s70, m0
	s_mov_b32 m0, s87
	s_nop 0
	global_load_lds_dwordx4 v135, s[64:65]
	s_mov_b32 m0, s70
	s_nop 0
	s_mov_b32 s70, m0
	s_mov_b32 m0, s88
	s_nop 0
	global_load_lds_dwordx4 v137, s[64:65]
	s_mov_b32 m0, s70
	s_mov_b32 s64, m0
	s_mov_b32 m0, s85
	s_nop 0
	global_load_lds_dwordx4 v134, s[68:69]
	s_mov_b32 m0, s64
	s_nop 0
	s_mov_b32 s64, m0
	s_mov_b32 m0, s86
	s_nop 0
	global_load_lds_dwordx4 v136, s[68:69]
	s_mov_b32 m0, s64
	s_waitcnt vmcnt(8)
	s_waitcnt lgkmcnt(0)
	s_barrier
	s_setprio 1
	v_mfma_f32_16x16x32_bf16 v[60:63], v[146:149], v[178:181], v[60:63]
	v_mfma_f32_16x16x32_bf16 v[56:59], v[154:157], v[178:181], v[56:59]
	v_mfma_f32_16x16x32_bf16 v[44:47], v[146:149], v[186:189], v[44:47]
	v_mfma_f32_16x16x32_bf16 v[40:43], v[154:157], v[186:189], v[40:43]
	v_mfma_f32_16x16x32_bf16 v[28:31], v[146:149], v[194:197], v[28:31]
	v_mfma_f32_16x16x32_bf16 v[24:27], v[154:157], v[194:197], v[24:27]
	v_mfma_f32_16x16x32_bf16 v[12:15], v[146:149], v[202:205], v[12:15]
	v_mfma_f32_16x16x32_bf16 v[8:11], v[154:157], v[202:205], v[8:11]
	v_mfma_f32_16x16x32_bf16 v[60:63], v[150:153], v[182:185], v[60:63]
	v_mfma_f32_16x16x32_bf16 v[56:59], v[158:161], v[182:185], v[56:59]
	v_mfma_f32_16x16x32_bf16 v[44:47], v[150:153], v[190:193], v[44:47]
	v_mfma_f32_16x16x32_bf16 v[40:43], v[158:161], v[190:193], v[40:43]
	v_mfma_f32_16x16x32_bf16 v[28:31], v[150:153], v[198:201], v[28:31]
	v_mfma_f32_16x16x32_bf16 v[24:27], v[158:161], v[198:201], v[24:27]
	v_mfma_f32_16x16x32_bf16 v[12:15], v[150:153], v[206:209], v[12:15]
	v_mfma_f32_16x16x32_bf16 v[8:11], v[158:161], v[206:209], v[8:11]
	v_mfma_f32_16x16x32_bf16 v[52:55], v[162:165], v[178:181], v[52:55]
	v_mfma_f32_16x16x32_bf16 v[48:51], v[170:173], v[178:181], v[48:51]
	v_mfma_f32_16x16x32_bf16 v[36:39], v[162:165], v[186:189], v[36:39]
	v_mfma_f32_16x16x32_bf16 v[32:35], v[170:173], v[186:189], v[32:35]
	v_mfma_f32_16x16x32_bf16 v[20:23], v[162:165], v[194:197], v[20:23]
	v_mfma_f32_16x16x32_bf16 v[16:19], v[170:173], v[194:197], v[16:19]
	v_mfma_f32_16x16x32_bf16 v[4:7], v[162:165], v[202:205], v[4:7]
	v_mfma_f32_16x16x32_bf16 v[0:3], v[170:173], v[202:205], v[0:3]
	v_mfma_f32_16x16x32_bf16 v[52:55], v[166:169], v[182:185], v[52:55]
	v_mfma_f32_16x16x32_bf16 v[48:51], v[174:177], v[182:185], v[48:51]
	v_mfma_f32_16x16x32_bf16 v[36:39], v[166:169], v[190:193], v[36:39]
	v_mfma_f32_16x16x32_bf16 v[32:35], v[174:177], v[190:193], v[32:35]
	v_mfma_f32_16x16x32_bf16 v[20:23], v[166:169], v[198:201], v[20:23]
	v_mfma_f32_16x16x32_bf16 v[16:19], v[174:177], v[198:201], v[16:19]
	v_mfma_f32_16x16x32_bf16 v[4:7], v[166:169], v[206:209], v[4:7]
	v_mfma_f32_16x16x32_bf16 v[0:3], v[174:177], v[206:209], v[0:3]
	s_setprio 0
	s_barrier
	s_add_i32 s97, s97, 2
	s_add_u32 s95, s95, 0x100
	s_addc_u32 s96, s96, 0
	s_cmp_gt_u32 s97, 29
	s_mov_b64 s[64:65], s[66:67]
	s_cbranch_scc0 .LBB0_569
	s_and_b64 vcc, exec, s[14:15]
	s_cbranch_vccz .LBB0_572
	s_barrier

; #define PG8_STAGE(bufoff, gbase, voff) do { _Pragma("unroll") for (int _i = 0; _i < 2; ++_i) { unsigned keep_; \
;         asm volatile("s_mov_b32 %0, m0\n\ts_mov_b32 m0, %3\n\ts_nop 0\n\tglobal_load_lds_dwordx4 %1, %2\n\ts_mov_b32 m0, %0" : "=&s"(keep_) : "v"((voff)[_i]), "s"((const char*)(gbase)), "s"(ldsbase + (unsigned)((bufoff) + _i * 8192)) : "memory"); } } while (0)
; #define PG8_WAIT_V(n) asm volatile("s_waitcnt vmcnt(" #n ")" ::: "memory")
; #define PG8_WAIT_L(n) asm volatile("s_waitcnt lgkmcnt(" #n ")" ::: "memory")
; #define PG8_BAR __builtin_amdgcn_s_barrier()
; #define PG8_SCHED __builtin_amdgcn_sched_barrier(0)
; template <class Epi, class Sched, bool ALIGN_EPI, bool FP8 = false>
; DI void gemm_phase(LAS unsigned char* lds, const Gemm g, const Sched& S, const Epi& E) {
;     ...
;             PG8_LDB(B0, 0, 0); PG8_LDB(B1, 0, 1); PG8_SCHED; PG8_LDA(At, 0, 0); PG8_STAGE(PG8_SA(1, 1), a1 + hstepA, voffA);
;             PG8_WAIT_V(8); PG8_WAIT_L(0); PG8_BAR; PG8_MMA(0, 0, At, B0); PG8_MMA(0, 1, At, B1); PG8_BAR; PG8_SCHED;
;             PG8_LDA(At, 0, 1); PG8_STAGE(PG8_SB(0, 0), b2, voffB); PG8_STAGE(PG8_SB(0, 1), b2 + hstepB, voffB); PG8_STAGE(PG8_SA(0, 0), a2, voffA);
;             PG8_WAIT_V(8); PG8_WAIT_L(0); PG8_BAR; PG8_MMA(1, 0, At, B0); PG8_MMA(1, 1, At, B1); PG8_BAR; PG8_SCHED;
.LBB0_700:
	ds_read_b128 v[148:151], v142
	ds_read_b128 v[152:155], v142 offset:1024
	ds_read_b128 v[156:159], v142 offset:2048
	ds_read_b128 v[160:163], v142 offset:3072
	ds_read_b128 v[164:167], v143
	ds_read_b128 v[168:171], v143 offset:1024
	ds_read_b128 v[172:175], v143 offset:2048
	ds_read_b128 v[176:179], v143 offset:3072
	s_add_u32 s26, s24, 0x100
	s_addc_u32 s27, s25, 0
	s_cmp_eq_u32 s71, 28
	s_cselect_b32 s42, s67, s26
	s_cselect_b32 s43, s17, s27
	s_cselect_b32 s40, s68, s69
	s_cselect_b32 s41, s13, s70
	s_add_u32 s28, s42, 0x80
	s_addc_u32 s29, s43, 0
	ds_read_b128 v[180:183], v144
	ds_read_b128 v[184:187], v144 offset:1024
	ds_read_b128 v[188:191], v144 offset:2048
	ds_read_b128 v[192:195], v144 offset:3072
	ds_read_b128 v[196:199], v144 offset:4096
	ds_read_b128 v[200:203], v144 offset:5120
	ds_read_b128 v[204:207], v144 offset:6144
	ds_read_b128 v[208:211], v144 offset:7168
	s_add_u32 s24, s24, 0x80080
	s_addc_u32 s25, s25, 0
	s_mov_b32 s72, m0
	s_mov_b32 m0, s61
	s_nop 0
	global_load_lds_dwordx4 v136, s[24:25]
	s_mov_b32 m0, s72
	s_nop 0
	s_mov_b32 s72, m0
	s_mov_b32 m0, s62
	s_nop 0
	global_load_lds_dwordx4 v138, s[24:25]
	s_mov_b32 m0, s72
	s_waitcnt vmcnt(8)
	s_waitcnt lgkmcnt(0)
	s_barrier
	s_setprio 1
	v_mfma_f32_16x16x32_bf16 v[124:127], v[148:151], v[180:183], v[124:127]
	v_mfma_f32_16x16x32_bf16 v[116:119], v[156:159], v[180:183], v[116:119]
	v_mfma_f32_16x16x32_bf16 v[108:111], v[148:151], v[188:191], v[108:111]
	v_mfma_f32_16x16x32_bf16 v[100:103], v[156:159], v[188:191], v[100:103]
	v_mfma_f32_16x16x32_bf16 v[92:95], v[148:151], v[196:199], v[92:95]
	v_mfma_f32_16x16x32_bf16 v[84:87], v[156:159], v[196:199], v[84:87]
	v_mfma_f32_16x16x32_bf16 v[76:79], v[148:151], v[204:207], v[76:79]
	v_mfma_f32_16x16x32_bf16 v[68:71], v[156:159], v[204:207], v[68:71]
	v_mfma_f32_16x16x32_bf16 v[124:127], v[152:155], v[184:187], v[124:127]
	v_mfma_f32_16x16x32_bf16 v[116:119], v[160:163], v[184:187], v[116:119]
	v_mfma_f32_16x16x32_bf16 v[108:111], v[152:155], v[192:195], v[108:111]
	v_mfma_f32_16x16x32_bf16 v[100:103], v[160:163], v[192:195], v[100:103]
	v_mfma_f32_16x16x32_bf16 v[92:95], v[152:155], v[200:203], v[92:95]
	v_mfma_f32_16x16x32_bf16 v[84:87], v[160:163], v[200:203], v[84:87]
	v_mfma_f32_16x16x32_bf16 v[76:79], v[152:155], v[208:211], v[76:79]
	v_mfma_f32_16x16x32_bf16 v[68:71], v[160:163], v[208:211], v[68:71]
	v_mfma_f32_16x16x32_bf16 v[120:123], v[164:167], v[180:183], v[120:123]
	v_mfma_f32_16x16x32_bf16 v[112:115], v[172:175], v[180:183], v[112:115]
	v_mfma_f32_16x16x32_bf16 v[104:107], v[164:167], v[188:191], v[104:107]
	v_mfma_f32_16x16x32_bf16 v[96:99], v[172:175], v[188:191], v[96:99]
	v_mfma_f32_16x16x32_bf16 v[88:91], v[164:167], v[196:199], v[88:91]
	v_mfma_f32_16x16x32_bf16 v[80:83], v[172:175], v[196:199], v[80:83]
	v_mfma_f32_16x16x32_bf16 v[72:75], v[164:167], v[204:207], v[72:75]
	v_mfma_f32_16x16x32_bf16 v[64:67], v[172:175], v[204:207], v[64:67]
	v_mfma_f32_16x16x32_bf16 v[120:123], v[168:171], v[184:187], v[120:123]
	v_mfma_f32_16x16x32_bf16 v[112:115], v[176:179], v[184:187], v[112:115]
	v_mfma_f32_16x16x32_bf16 v[104:107], v[168:171], v[192:195], v[104:107]
	v_mfma_f32_16x16x32_bf16 v[96:99], v[176:179], v[192:195], v[96:99]
	v_mfma_f32_16x16x32_bf16 v[88:91], v[168:171], v[200:203], v[88:91]
	v_mfma_f32_16x16x32_bf16 v[80:83], v[176:179], v[200:203], v[80:83]
	v_mfma_f32_16x16x32_bf16 v[72:75], v[168:171], v[208:211], v[72:75]
	v_mfma_f32_16x16x32_bf16 v[64:67], v[176:179], v[208:211], v[64:67]
	s_setprio 0
	s_barrier
	ds_read_b128 v[180:183], v144 offset:16384
	ds_read_b128 v[184:187], v144 offset:17408
	ds_read_b128 v[188:191], v144 offset:18432
	ds_read_b128 v[192:195], v144 offset:19456
	ds_read_b128 v[196:199], v144 offset:20480
	ds_read_b128 v[200:203], v144 offset:21504
	ds_read_b128 v[204:207], v144 offset:22528
	ds_read_b128 v[208:211], v144 offset:23552
	s_mov_b32 s24, m0
	s_mov_b32 m0, s23
	s_nop 0
	global_load_lds_dwordx4 v137, s[40:41]
	s_mov_b32 m0, s24
	s_nop 0
	s_mov_b32 s24, m0
	s_mov_b32 m0, s47
	s_nop 0
	global_load_lds_dwordx4 v139, s[40:41]
	s_mov_b32 m0, s24
	s_add_u32 s24, s40, 0x80000
	s_addc_u32 s25, s41, 0
	s_mov_b32 s72, m0
	s_mov_b32 m0, s48
	s_nop 0
	global_load_lds_dwordx4 v137, s[24:25]
	s_mov_b32 m0, s72
	s_nop 0
	s_mov_b32 s72, m0
	s_mov_b32 m0, s49
	s_nop 0
	global_load_lds_dwordx4 v139, s[24:25]
	s_mov_b32 m0, s72
	s_mov_b32 s24, m0
	s_mov_b32 m0, s44
	s_nop 0
	global_load_lds_dwordx4 v136, s[42:43]
	s_mov_b32 m0, s24
	s_nop 0
	s_mov_b32 s24, m0
	s_mov_b32 m0, s50
	s_nop 0
	global_load_lds_dwordx4 v138, s[42:43]
	s_mov_b32 m0, s24
	s_waitcnt vmcnt(8)
	s_waitcnt lgkmcnt(0)
	s_barrier
; #define PG8_STAGE(bufoff, gbase, voff) do { _Pragma("unroll") for (int _i = 0; _i < 2; ++_i) { unsigned keep_; \
;         asm volatile("s_mov_b32 %0, m0\n\ts_mov_b32 m0, %3\n\ts_nop 0\n\tglobal_load_lds_dwordx4 %1, %2\n\ts_mov_b32 m0, %0" : "=&s"(keep_) : "v"((voff)[_i]), "s"((const char*)(gbase)), "s"(ldsbase + (unsigned)((bufoff) + _i * 8192)) : "memory"); } } while (0)
; #define PG8_WAIT_V(n) asm volatile("s_waitcnt vmcnt(" #n ")" ::: "memory")
; #define PG8_WAIT_L(n) asm volatile("s_waitcnt lgkmcnt(" #n ")" ::: "memory")
; #define PG8_BAR __builtin_amdgcn_s_barrier()
; #define PG8_SCHED __builtin_amdgcn_sched_barrier(0)
; template <class Epi, class Sched, bool ALIGN_EPI, bool FP8 = false>
; DI void gemm_phase(LAS unsigned char* lds, const Gemm g, const Sched& S, const Epi& E) {
;     ...
;             PG8_WAIT_V(8); PG8_WAIT_L(0); PG8_BAR; PG8_MMA(1, 0, At, B0); PG8_MMA(1, 1, At, B1); PG8_BAR; PG8_SCHED;
;             PG8_LDB(B0, 1, 0); PG8_LDB(B1, 1, 1); PG8_SCHED; PG8_LDA(At, 1, 0); PG8_STAGE(PG8_SA(0, 1), a2 + hstepA, voffA);
;             PG8_WAIT_V(8); PG8_WAIT_L(0); PG8_BAR; PG8_MMA(0, 0, At, B0); PG8_MMA(0, 1, At, B1); PG8_BAR; PG8_SCHED;
	s_setprio 1
	v_mfma_f32_16x16x32_bf16 v[60:63], v[148:151], v[180:183], v[60:63]
	v_mfma_f32_16x16x32_bf16 v[52:55], v[156:159], v[180:183], v[52:55]
	v_mfma_f32_16x16x32_bf16 v[44:47], v[148:151], v[188:191], v[44:47]
	v_mfma_f32_16x16x32_bf16 v[36:39], v[156:159], v[188:191], v[36:39]
	v_mfma_f32_16x16x32_bf16 v[28:31], v[148:151], v[196:199], v[28:31]
	v_mfma_f32_16x16x32_bf16 v[20:23], v[156:159], v[196:199], v[20:23]
	v_mfma_f32_16x16x32_bf16 v[12:15], v[148:151], v[204:207], v[12:15]
	v_mfma_f32_16x16x32_bf16 v[4:7], v[156:159], v[204:207], v[4:7]
	v_mfma_f32_16x16x32_bf16 v[60:63], v[152:155], v[184:187], v[60:63]
	v_mfma_f32_16x16x32_bf16 v[52:55], v[160:163], v[184:187], v[52:55]
	v_mfma_f32_16x16x32_bf16 v[44:47], v[152:155], v[192:195], v[44:47]
	v_mfma_f32_16x16x32_bf16 v[36:39], v[160:163], v[192:195], v[36:39]
	v_mfma_f32_16x16x32_bf16 v[28:31], v[152:155], v[200:203], v[28:31]
	v_mfma_f32_16x16x32_bf16 v[20:23], v[160:163], v[200:203], v[20:23]
	v_mfma_f32_16x16x32_bf16 v[12:15], v[152:155], v[208:211], v[12:15]
	v_mfma_f32_16x16x32_bf16 v[4:7], v[160:163], v[208:211], v[4:7]
	v_mfma_f32_16x16x32_bf16 v[56:59], v[164:167], v[180:183], v[56:59]
	v_mfma_f32_16x16x32_bf16 v[48:51], v[172:175], v[180:183], v[48:51]
	v_mfma_f32_16x16x32_bf16 v[40:43], v[164:167], v[188:191], v[40:43]
	v_mfma_f32_16x16x32_bf16 v[32:35], v[172:175], v[188:191], v[32:35]
	v_mfma_f32_16x16x32_bf16 v[24:27], v[164:167], v[196:199], v[24:27]
	v_mfma_f32_16x16x32_bf16 v[16:19], v[172:175], v[196:199], v[16:19]
	v_mfma_f32_16x16x32_bf16 v[8:11], v[164:167], v[204:207], v[8:11]
	v_mfma_f32_16x16x32_bf16 v[0:3], v[172:175], v[204:207], v[0:3]
	v_mfma_f32_16x16x32_bf16 v[56:59], v[168:171], v[184:187], v[56:59]
	v_mfma_f32_16x16x32_bf16 v[48:51], v[176:179], v[184:187], v[48:51]
	v_mfma_f32_16x16x32_bf16 v[40:43], v[168:171], v[192:195], v[40:43]
	v_mfma_f32_16x16x32_bf16 v[32:35], v[176:179], v[192:195], v[32:35]
	v_mfma_f32_16x16x32_bf16 v[24:27], v[168:171], v[200:203], v[24:27]
	v_mfma_f32_16x16x32_bf16 v[16:19], v[176:179], v[200:203], v[16:19]
	v_mfma_f32_16x16x32_bf16 v[8:11], v[168:171], v[208:211], v[8:11]
	v_mfma_f32_16x16x32_bf16 v[0:3], v[176:179], v[208:211], v[0:3]
	s_setprio 0
	s_barrier
	ds_read_b128 v[148:151], v145
	ds_read_b128 v[152:155], v145 offset:1024
	ds_read_b128 v[156:159], v145 offset:2048
	ds_read_b128 v[160:163], v145 offset:3072
	ds_read_b128 v[164:167], v146
	ds_read_b128 v[168:171], v146 offset:1024
	ds_read_b128 v[172:175], v146 offset:2048
	ds_read_b128 v[176:179], v146 offset:3072
	ds_read_b128 v[180:183], v144 offset:32768
	ds_read_b128 v[184:187], v144 offset:33792
	ds_read_b128 v[188:191], v144 offset:34816
	ds_read_b128 v[192:195], v144 offset:35840
	ds_read_b128 v[196:199], v144 offset:36864
	ds_read_b128 v[200:203], v144 offset:37888
	ds_read_b128 v[204:207], v144 offset:38912
	ds_read_b128 v[208:211], v144 offset:39936
	s_add_u32 s24, s42, 0x80000
	s_addc_u32 s25, s43, 0
	s_mov_b32 s42, m0
	s_mov_b32 m0, s51
	s_nop 0
	global_load_lds_dwordx4 v136, s[24:25]
	s_mov_b32 m0, s42
	s_nop 0
	s_mov_b32 s42, m0
	s_mov_b32 m0, s52
	s_nop 0
	global_load_lds_dwordx4 v138, s[24:25]
	s_mov_b32 m0, s42
	s_waitcnt vmcnt(8)
	s_waitcnt lgkmcnt(0)
	s_barrier
	s_setprio 1
	v_mfma_f32_16x16x32_bf16 v[124:127], v[148:151], v[180:183], v[124:127]
	v_mfma_f32_16x16x32_bf16 v[116:119], v[156:159], v[180:183], v[116:119]
	v_mfma_f32_16x16x32_bf16 v[108:111], v[148:151], v[188:191], v[108:111]
	v_mfma_f32_16x16x32_bf16 v[100:103], v[156:159], v[188:191], v[100:103]
	v_mfma_f32_16x16x32_bf16 v[92:95], v[148:151], v[196:199], v[92:95]
	v_mfma_f32_16x16x32_bf16 v[84:87], v[156:159], v[196:199], v[84:87]
	v_mfma_f32_16x16x32_bf16 v[76:79], v[148:151], v[204:207], v[76:79]
	v_mfma_f32_16x16x32_bf16 v[68:71], v[156:159], v[204:207], v[68:71]
	v_mfma_f32_16x16x32_bf16 v[124:127], v[152:155], v[184:187], v[124:127]
	v_mfma_f32_16x16x32_bf16 v[116:119], v[160:163], v[184:187], v[116:119]
	v_mfma_f32_16x16x32_bf16 v[108:111], v[152:155], v[192:195], v[108:111]
	v_mfma_f32_16x16x32_bf16 v[100:103], v[160:163], v[192:195], v[100:103]
	v_mfma_f32_16x16x32_bf16 v[92:95], v[152:155], v[200:203], v[92:95]
	v_mfma_f32_16x16x32_bf16 v[84:87], v[160:163], v[200:203], v[84:87]
	v_mfma_f32_16x16x32_bf16 v[76:79], v[152:155], v[208:211], v[76:79]
	v_mfma_f32_16x16x32_bf16 v[68:71], v[160:163], v[208:211], v[68:71]
	v_mfma_f32_16x16x32_bf16 v[120:123], v[164:167], v[180:183], v[120:123]
	v_mfma_f32_16x16x32_bf16 v[112:115], v[172:175], v[180:183], v[112:115]
	v_mfma_f32_16x16x32_bf16 v[104:107], v[164:167], v[188:191], v[104:107]
	v_mfma_f32_16x16x32_bf16 v[96:99], v[172:175], v[188:191], v[96:99]
	v_mfma_f32_16x16x32_bf16 v[88:91], v[164:167], v[196:199], v[88:91]
	v_mfma_f32_16x16x32_bf16 v[80:83], v[172:175], v[196:199], v[80:83]
	v_mfma_f32_16x16x32_bf16 v[72:75], v[164:167], v[204:207], v[72:75]
	v_mfma_f32_16x16x32_bf16 v[64:67], v[172:175], v[204:207], v[64:67]
	v_mfma_f32_16x16x32_bf16 v[120:123], v[168:171], v[184:187], v[120:123]
	v_mfma_f32_16x16x32_bf16 v[112:115], v[176:179], v[184:187], v[112:115]
	v_mfma_f32_16x16x32_bf16 v[104:107], v[168:171], v[192:195], v[104:107]
	v_mfma_f32_16x16x32_bf16 v[96:99], v[176:179], v[192:195], v[96:99]
	v_mfma_f32_16x16x32_bf16 v[88:91], v[168:171], v[200:203], v[88:91]
	v_mfma_f32_16x16x32_bf16 v[80:83], v[176:179], v[200:203], v[80:83]
	v_mfma_f32_16x16x32_bf16 v[72:75], v[168:171], v[208:211], v[72:75]
	v_mfma_f32_16x16x32_bf16 v[64:67], v[176:179], v[208:211], v[64:67]
	s_setprio 0
	s_barrier
; #define PG8_STAGE(bufoff, gbase, voff) do { _Pragma("unroll") for (int _i = 0; _i < 2; ++_i) { unsigned keep_; \
;         asm volatile("s_mov_b32 %0, m0\n\ts_mov_b32 m0, %3\n\ts_nop 0\n\tglobal_load_lds_dwordx4 %1, %2\n\ts_mov_b32 m0, %0" : "=&s"(keep_) : "v"((voff)[_i]), "s"((const char*)(gbase)), "s"(ldsbase + (unsigned)((bufoff) + _i * 8192)) : "memory"); } } while (0)
; #define PG8_WAIT_V(n) asm volatile("s_waitcnt vmcnt(" #n ")" ::: "memory")
; #define PG8_WAIT_L(n) asm volatile("s_waitcnt lgkmcnt(" #n ")" ::: "memory")
; #define PG8_BAR __builtin_amdgcn_s_barrier()
; #define PG8_SCHED __builtin_amdgcn_sched_barrier(0)
; template <class Epi, class Sched, bool ALIGN_EPI, bool FP8 = false>
; DI void gemm_phase(LAS unsigned char* lds, const Gemm g, const Sched& S, const Epi& E) {
;     ...
;             PG8_LDA(At, 1, 1); PG8_STAGE(PG8_SB(1, 0), b3, voffB); PG8_STAGE(PG8_SB(1, 1), b3 + hstepB, voffB); PG8_STAGE(PG8_SA(1, 0), a3, voffA);
;             PG8_WAIT_V(8); PG8_WAIT_L(0); PG8_BAR; PG8_MMA(1, 0, At, B0); PG8_MMA(1, 1, At, B1); PG8_BAR; PG8_SCHED;
;         }
;         if constexpr (ALIGN_EPI) { if (wr == 0) PG8_BAR; }
;         E(acc, cur, wr, wc, fr, fq);
;         if (!has_next) break;
	ds_read_b128 v[180:183], v144 offset:49152
	ds_read_b128 v[184:187], v144 offset:50176
	ds_read_b128 v[188:191], v144 offset:51200
	ds_read_b128 v[192:195], v144 offset:52224
	ds_read_b128 v[196:199], v144 offset:53248
	ds_read_b128 v[200:203], v144 offset:54272
	ds_read_b128 v[204:207], v144 offset:55296
	ds_read_b128 v[208:211], v144 offset:56320
	s_add_u32 s24, s40, 0x80
	s_addc_u32 s25, s41, 0
	s_mov_b32 s42, m0
	s_mov_b32 m0, s55
	s_nop 0
	global_load_lds_dwordx4 v137, s[24:25]
	s_mov_b32 m0, s42
	s_nop 0
	s_mov_b32 s42, m0
	s_mov_b32 m0, s56
	s_nop 0
	global_load_lds_dwordx4 v139, s[24:25]
	s_mov_b32 m0, s42
	s_add_u32 s24, s40, 0x80080
	s_addc_u32 s25, s41, 0
	s_mov_b32 s40, m0
	s_mov_b32 m0, s59
	s_nop 0
	global_load_lds_dwordx4 v137, s[24:25]
	s_mov_b32 m0, s40
	s_nop 0
	s_mov_b32 s40, m0
	s_mov_b32 m0, s60
	s_nop 0
	global_load_lds_dwordx4 v139, s[24:25]
	s_mov_b32 m0, s40
	s_mov_b32 s24, m0
	s_mov_b32 m0, s57
	s_nop 0
	global_load_lds_dwordx4 v136, s[28:29]
	s_mov_b32 m0, s24
	s_nop 0
	s_mov_b32 s24, m0
	s_mov_b32 m0, s58
	s_nop 0
	global_load_lds_dwordx4 v138, s[28:29]
	s_mov_b32 m0, s24
	s_waitcnt vmcnt(8)
	s_waitcnt lgkmcnt(0)
	s_barrier
	s_setprio 1
	v_mfma_f32_16x16x32_bf16 v[60:63], v[148:151], v[180:183], v[60:63]
	v_mfma_f32_16x16x32_bf16 v[52:55], v[156:159], v[180:183], v[52:55]
	v_mfma_f32_16x16x32_bf16 v[44:47], v[148:151], v[188:191], v[44:47]
	v_mfma_f32_16x16x32_bf16 v[36:39], v[156:159], v[188:191], v[36:39]
	v_mfma_f32_16x16x32_bf16 v[28:31], v[148:151], v[196:199], v[28:31]
	v_mfma_f32_16x16x32_bf16 v[20:23], v[156:159], v[196:199], v[20:23]
	v_mfma_f32_16x16x32_bf16 v[12:15], v[148:151], v[204:207], v[12:15]
	v_mfma_f32_16x16x32_bf16 v[4:7], v[156:159], v[204:207], v[4:7]
	v_mfma_f32_16x16x32_bf16 v[60:63], v[152:155], v[184:187], v[60:63]
	v_mfma_f32_16x16x32_bf16 v[52:55], v[160:163], v[184:187], v[52:55]
	v_mfma_f32_16x16x32_bf16 v[44:47], v[152:155], v[192:195], v[44:47]
	v_mfma_f32_16x16x32_bf16 v[36:39], v[160:163], v[192:195], v[36:39]
	v_mfma_f32_16x16x32_bf16 v[28:31], v[152:155], v[200:203], v[28:31]
	v_mfma_f32_16x16x32_bf16 v[20:23], v[160:163], v[200:203], v[20:23]
	v_mfma_f32_16x16x32_bf16 v[12:15], v[152:155], v[208:211], v[12:15]
	v_mfma_f32_16x16x32_bf16 v[4:7], v[160:163], v[208:211], v[4:7]
	v_mfma_f32_16x16x32_bf16 v[56:59], v[164:167], v[180:183], v[56:59]
	v_mfma_f32_16x16x32_bf16 v[48:51], v[172:175], v[180:183], v[48:51]
	v_mfma_f32_16x16x32_bf16 v[40:43], v[164:167], v[188:191], v[40:43]
	v_mfma_f32_16x16x32_bf16 v[32:35], v[172:175], v[188:191], v[32:35]
	v_mfma_f32_16x16x32_bf16 v[24:27], v[164:167], v[196:199], v[24:27]
	v_mfma_f32_16x16x32_bf16 v[16:19], v[172:175], v[196:199], v[16:19]
	v_mfma_f32_16x16x32_bf16 v[8:11], v[164:167], v[204:207], v[8:11]
	v_mfma_f32_16x16x32_bf16 v[0:3], v[172:175], v[204:207], v[0:3]
	v_mfma_f32_16x16x32_bf16 v[56:59], v[168:171], v[184:187], v[56:59]
	v_mfma_f32_16x16x32_bf16 v[48:51], v[176:179], v[184:187], v[48:51]
	v_mfma_f32_16x16x32_bf16 v[40:43], v[168:171], v[192:195], v[40:43]
	v_mfma_f32_16x16x32_bf16 v[32:35], v[176:179], v[192:195], v[32:35]
	v_mfma_f32_16x16x32_bf16 v[24:27], v[168:171], v[200:203], v[24:27]
	v_mfma_f32_16x16x32_bf16 v[16:19], v[176:179], v[200:203], v[16:19]
	v_mfma_f32_16x16x32_bf16 v[8:11], v[168:171], v[208:211], v[8:11]
	v_mfma_f32_16x16x32_bf16 v[0:3], v[176:179], v[208:211], v[0:3]
	s_setprio 0
	s_barrier
	s_add_i32 s71, s71, 2
	s_add_u32 s69, s69, 0x100
	s_addc_u32 s70, s70, 0
	s_cmp_gt_u32 s71, 29
	s_mov_b64 s[24:25], s[26:27]
	s_cbranch_scc0 .LBB0_700
	s_and_b64 vcc, exec, s[10:11]
	s_cbranch_vccz .LBB0_703
	s_barrier

; #define PG8_STAGE(bufoff, gbase, voff) do { _Pragma("unroll") for (int _i = 0; _i < 2; ++_i) { unsigned keep_; \
;         asm volatile("s_mov_b32 %0, m0\n\ts_mov_b32 m0, %3\n\ts_nop 0\n\tglobal_load_lds_dwordx4 %1, %2\n\ts_mov_b32 m0, %0" : "=&s"(keep_) : "v"((voff)[_i]), "s"((const char*)(gbase)), "s"(ldsbase + (unsigned)((bufoff) + _i * 8192)) : "memory"); } } while (0)
; #define PG8_WAIT_V(n) asm volatile("s_waitcnt vmcnt(" #n ")" ::: "memory")
; #define PG8_WAIT_L(n) asm volatile("s_waitcnt lgkmcnt(" #n ")" ::: "memory")
; #define PG8_BAR __builtin_amdgcn_s_barrier()
; #define PG8_SCHED __builtin_amdgcn_sched_barrier(0)
; template <class Epi, class Sched, bool ALIGN_EPI, bool FP8 = false>
; DI void gemm_phase(LAS unsigned char* lds, const Gemm g, const Sched& S, const Epi& E) {
;     ...
;             PG8_LDB(B0, 0, 0); PG8_LDB(B1, 0, 1); PG8_SCHED; PG8_LDA(At, 0, 0); PG8_STAGE(PG8_SA(1, 1), a1 + hstepA, voffA);
;             PG8_WAIT_V(8); PG8_WAIT_L(0); PG8_BAR; PG8_MMA(0, 0, At, B0); PG8_MMA(0, 1, At, B1); PG8_BAR; PG8_SCHED;
;             PG8_LDA(At, 0, 1); PG8_STAGE(PG8_SB(0, 0), b2, voffB); PG8_STAGE(PG8_SB(0, 1), b2 + hstepB, voffB); PG8_STAGE(PG8_SA(0, 0), a2, voffA);
;             PG8_WAIT_V(8); PG8_WAIT_L(0); PG8_BAR; PG8_MMA(1, 0, At, B0); PG8_MMA(1, 1, At, B1); PG8_BAR; PG8_SCHED;
.LBB0_724:
	ds_read_b128 v[146:149], v140
	ds_read_b128 v[150:153], v140 offset:1024
	ds_read_b128 v[154:157], v140 offset:2048
	ds_read_b128 v[158:161], v140 offset:3072
	ds_read_b128 v[162:165], v141
	ds_read_b128 v[166:169], v141 offset:1024
	ds_read_b128 v[170:173], v141 offset:2048
	ds_read_b128 v[174:177], v141 offset:3072
	s_add_u32 s66, s64, 0x100
	s_addc_u32 s67, s65, 0
	s_cmp_eq_u32 vcc_lo, 28
	s_cselect_b32 s72, s94, s66
	s_cselect_b32 s73, s57, s67
	s_cselect_b32 s70, s95, s96
	s_cselect_b32 s71, s55, s97
	s_add_u32 s68, s72, 0x80
	s_addc_u32 s69, s73, 0
	ds_read_b128 v[178:181], v142
	ds_read_b128 v[182:185], v142 offset:1024
	ds_read_b128 v[186:189], v142 offset:2048
	ds_read_b128 v[190:193], v142 offset:3072
	ds_read_b128 v[194:197], v142 offset:4096
	ds_read_b128 v[198:201], v142 offset:5120
	ds_read_b128 v[202:205], v142 offset:6144
	ds_read_b128 v[206:209], v142 offset:7168
	s_add_u32 s64, s64, 0x80080
	s_addc_u32 s65, s65, 0
	s_mov_b32 vcc_hi, m0
	s_mov_b32 m0, s90
	s_nop 0
	global_load_lds_dwordx4 v134, s[64:65]
	s_mov_b32 m0, vcc_hi
	s_nop 0
	s_mov_b32 vcc_hi, m0
	s_mov_b32 m0, s91
	s_nop 0
	global_load_lds_dwordx4 v136, s[64:65]
	s_mov_b32 m0, vcc_hi
	s_waitcnt vmcnt(8)
	s_waitcnt lgkmcnt(0)
	s_barrier
	s_setprio 1
	v_mfma_f32_16x16x32_bf16 v[124:127], v[146:149], v[178:181], v[124:127]
	v_mfma_f32_16x16x32_bf16 v[120:123], v[154:157], v[178:181], v[120:123]
	v_mfma_f32_16x16x32_bf16 v[108:111], v[146:149], v[186:189], v[108:111]
	v_mfma_f32_16x16x32_bf16 v[104:107], v[154:157], v[186:189], v[104:107]
	v_mfma_f32_16x16x32_bf16 v[92:95], v[146:149], v[194:197], v[92:95]
	v_mfma_f32_16x16x32_bf16 v[88:91], v[154:157], v[194:197], v[88:91]
	v_mfma_f32_16x16x32_bf16 v[76:79], v[146:149], v[202:205], v[76:79]
	v_mfma_f32_16x16x32_bf16 v[72:75], v[154:157], v[202:205], v[72:75]
	v_mfma_f32_16x16x32_bf16 v[124:127], v[150:153], v[182:185], v[124:127]
	v_mfma_f32_16x16x32_bf16 v[120:123], v[158:161], v[182:185], v[120:123]
	v_mfma_f32_16x16x32_bf16 v[108:111], v[150:153], v[190:193], v[108:111]
	v_mfma_f32_16x16x32_bf16 v[104:107], v[158:161], v[190:193], v[104:107]
	v_mfma_f32_16x16x32_bf16 v[92:95], v[150:153], v[198:201], v[92:95]
	v_mfma_f32_16x16x32_bf16 v[88:91], v[158:161], v[198:201], v[88:91]
	v_mfma_f32_16x16x32_bf16 v[76:79], v[150:153], v[206:209], v[76:79]
	v_mfma_f32_16x16x32_bf16 v[72:75], v[158:161], v[206:209], v[72:75]
	v_mfma_f32_16x16x32_bf16 v[116:119], v[162:165], v[178:181], v[116:119]
	v_mfma_f32_16x16x32_bf16 v[112:115], v[170:173], v[178:181], v[112:115]
	v_mfma_f32_16x16x32_bf16 v[100:103], v[162:165], v[186:189], v[100:103]
	v_mfma_f32_16x16x32_bf16 v[96:99], v[170:173], v[186:189], v[96:99]
	v_mfma_f32_16x16x32_bf16 v[84:87], v[162:165], v[194:197], v[84:87]
	v_mfma_f32_16x16x32_bf16 v[80:83], v[170:173], v[194:197], v[80:83]
	v_mfma_f32_16x16x32_bf16 v[68:71], v[162:165], v[202:205], v[68:71]
	v_mfma_f32_16x16x32_bf16 v[64:67], v[170:173], v[202:205], v[64:67]
	v_mfma_f32_16x16x32_bf16 v[116:119], v[166:169], v[182:185], v[116:119]
	v_mfma_f32_16x16x32_bf16 v[112:115], v[174:177], v[182:185], v[112:115]
	v_mfma_f32_16x16x32_bf16 v[100:103], v[166:169], v[190:193], v[100:103]
	v_mfma_f32_16x16x32_bf16 v[96:99], v[174:177], v[190:193], v[96:99]
	v_mfma_f32_16x16x32_bf16 v[84:87], v[166:169], v[198:201], v[84:87]
	v_mfma_f32_16x16x32_bf16 v[80:83], v[174:177], v[198:201], v[80:83]
	v_mfma_f32_16x16x32_bf16 v[68:71], v[166:169], v[206:209], v[68:71]
	v_mfma_f32_16x16x32_bf16 v[64:67], v[174:177], v[206:209], v[64:67]
	s_setprio 0
	s_barrier
	ds_read_b128 v[178:181], v142 offset:16384
	ds_read_b128 v[182:185], v142 offset:17408
	ds_read_b128 v[186:189], v142 offset:18432
	ds_read_b128 v[190:193], v142 offset:19456
	ds_read_b128 v[194:197], v142 offset:20480
	ds_read_b128 v[198:201], v142 offset:21504
	ds_read_b128 v[202:205], v142 offset:22528
	ds_read_b128 v[206:209], v142 offset:23552
	s_mov_b32 s64, m0
	s_mov_b32 m0, s63
	s_nop 0
	global_load_lds_dwordx4 v135, s[70:71]
	s_mov_b32 m0, s64
	s_nop 0
	s_mov_b32 s64, m0
	s_mov_b32 m0, s77
	s_nop 0
	global_load_lds_dwordx4 v137, s[70:71]
	s_mov_b32 m0, s64
	s_add_u32 s64, s70, 0x80000
	s_addc_u32 s65, s71, 0
	s_mov_b32 vcc_hi, m0
	s_mov_b32 m0, s79
	s_nop 0
	global_load_lds_dwordx4 v135, s[64:65]
	s_mov_b32 m0, vcc_hi
	s_nop 0
	s_mov_b32 vcc_hi, m0
	s_mov_b32 m0, s80
	s_nop 0
	global_load_lds_dwordx4 v137, s[64:65]
	s_mov_b32 m0, vcc_hi
	s_mov_b32 s64, m0
	s_mov_b32 m0, s75
	s_nop 0
	global_load_lds_dwordx4 v134, s[72:73]
	s_mov_b32 m0, s64
	s_nop 0
	s_mov_b32 s64, m0
	s_mov_b32 m0, s81
	s_nop 0
	global_load_lds_dwordx4 v136, s[72:73]
	s_mov_b32 m0, s64
	s_waitcnt vmcnt(8)
	s_waitcnt lgkmcnt(0)
	s_barrier
; #define PG8_STAGE(bufoff, gbase, voff) do { _Pragma("unroll") for (int _i = 0; _i < 2; ++_i) { unsigned keep_; \
;         asm volatile("s_mov_b32 %0, m0\n\ts_mov_b32 m0, %3\n\ts_nop 0\n\tglobal_load_lds_dwordx4 %1, %2\n\ts_mov_b32 m0, %0" : "=&s"(keep_) : "v"((voff)[_i]), "s"((const char*)(gbase)), "s"(ldsbase + (unsigned)((bufoff) + _i * 8192)) : "memory"); } } while (0)
; #define PG8_WAIT_V(n) asm volatile("s_waitcnt vmcnt(" #n ")" ::: "memory")
; #define PG8_WAIT_L(n) asm volatile("s_waitcnt lgkmcnt(" #n ")" ::: "memory")
; #define PG8_BAR __builtin_amdgcn_s_barrier()
; #define PG8_SCHED __builtin_amdgcn_sched_barrier(0)
; template <class Epi, class Sched, bool ALIGN_EPI, bool FP8 = false>
; DI void gemm_phase(LAS unsigned char* lds, const Gemm g, const Sched& S, const Epi& E) {
;     ...
;             PG8_WAIT_V(8); PG8_WAIT_L(0); PG8_BAR; PG8_MMA(1, 0, At, B0); PG8_MMA(1, 1, At, B1); PG8_BAR; PG8_SCHED;
;             PG8_LDB(B0, 1, 0); PG8_LDB(B1, 1, 1); PG8_SCHED; PG8_LDA(At, 1, 0); PG8_STAGE(PG8_SA(0, 1), a2 + hstepA, voffA);
;             PG8_WAIT_V(8); PG8_WAIT_L(0); PG8_BAR; PG8_MMA(0, 0, At, B0); PG8_MMA(0, 1, At, B1); PG8_BAR; PG8_SCHED;
	s_setprio 1
	v_mfma_f32_16x16x32_bf16 v[60:63], v[146:149], v[178:181], v[60:63]
	v_mfma_f32_16x16x32_bf16 v[56:59], v[154:157], v[178:181], v[56:59]
	v_mfma_f32_16x16x32_bf16 v[44:47], v[146:149], v[186:189], v[44:47]
	v_mfma_f32_16x16x32_bf16 v[40:43], v[154:157], v[186:189], v[40:43]
	v_mfma_f32_16x16x32_bf16 v[28:31], v[146:149], v[194:197], v[28:31]
	v_mfma_f32_16x16x32_bf16 v[24:27], v[154:157], v[194:197], v[24:27]
	v_mfma_f32_16x16x32_bf16 v[12:15], v[146:149], v[202:205], v[12:15]
	v_mfma_f32_16x16x32_bf16 v[8:11], v[154:157], v[202:205], v[8:11]
	v_mfma_f32_16x16x32_bf16 v[60:63], v[150:153], v[182:185], v[60:63]
	v_mfma_f32_16x16x32_bf16 v[56:59], v[158:161], v[182:185], v[56:59]
	v_mfma_f32_16x16x32_bf16 v[44:47], v[150:153], v[190:193], v[44:47]
	v_mfma_f32_16x16x32_bf16 v[40:43], v[158:161], v[190:193], v[40:43]
	v_mfma_f32_16x16x32_bf16 v[28:31], v[150:153], v[198:201], v[28:31]
	v_mfma_f32_16x16x32_bf16 v[24:27], v[158:161], v[198:201], v[24:27]
	v_mfma_f32_16x16x32_bf16 v[12:15], v[150:153], v[206:209], v[12:15]
	v_mfma_f32_16x16x32_bf16 v[8:11], v[158:161], v[206:209], v[8:11]
	v_mfma_f32_16x16x32_bf16 v[52:55], v[162:165], v[178:181], v[52:55]
	v_mfma_f32_16x16x32_bf16 v[48:51], v[170:173], v[178:181], v[48:51]
	v_mfma_f32_16x16x32_bf16 v[36:39], v[162:165], v[186:189], v[36:39]
	v_mfma_f32_16x16x32_bf16 v[32:35], v[170:173], v[186:189], v[32:35]
	v_mfma_f32_16x16x32_bf16 v[20:23], v[162:165], v[194:197], v[20:23]
	v_mfma_f32_16x16x32_bf16 v[16:19], v[170:173], v[194:197], v[16:19]
	v_mfma_f32_16x16x32_bf16 v[4:7], v[162:165], v[202:205], v[4:7]
	v_mfma_f32_16x16x32_bf16 v[0:3], v[170:173], v[202:205], v[0:3]
	v_mfma_f32_16x16x32_bf16 v[52:55], v[166:169], v[182:185], v[52:55]
	v_mfma_f32_16x16x32_bf16 v[48:51], v[174:177], v[182:185], v[48:51]
	v_mfma_f32_16x16x32_bf16 v[36:39], v[166:169], v[190:193], v[36:39]
	v_mfma_f32_16x16x32_bf16 v[32:35], v[174:177], v[190:193], v[32:35]
	v_mfma_f32_16x16x32_bf16 v[20:23], v[166:169], v[198:201], v[20:23]
	v_mfma_f32_16x16x32_bf16 v[16:19], v[174:177], v[198:201], v[16:19]
	v_mfma_f32_16x16x32_bf16 v[4:7], v[166:169], v[206:209], v[4:7]
	v_mfma_f32_16x16x32_bf16 v[0:3], v[174:177], v[206:209], v[0:3]
	s_setprio 0
	s_barrier
	ds_read_b128 v[146:149], v143
	ds_read_b128 v[150:153], v143 offset:1024
	ds_read_b128 v[154:157], v143 offset:2048
	ds_read_b128 v[158:161], v143 offset:3072
	ds_read_b128 v[162:165], v144
	ds_read_b128 v[166:169], v144 offset:1024
	ds_read_b128 v[170:173], v144 offset:2048
	ds_read_b128 v[174:177], v144 offset:3072
	ds_read_b128 v[178:181], v142 offset:32768
	ds_read_b128 v[182:185], v142 offset:33792
	ds_read_b128 v[186:189], v142 offset:34816
	ds_read_b128 v[190:193], v142 offset:35840
	ds_read_b128 v[194:197], v142 offset:36864
	ds_read_b128 v[198:201], v142 offset:37888
	ds_read_b128 v[202:205], v142 offset:38912
	ds_read_b128 v[206:209], v142 offset:39936
	s_add_u32 s64, s72, 0x80000
	s_addc_u32 s65, s73, 0
	s_mov_b32 s72, m0
	s_mov_b32 m0, s82
	s_nop 0
	global_load_lds_dwordx4 v134, s[64:65]
	s_mov_b32 m0, s72
	s_nop 0
	s_mov_b32 s72, m0
	s_mov_b32 m0, s83
	s_nop 0
	global_load_lds_dwordx4 v136, s[64:65]
	s_mov_b32 m0, s72
	s_waitcnt vmcnt(8)
	s_waitcnt lgkmcnt(0)
	s_barrier
	s_setprio 1
	v_mfma_f32_16x16x32_bf16 v[124:127], v[146:149], v[178:181], v[124:127]
	v_mfma_f32_16x16x32_bf16 v[120:123], v[154:157], v[178:181], v[120:123]
	v_mfma_f32_16x16x32_bf16 v[108:111], v[146:149], v[186:189], v[108:111]
	v_mfma_f32_16x16x32_bf16 v[104:107], v[154:157], v[186:189], v[104:107]
	v_mfma_f32_16x16x32_bf16 v[92:95], v[146:149], v[194:197], v[92:95]
	v_mfma_f32_16x16x32_bf16 v[88:91], v[154:157], v[194:197], v[88:91]
	v_mfma_f32_16x16x32_bf16 v[76:79], v[146:149], v[202:205], v[76:79]
	v_mfma_f32_16x16x32_bf16 v[72:75], v[154:157], v[202:205], v[72:75]
	v_mfma_f32_16x16x32_bf16 v[124:127], v[150:153], v[182:185], v[124:127]
	v_mfma_f32_16x16x32_bf16 v[120:123], v[158:161], v[182:185], v[120:123]
	v_mfma_f32_16x16x32_bf16 v[108:111], v[150:153], v[190:193], v[108:111]
	v_mfma_f32_16x16x32_bf16 v[104:107], v[158:161], v[190:193], v[104:107]
	v_mfma_f32_16x16x32_bf16 v[92:95], v[150:153], v[198:201], v[92:95]
	v_mfma_f32_16x16x32_bf16 v[88:91], v[158:161], v[198:201], v[88:91]
	v_mfma_f32_16x16x32_bf16 v[76:79], v[150:153], v[206:209], v[76:79]
	v_mfma_f32_16x16x32_bf16 v[72:75], v[158:161], v[206:209], v[72:75]
	v_mfma_f32_16x16x32_bf16 v[116:119], v[162:165], v[178:181], v[116:119]
	v_mfma_f32_16x16x32_bf16 v[112:115], v[170:173], v[178:181], v[112:115]
	v_mfma_f32_16x16x32_bf16 v[100:103], v[162:165], v[186:189], v[100:103]
	v_mfma_f32_16x16x32_bf16 v[96:99], v[170:173], v[186:189], v[96:99]
	v_mfma_f32_16x16x32_bf16 v[84:87], v[162:165], v[194:197], v[84:87]
	v_mfma_f32_16x16x32_bf16 v[80:83], v[170:173], v[194:197], v[80:83]
	v_mfma_f32_16x16x32_bf16 v[68:71], v[162:165], v[202:205], v[68:71]
	v_mfma_f32_16x16x32_bf16 v[64:67], v[170:173], v[202:205], v[64:67]
	v_mfma_f32_16x16x32_bf16 v[116:119], v[166:169], v[182:185], v[116:119]
	v_mfma_f32_16x16x32_bf16 v[112:115], v[174:177], v[182:185], v[112:115]
	v_mfma_f32_16x16x32_bf16 v[100:103], v[166:169], v[190:193], v[100:103]
	v_mfma_f32_16x16x32_bf16 v[96:99], v[174:177], v[190:193], v[96:99]
	v_mfma_f32_16x16x32_bf16 v[84:87], v[166:169], v[198:201], v[84:87]
	v_mfma_f32_16x16x32_bf16 v[80:83], v[174:177], v[198:201], v[80:83]
	v_mfma_f32_16x16x32_bf16 v[68:71], v[166:169], v[206:209], v[68:71]
	v_mfma_f32_16x16x32_bf16 v[64:67], v[174:177], v[206:209], v[64:67]
	s_setprio 0
	s_barrier
; #define PG8_STAGE(bufoff, gbase, voff) do { _Pragma("unroll") for (int _i = 0; _i < 2; ++_i) { unsigned keep_; \
;         asm volatile("s_mov_b32 %0, m0\n\ts_mov_b32 m0, %3\n\ts_nop 0\n\tglobal_load_lds_dwordx4 %1, %2\n\ts_mov_b32 m0, %0" : "=&s"(keep_) : "v"((voff)[_i]), "s"((const char*)(gbase)), "s"(ldsbase + (unsigned)((bufoff) + _i * 8192)) : "memory"); } } while (0)
; #define PG8_WAIT_V(n) asm volatile("s_waitcnt vmcnt(" #n ")" ::: "memory")
; #define PG8_WAIT_L(n) asm volatile("s_waitcnt lgkmcnt(" #n ")" ::: "memory")
; #define PG8_BAR __builtin_amdgcn_s_barrier()
; #define PG8_SCHED __builtin_amdgcn_sched_barrier(0)
; template <class Epi, class Sched, bool ALIGN_EPI, bool FP8 = false>
; DI void gemm_phase(LAS unsigned char* lds, const Gemm g, const Sched& S, const Epi& E) {
;     ...
;             PG8_LDA(At, 1, 1); PG8_STAGE(PG8_SB(1, 0), b3, voffB); PG8_STAGE(PG8_SB(1, 1), b3 + hstepB, voffB); PG8_STAGE(PG8_SA(1, 0), a3, voffA);
;             PG8_WAIT_V(8); PG8_WAIT_L(0); PG8_BAR; PG8_MMA(1, 0, At, B0); PG8_MMA(1, 1, At, B1); PG8_BAR; PG8_SCHED;
;         }
;         if constexpr (ALIGN_EPI) { if (wr == 0) PG8_BAR; }
;         E(acc, cur, wr, wc, fr, fq);
;         if (!has_next) break;
	ds_read_b128 v[178:181], v142 offset:49152
	ds_read_b128 v[182:185], v142 offset:50176
	ds_read_b128 v[186:189], v142 offset:51200
	ds_read_b128 v[190:193], v142 offset:52224
	ds_read_b128 v[194:197], v142 offset:53248
	ds_read_b128 v[198:201], v142 offset:54272
	ds_read_b128 v[202:205], v142 offset:55296
	ds_read_b128 v[206:209], v142 offset:56320
	s_add_u32 s64, s70, 0x80
	s_addc_u32 s65, s71, 0
	s_mov_b32 s72, m0
	s_mov_b32 m0, s84
	s_nop 0
	global_load_lds_dwordx4 v135, s[64:65]
	s_mov_b32 m0, s72
	s_nop 0
	s_mov_b32 s72, m0
	s_mov_b32 m0, s85
	s_nop 0
	global_load_lds_dwordx4 v137, s[64:65]
	s_mov_b32 m0, s72
	s_add_u32 s64, s70, 0x80080
	s_addc_u32 s65, s71, 0
	s_mov_b32 s70, m0
	s_mov_b32 m0, s88
	s_nop 0
	global_load_lds_dwordx4 v135, s[64:65]
	s_mov_b32 m0, s70
	s_nop 0
	s_mov_b32 s70, m0
	s_mov_b32 m0, s89
	s_nop 0
	global_load_lds_dwordx4 v137, s[64:65]
	s_mov_b32 m0, s70
	s_mov_b32 s64, m0
	s_mov_b32 m0, s86
	s_nop 0
	global_load_lds_dwordx4 v134, s[68:69]
	s_mov_b32 m0, s64
	s_nop 0
	s_mov_b32 s64, m0
	s_mov_b32 m0, s87
	s_nop 0
	global_load_lds_dwordx4 v136, s[68:69]
	s_mov_b32 m0, s64
	s_waitcnt vmcnt(8)
	s_waitcnt lgkmcnt(0)
	s_barrier
	s_setprio 1
	v_mfma_f32_16x16x32_bf16 v[60:63], v[146:149], v[178:181], v[60:63]
	v_mfma_f32_16x16x32_bf16 v[56:59], v[154:157], v[178:181], v[56:59]
	v_mfma_f32_16x16x32_bf16 v[44:47], v[146:149], v[186:189], v[44:47]
	v_mfma_f32_16x16x32_bf16 v[40:43], v[154:157], v[186:189], v[40:43]
	v_mfma_f32_16x16x32_bf16 v[28:31], v[146:149], v[194:197], v[28:31]
	v_mfma_f32_16x16x32_bf16 v[24:27], v[154:157], v[194:197], v[24:27]
	v_mfma_f32_16x16x32_bf16 v[12:15], v[146:149], v[202:205], v[12:15]
	v_mfma_f32_16x16x32_bf16 v[8:11], v[154:157], v[202:205], v[8:11]
	v_mfma_f32_16x16x32_bf16 v[60:63], v[150:153], v[182:185], v[60:63]
	v_mfma_f32_16x16x32_bf16 v[56:59], v[158:161], v[182:185], v[56:59]
	v_mfma_f32_16x16x32_bf16 v[44:47], v[150:153], v[190:193], v[44:47]
	v_mfma_f32_16x16x32_bf16 v[40:43], v[158:161], v[190:193], v[40:43]
	v_mfma_f32_16x16x32_bf16 v[28:31], v[150:153], v[198:201], v[28:31]
	v_mfma_f32_16x16x32_bf16 v[24:27], v[158:161], v[198:201], v[24:27]
	v_mfma_f32_16x16x32_bf16 v[12:15], v[150:153], v[206:209], v[12:15]
	v_mfma_f32_16x16x32_bf16 v[8:11], v[158:161], v[206:209], v[8:11]
	v_mfma_f32_16x16x32_bf16 v[52:55], v[162:165], v[178:181], v[52:55]
	v_mfma_f32_16x16x32_bf16 v[48:51], v[170:173], v[178:181], v[48:51]
	v_mfma_f32_16x16x32_bf16 v[36:39], v[162:165], v[186:189], v[36:39]
	v_mfma_f32_16x16x32_bf16 v[32:35], v[170:173], v[186:189], v[32:35]
	v_mfma_f32_16x16x32_bf16 v[20:23], v[162:165], v[194:197], v[20:23]
	v_mfma_f32_16x16x32_bf16 v[16:19], v[170:173], v[194:197], v[16:19]
	v_mfma_f32_16x16x32_bf16 v[4:7], v[162:165], v[202:205], v[4:7]
	v_mfma_f32_16x16x32_bf16 v[0:3], v[170:173], v[202:205], v[0:3]
	v_mfma_f32_16x16x32_bf16 v[52:55], v[166:169], v[182:185], v[52:55]
	v_mfma_f32_16x16x32_bf16 v[48:51], v[174:177], v[182:185], v[48:51]
	v_mfma_f32_16x16x32_bf16 v[36:39], v[166:169], v[190:193], v[36:39]
	v_mfma_f32_16x16x32_bf16 v[32:35], v[174:177], v[190:193], v[32:35]
	v_mfma_f32_16x16x32_bf16 v[20:23], v[166:169], v[198:201], v[20:23]
	v_mfma_f32_16x16x32_bf16 v[16:19], v[174:177], v[198:201], v[16:19]
	v_mfma_f32_16x16x32_bf16 v[4:7], v[166:169], v[206:209], v[4:7]
	v_mfma_f32_16x16x32_bf16 v[0:3], v[174:177], v[206:209], v[0:3]
	s_setprio 0
	s_barrier
	s_add_i32 vcc_lo, vcc_lo, 2
	s_add_u32 s96, s96, 0x100
	s_addc_u32 s97, s97, 0
	s_cmp_gt_u32 vcc_lo, 29
	s_mov_b64 s[64:65], s[66:67]
	s_cbranch_scc0 .LBB0_724
	s_and_b64 vcc, exec, s[16:17]
	s_cbranch_vccz .LBB0_727
	s_barrier

; #define PG8_STAGE(bufoff, gbase, voff) do { _Pragma("unroll") for (int _i = 0; _i < 2; ++_i) { unsigned keep_; \
;         asm volatile("s_mov_b32 %0, m0\n\ts_mov_b32 m0, %3\n\ts_nop 0\n\tglobal_load_lds_dwordx4 %1, %2\n\ts_mov_b32 m0, %0" : "=&s"(keep_) : "v"((voff)[_i]), "s"((const char*)(gbase)), "s"(ldsbase + (unsigned)((bufoff) + _i * 8192)) : "memory"); } } while (0)
; #define PG8_WAIT_V(n) asm volatile("s_waitcnt vmcnt(" #n ")" ::: "memory")
; #define PG8_WAIT_L(n) asm volatile("s_waitcnt lgkmcnt(" #n ")" ::: "memory")
; #define PG8_BAR __builtin_amdgcn_s_barrier()
; #define PG8_SCHED __builtin_amdgcn_sched_barrier(0)
; template <class Epi, class Sched, bool ALIGN_EPI, bool FP8 = false>
; DI void gemm_phase(LAS unsigned char* lds, const Gemm g, const Sched& S, const Epi& E) {
;     ...
;             PG8_LDB(B0, 0, 0); PG8_LDB(B1, 0, 1); PG8_SCHED; PG8_LDA(At, 0, 0); PG8_STAGE(PG8_SA(1, 1), a1 + hstepA, voffA);
;             PG8_WAIT_V(8); PG8_WAIT_L(0); PG8_BAR; PG8_MMA(0, 0, At, B0); PG8_MMA(0, 1, At, B1); PG8_BAR; PG8_SCHED;
;             PG8_LDA(At, 0, 1); PG8_STAGE(PG8_SB(0, 0), b2, voffB); PG8_STAGE(PG8_SB(0, 1), b2 + hstepB, voffB); PG8_STAGE(PG8_SA(0, 0), a2, voffA);
;             PG8_WAIT_V(8); PG8_WAIT_L(0); PG8_BAR; PG8_MMA(1, 0, At, B0); PG8_MMA(1, 1, At, B1); PG8_BAR; PG8_SCHED;
.LBB0_809:
	ds_read_b128 v[144:147], v135
	ds_read_b128 v[148:151], v135 offset:16
	ds_read_b128 v[152:155], v135 offset:2048
	ds_read_b128 v[156:159], v135 offset:2064
	ds_read_b128 v[160:163], v135 offset:16384
	ds_read_b128 v[164:167], v135 offset:16400
	ds_read_b128 v[168:171], v135 offset:18432
	ds_read_b128 v[172:175], v135 offset:18448
	s_add_u32 s50, s48, 0x100
	s_addc_u32 s51, s49, 0
	s_cmp_eq_u32 s83, 40
	s_cselect_b32 s56, s6, s50
	s_cselect_b32 s57, s7, s51
	s_cselect_b32 s54, s46, s81
	s_cselect_b32 s55, s47, s82
	s_add_u32 s52, s56, 0x80
	s_addc_u32 s53, s57, 0
	ds_read_b128 v[176:179], v134
	ds_read_b128 v[180:183], v134 offset:16
	ds_read_b128 v[184:187], v134 offset:2048
	ds_read_b128 v[188:191], v134 offset:2064
	ds_read_b128 v[192:195], v134 offset:4096
	ds_read_b128 v[196:199], v134 offset:4112
	ds_read_b128 v[200:203], v134 offset:6144
	ds_read_b128 v[204:207], v134 offset:6160
	s_add_u32 s48, s48, 0xb0080
	s_addc_u32 s49, s49, 0
	s_mov_b32 s84, m0
	s_mov_b32 m0, s72
	s_nop 0
	global_load_lds_dwordx4 v136, s[48:49]
	s_mov_b32 m0, s84
	s_nop 0
	s_mov_b32 s84, m0
	s_mov_b32 m0, s73
	s_nop 0
	global_load_lds_dwordx4 v138, s[48:49]
	s_mov_b32 m0, s84
	s_waitcnt vmcnt(8)
	s_waitcnt lgkmcnt(0)
	s_barrier
	s_setprio 1
	v_mfma_scale_f32_16x16x128_f8f6f4 v[124:127], v[144:151], v[176:183], v[124:127], v142, v142 op_sel_hi:[0,0,0]
	v_mfma_scale_f32_16x16x128_f8f6f4 v[120:123], v[152:159], v[176:183], v[120:123], v142, v142 op_sel_hi:[0,0,0]
	v_mfma_scale_f32_16x16x128_f8f6f4 v[108:111], v[144:151], v[184:191], v[108:111], v142, v142 op_sel_hi:[0,0,0]
	v_mfma_scale_f32_16x16x128_f8f6f4 v[104:107], v[152:159], v[184:191], v[104:107], v142, v142 op_sel_hi:[0,0,0]
	v_mfma_scale_f32_16x16x128_f8f6f4 v[208:211], v[144:151], v[192:199], v[92:95], v142, v142 op_sel_hi:[0,0,0]
	v_mfma_scale_f32_16x16x128_f8f6f4 v[212:215], v[152:159], v[192:199], v[88:91], v142, v142 op_sel_hi:[0,0,0]
	v_mfma_scale_f32_16x16x128_f8f6f4 v[216:219], v[144:151], v[200:207], v[76:79], v142, v142 op_sel_hi:[0,0,0]
	v_mfma_scale_f32_16x16x128_f8f6f4 v[220:223], v[152:159], v[200:207], v[72:75], v142, v142 op_sel_hi:[0,0,0]
	v_mfma_scale_f32_16x16x128_f8f6f4 v[116:119], v[160:167], v[176:183], v[116:119], v142, v142 op_sel_hi:[0,0,0]
	v_mfma_scale_f32_16x16x128_f8f6f4 v[112:115], v[168:175], v[176:183], v[112:115], v142, v142 op_sel_hi:[0,0,0]
	v_mfma_scale_f32_16x16x128_f8f6f4 v[100:103], v[160:167], v[184:191], v[100:103], v142, v142 op_sel_hi:[0,0,0]
	v_mfma_scale_f32_16x16x128_f8f6f4 v[96:99], v[168:175], v[184:191], v[96:99], v142, v142 op_sel_hi:[0,0,0]
	v_mfma_scale_f32_16x16x128_f8f6f4 v[176:179], v[160:167], v[192:199], v[84:87], v142, v142 op_sel_hi:[0,0,0]
	v_mfma_scale_f32_16x16x128_f8f6f4 v[180:183], v[168:175], v[192:199], v[80:83], v142, v142 op_sel_hi:[0,0,0]
	v_mfma_scale_f32_16x16x128_f8f6f4 v[184:187], v[160:167], v[200:207], v[68:71], v142, v142 op_sel_hi:[0,0,0]
	v_mfma_scale_f32_16x16x128_f8f6f4 v[188:191], v[168:175], v[200:207], v[64:67], v142, v142 op_sel_hi:[0,0,0]
	s_setprio 0
	s_barrier
	s_nop 4
	ds_read_b128 v[64:67], v134 offset:16384
	ds_read_b128 v[68:71], v134 offset:16400
	ds_read_b128 v[72:75], v134 offset:18432
	ds_read_b128 v[76:79], v134 offset:18448
	ds_read_b128 v[80:83], v134 offset:20480
	ds_read_b128 v[84:87], v134 offset:20496
	ds_read_b128 v[88:91], v134 offset:22528
	ds_read_b128 v[92:95], v134 offset:22544
	s_mov_b32 s48, m0
	s_mov_b32 m0, s59
	s_nop 0
	global_load_lds_dwordx4 v137, s[54:55]
	s_mov_b32 m0, s48
	s_nop 0
	s_mov_b32 s48, m0
	s_mov_b32 m0, s60
	s_nop 0
	global_load_lds_dwordx4 v139, s[54:55]
	s_mov_b32 m0, s48
	s_add_u32 s48, s54, 0xb0000
	s_addc_u32 s49, s55, 0
	s_mov_b32 s84, m0
	s_mov_b32 m0, s61
	s_nop 0
	global_load_lds_dwordx4 v137, s[48:49]
	s_mov_b32 m0, s84
	s_nop 0
	s_mov_b32 s84, m0
	s_mov_b32 m0, s62
	s_nop 0
	global_load_lds_dwordx4 v139, s[48:49]
	s_mov_b32 m0, s84
	s_mov_b32 s48, m0
	s_mov_b32 m0, s58
	s_nop 0
	global_load_lds_dwordx4 v136, s[56:57]
	s_mov_b32 m0, s48
	s_nop 0
	s_mov_b32 s48, m0
	s_mov_b32 m0, s63
	s_nop 0
	global_load_lds_dwordx4 v138, s[56:57]
	s_mov_b32 m0, s48
	s_waitcnt vmcnt(8)
	s_waitcnt lgkmcnt(0)
	s_barrier
	s_setprio 1
	v_mfma_scale_f32_16x16x128_f8f6f4 v[60:63], v[144:151], v[64:71], v[60:63], v142, v142 op_sel_hi:[0,0,0]
	v_mfma_scale_f32_16x16x128_f8f6f4 v[56:59], v[152:159], v[64:71], v[56:59], v142, v142 op_sel_hi:[0,0,0]
	v_mfma_scale_f32_16x16x128_f8f6f4 v[192:195], v[144:151], v[72:79], v[44:47], v142, v142 op_sel_hi:[0,0,0]
	v_mfma_scale_f32_16x16x128_f8f6f4 v[196:199], v[152:159], v[72:79], v[40:43], v142, v142 op_sel_hi:[0,0,0]
	v_mfma_scale_f32_16x16x128_f8f6f4 v[200:203], v[144:151], v[80:87], v[28:31], v142, v142 op_sel_hi:[0,0,0]
	v_mfma_scale_f32_16x16x128_f8f6f4 v[204:207], v[152:159], v[80:87], v[24:27], v142, v142 op_sel_hi:[0,0,0]
	v_mfma_scale_f32_16x16x128_f8f6f4 v[224:227], v[144:151], v[88:95], v[12:15], v142, v142 op_sel_hi:[0,0,0]
	v_mfma_scale_f32_16x16x128_f8f6f4 v[228:231], v[152:159], v[88:95], v[8:11], v142, v142 op_sel_hi:[0,0,0]
	v_mfma_scale_f32_16x16x128_f8f6f4 v[52:55], v[160:167], v[64:71], v[52:55], v142, v142 op_sel_hi:[0,0,0]
	v_mfma_scale_f32_16x16x128_f8f6f4 v[48:51], v[168:175], v[64:71], v[48:51], v142, v142 op_sel_hi:[0,0,0]
	v_mfma_scale_f32_16x16x128_f8f6f4 v[232:235], v[160:167], v[72:79], v[36:39], v142, v142 op_sel_hi:[0,0,0]
	v_mfma_scale_f32_16x16x128_f8f6f4 v[236:239], v[168:175], v[72:79], v[32:35], v142, v142 op_sel_hi:[0,0,0]
	v_mfma_scale_f32_16x16x128_f8f6f4 v[240:243], v[160:167], v[80:87], v[20:23], v142, v142 op_sel_hi:[0,0,0]
	v_mfma_scale_f32_16x16x128_f8f6f4 v[244:247], v[168:175], v[80:87], v[16:19], v142, v142 op_sel_hi:[0,0,0]
	v_mfma_scale_f32_16x16x128_f8f6f4 v[248:251], v[160:167], v[88:95], v[4:7], v142, v142 op_sel_hi:[0,0,0]
	v_mfma_scale_f32_16x16x128_f8f6f4 v[128:131], v[168:175], v[88:95], v[0:3], v142, v142 op_sel_hi:[0,0,0]
	s_setprio 0
	s_barrier
; #define PG8_STAGE(bufoff, gbase, voff) do { _Pragma("unroll") for (int _i = 0; _i < 2; ++_i) { unsigned keep_; \
;         asm volatile("s_mov_b32 %0, m0\n\ts_mov_b32 m0, %3\n\ts_nop 0\n\tglobal_load_lds_dwordx4 %1, %2\n\ts_mov_b32 m0, %0" : "=&s"(keep_) : "v"((voff)[_i]), "s"((const char*)(gbase)), "s"(ldsbase + (unsigned)((bufoff) + _i * 8192)) : "memory"); } } while (0)
; #define PG8_WAIT_V(n) asm volatile("s_waitcnt vmcnt(" #n ")" ::: "memory")
; #define PG8_WAIT_L(n) asm volatile("s_waitcnt lgkmcnt(" #n ")" ::: "memory")
; #define PG8_BAR __builtin_amdgcn_s_barrier()
; #define PG8_SCHED __builtin_amdgcn_sched_barrier(0)
; template <class Epi, class Sched, bool ALIGN_EPI, bool FP8 = false>
; DI void gemm_phase(LAS unsigned char* lds, const Gemm g, const Sched& S, const Epi& E) {
;     ...
;             PG8_LDB(B0, 1, 0); PG8_LDB(B1, 1, 1); PG8_SCHED; PG8_LDA(At, 1, 0); PG8_STAGE(PG8_SA(0, 1), a2 + hstepA, voffA);
;             PG8_WAIT_V(8); PG8_WAIT_L(0); PG8_BAR; PG8_MMA(0, 0, At, B0); PG8_MMA(0, 1, At, B1); PG8_BAR; PG8_SCHED;
;             PG8_LDA(At, 1, 1); PG8_STAGE(PG8_SB(1, 0), b3, voffB); PG8_STAGE(PG8_SB(1, 1), b3 + hstepB, voffB); PG8_STAGE(PG8_SA(1, 0), a3, voffA);
;             PG8_WAIT_V(8); PG8_WAIT_L(0); PG8_BAR; PG8_MMA(1, 0, At, B0); PG8_MMA(1, 1, At, B1); PG8_BAR; PG8_SCHED;
;         }
;         if constexpr (ALIGN_EPI) { if (wr == 0) PG8_BAR; }
;         E(acc, cur, wr, wc, fr, fq);
;         if (!has_next) break;
	s_nop 4
	ds_read_b128 v[0:3], v135 offset:32768
	ds_read_b128 v[4:7], v135 offset:32784
	ds_read_b128 v[16:19], v135 offset:34816
	ds_read_b128 v[20:23], v135 offset:34832
	ds_read_b128 v[144:147], v135 offset:49152
	ds_read_b128 v[148:151], v135 offset:49168
	ds_read_b128 v[152:155], v135 offset:51200
	ds_read_b128 v[156:159], v135 offset:51216
	ds_read_b128 v[8:11], v134 offset:32768
	ds_read_b128 v[12:15], v134 offset:32784
	ds_read_b128 v[24:27], v134 offset:34816
	ds_read_b128 v[28:31], v134 offset:34832
	ds_read_b128 v[32:35], v134 offset:36864
	ds_read_b128 v[36:39], v134 offset:36880
	ds_read_b128 v[40:43], v134 offset:38912
	ds_read_b128 v[44:47], v134 offset:38928
	s_add_u32 s48, s56, 0xb0000
	s_addc_u32 s49, s57, 0
	s_mov_b32 s56, m0
	s_mov_b32 m0, s64
	s_nop 0
	global_load_lds_dwordx4 v136, s[48:49]
	s_mov_b32 m0, s56
	s_nop 0
	s_mov_b32 s56, m0
	s_mov_b32 m0, s65
	s_nop 0
	global_load_lds_dwordx4 v138, s[48:49]
	s_mov_b32 m0, s56
	s_waitcnt vmcnt(8)
	s_waitcnt lgkmcnt(0)
	s_barrier
	s_setprio 1
	v_mfma_scale_f32_16x16x128_f8f6f4 v[124:127], v[0:7], v[8:15], v[124:127], v142, v142 op_sel_hi:[0,0,0]
	v_mfma_scale_f32_16x16x128_f8f6f4 v[120:123], v[16:23], v[8:15], v[120:123], v142, v142 op_sel_hi:[0,0,0]
	v_mfma_scale_f32_16x16x128_f8f6f4 v[108:111], v[0:7], v[24:31], v[108:111], v142, v142 op_sel_hi:[0,0,0]
	v_mfma_scale_f32_16x16x128_f8f6f4 v[104:107], v[16:23], v[24:31], v[104:107], v142, v142 op_sel_hi:[0,0,0]
	v_mfma_scale_f32_16x16x128_f8f6f4 v[92:95], v[0:7], v[32:39], v[208:211], v142, v142 op_sel_hi:[0,0,0]
	v_mfma_scale_f32_16x16x128_f8f6f4 v[88:91], v[16:23], v[32:39], v[212:215], v142, v142 op_sel_hi:[0,0,0]
	v_mfma_scale_f32_16x16x128_f8f6f4 v[76:79], v[0:7], v[40:47], v[216:219], v142, v142 op_sel_hi:[0,0,0]
	v_mfma_scale_f32_16x16x128_f8f6f4 v[72:75], v[16:23], v[40:47], v[220:223], v142, v142 op_sel_hi:[0,0,0]
	v_mfma_scale_f32_16x16x128_f8f6f4 v[116:119], v[144:151], v[8:15], v[116:119], v142, v142 op_sel_hi:[0,0,0]
	v_mfma_scale_f32_16x16x128_f8f6f4 v[112:115], v[152:159], v[8:15], v[112:115], v142, v142 op_sel_hi:[0,0,0]
	v_mfma_scale_f32_16x16x128_f8f6f4 v[100:103], v[144:151], v[24:31], v[100:103], v142, v142 op_sel_hi:[0,0,0]
	v_mfma_scale_f32_16x16x128_f8f6f4 v[96:99], v[152:159], v[24:31], v[96:99], v142, v142 op_sel_hi:[0,0,0]
	v_mfma_scale_f32_16x16x128_f8f6f4 v[84:87], v[144:151], v[32:39], v[176:179], v142, v142 op_sel_hi:[0,0,0]
	v_mfma_scale_f32_16x16x128_f8f6f4 v[80:83], v[152:159], v[32:39], v[180:183], v142, v142 op_sel_hi:[0,0,0]
	v_mfma_scale_f32_16x16x128_f8f6f4 v[68:71], v[144:151], v[40:47], v[184:187], v142, v142 op_sel_hi:[0,0,0]
	v_mfma_scale_f32_16x16x128_f8f6f4 v[64:67], v[152:159], v[40:47], v[188:191], v142, v142 op_sel_hi:[0,0,0]
	s_setprio 0
	s_barrier
	ds_read_b128 v[32:35], v134 offset:49152
	ds_read_b128 v[36:39], v134 offset:49168
	ds_read_b128 v[160:163], v134 offset:51200
	ds_read_b128 v[164:167], v134 offset:51216
	ds_read_b128 v[168:171], v134 offset:53248
	ds_read_b128 v[172:175], v134 offset:53264
	ds_read_b128 v[176:179], v134 offset:55296
	ds_read_b128 v[180:183], v134 offset:55312
	s_add_u32 s48, s54, 0x80
	s_addc_u32 s49, s55, 0
	s_mov_b32 s56, m0
	s_mov_b32 m0, s66
	s_nop 0
	global_load_lds_dwordx4 v137, s[48:49]
	s_mov_b32 m0, s56
	s_nop 0
	s_mov_b32 s56, m0
	s_mov_b32 m0, s67
	s_nop 0
	global_load_lds_dwordx4 v139, s[48:49]
	s_mov_b32 m0, s56
	s_add_u32 s48, s54, 0xb0080
	s_addc_u32 s49, s55, 0
	s_mov_b32 s54, m0
	s_mov_b32 m0, s70
	s_nop 0
	global_load_lds_dwordx4 v137, s[48:49]
	s_mov_b32 m0, s54
	s_nop 0
	s_mov_b32 s54, m0
	s_mov_b32 m0, s71
	s_nop 0
	global_load_lds_dwordx4 v139, s[48:49]
	s_mov_b32 m0, s54
	s_mov_b32 s48, m0
	s_mov_b32 m0, s68
	s_nop 0
	global_load_lds_dwordx4 v136, s[52:53]
	s_mov_b32 m0, s48
	s_nop 0
	s_mov_b32 s48, m0
	s_mov_b32 m0, s69
	s_nop 0
	global_load_lds_dwordx4 v138, s[52:53]
	s_mov_b32 m0, s48
	s_waitcnt vmcnt(8)
	s_waitcnt lgkmcnt(0)
	s_barrier
	s_setprio 1
	v_mfma_scale_f32_16x16x128_f8f6f4 v[60:63], v[0:7], v[32:39], v[60:63], v142, v142 op_sel_hi:[0,0,0]
	v_mfma_scale_f32_16x16x128_f8f6f4 v[56:59], v[16:23], v[32:39], v[56:59], v142, v142 op_sel_hi:[0,0,0]
	v_mfma_scale_f32_16x16x128_f8f6f4 v[44:47], v[0:7], v[160:167], v[192:195], v142, v142 op_sel_hi:[0,0,0]
	v_mfma_scale_f32_16x16x128_f8f6f4 v[40:43], v[16:23], v[160:167], v[196:199], v142, v142 op_sel_hi:[0,0,0]
	v_mfma_scale_f32_16x16x128_f8f6f4 v[28:31], v[0:7], v[168:175], v[200:203], v142, v142 op_sel_hi:[0,0,0]
	v_mfma_scale_f32_16x16x128_f8f6f4 v[24:27], v[16:23], v[168:175], v[204:207], v142, v142 op_sel_hi:[0,0,0]
	v_mfma_scale_f32_16x16x128_f8f6f4 v[12:15], v[0:7], v[176:183], v[224:227], v142, v142 op_sel_hi:[0,0,0]
	v_mfma_scale_f32_16x16x128_f8f6f4 v[8:11], v[16:23], v[176:183], v[228:231], v142, v142 op_sel_hi:[0,0,0]
	v_mfma_scale_f32_16x16x128_f8f6f4 v[52:55], v[144:151], v[32:39], v[52:55], v142, v142 op_sel_hi:[0,0,0]
	v_mfma_scale_f32_16x16x128_f8f6f4 v[48:51], v[152:159], v[32:39], v[48:51], v142, v142 op_sel_hi:[0,0,0]
	v_mfma_scale_f32_16x16x128_f8f6f4 v[36:39], v[144:151], v[160:167], v[232:235], v142, v142 op_sel_hi:[0,0,0]
	v_mfma_scale_f32_16x16x128_f8f6f4 v[32:35], v[152:159], v[160:167], v[236:239], v142, v142 op_sel_hi:[0,0,0]
	v_mfma_scale_f32_16x16x128_f8f6f4 v[20:23], v[144:151], v[168:175], v[240:243], v142, v142 op_sel_hi:[0,0,0]
	v_mfma_scale_f32_16x16x128_f8f6f4 v[16:19], v[152:159], v[168:175], v[244:247], v142, v142 op_sel_hi:[0,0,0]
	v_mfma_scale_f32_16x16x128_f8f6f4 v[4:7], v[144:151], v[176:183], v[248:251], v142, v142 op_sel_hi:[0,0,0]
	v_mfma_scale_f32_16x16x128_f8f6f4 v[0:3], v[152:159], v[176:183], v[128:131], v142, v142 op_sel_hi:[0,0,0]
	s_setprio 0
	s_barrier
	s_add_i32 s83, s83, 2
	s_add_u32 s81, s81, 0x100
	s_addc_u32 s82, s82, 0
	s_cmp_gt_u32 s83, 41
	s_mov_b64 s[48:49], s[50:51]
	s_cbranch_scc0 .LBB0_809
	s_and_b64 vcc, exec, s[20:21]
	s_cbranch_vccz .LBB0_812
	s_barrier

; #define PG8_STAGE(bufoff, gbase, voff) do { _Pragma("unroll") for (int _i = 0; _i < 2; ++_i) { unsigned keep_; \
;         asm volatile("s_mov_b32 %0, m0\n\ts_mov_b32 m0, %3\n\ts_nop 0\n\tglobal_load_lds_dwordx4 %1, %2\n\ts_mov_b32 m0, %0" : "=&s"(keep_) : "v"((voff)[_i]), "s"((const char*)(gbase)), "s"(ldsbase + (unsigned)((bufoff) + _i * 8192)) : "memory"); } } while (0)
; #define PG8_WAIT_V(n) asm volatile("s_waitcnt vmcnt(" #n ")" ::: "memory")
; #define PG8_WAIT_L(n) asm volatile("s_waitcnt lgkmcnt(" #n ")" ::: "memory")
; #define PG8_BAR __builtin_amdgcn_s_barrier()
; #define PG8_SCHED __builtin_amdgcn_sched_barrier(0)
;     DI int nt(const Unit& u) const { return (u.aux & 8) ? PLED / 64 : ((u.aux & 4) ? (D_ / 2) / 64 : D_ / 64); }
; template <class Epi, class Sched, bool ALIGN_EPI, bool FP8 = false>
; DI void gemm_phase(LAS unsigned char* lds, const Gemm g, const Sched& S, const Epi& E) {
;     ...
;             const bool last = (t == nt - 2);
;             const char* a1 = cA + (size_t)(t + 1) * kstep;
;             const char* a2 = last ? nA : cA + (size_t)(t + 2) * kstep; const char* b2 = last ? nB : cB + (size_t)(t + 2) * kstep;
;             const char* a3 = a2 + kstep; const char* b3 = b2 + kstep;
;             PG8_LDB(B0, 0, 0); PG8_LDB(B1, 0, 1); PG8_SCHED; PG8_LDA(At, 0, 0); PG8_STAGE(PG8_SA(1, 1), a1 + hstepA, voffA);
;             PG8_WAIT_V(8); PG8_WAIT_L(0); PG8_BAR; PG8_MMA(0, 0, At, B0); PG8_MMA(0, 1, At, B1); PG8_BAR; PG8_SCHED;
;             PG8_LDA(At, 0, 1); PG8_STAGE(PG8_SB(0, 0), b2, voffB); PG8_STAGE(PG8_SB(0, 1), b2 + hstepB, voffB); PG8_STAGE(PG8_SA(0, 0), a2, voffA);
;             PG8_WAIT_V(8); PG8_WAIT_L(0); PG8_BAR; PG8_MMA(1, 0, At, B0); PG8_MMA(1, 1, At, B1); PG8_BAR; PG8_SCHED;
.LBB0_991:
	s_add_i32 s53, s51, 2
	s_add_u32 s42, s18, s56
	s_addc_u32 s43, s19, s57
	s_add_u32 s58, s42, 0x100
	v_add_u32_e32 v130, 0x10000, v157
	s_addc_u32 s59, s43, 0
	ds_read_b128 v[146:149], v130
	ds_read_b128 v[150:153], v130 offset:1024
	ds_read_b128 v[160:163], v130 offset:2048
	ds_read_b128 v[164:167], v130 offset:3072
	v_add_u32_e32 v130, 0x14000, v157
	s_add_u32 s60, s22, s56
	ds_read_b128 v[168:171], v130
	ds_read_b128 v[172:175], v130 offset:1024
	ds_read_b128 v[176:179], v130 offset:2048
	ds_read_b128 v[180:183], v130 offset:3072
	s_addc_u32 s61, s23, s57
	s_add_u32 s60, s60, 0x100
	s_addc_u32 s61, s61, 0
	s_cmp_eq_u32 s20, s51
	s_cselect_b32 s62, s8, s58
	s_cselect_b32 s63, s9, s59
	s_cselect_b32 s60, s54, s60
	s_cselect_b32 s61, s55, s61
	s_add_u32 s58, s62, 0x80
	s_addc_u32 s59, s63, 0
	ds_read_b128 v[184:187], v158
	ds_read_b128 v[188:191], v158 offset:1024
	ds_read_b128 v[192:195], v158 offset:2048
	ds_read_b128 v[196:199], v158 offset:3072
	ds_read_b128 v[200:203], v158 offset:4096
	ds_read_b128 v[204:207], v158 offset:5120
	ds_read_b128 v[208:211], v158 offset:6144
	ds_read_b128 v[212:215], v158 offset:7168
	s_add_u32 s42, s42, 0x80080
	s_addc_u32 s43, s43, 0
	s_mov_b32 s51, m0
	s_mov_b32 m0, s89
	s_nop 0
	global_load_lds_dwordx4 v129, s[42:43]
	s_mov_b32 m0, s51
	s_nop 0
	s_mov_b32 s51, m0
	s_mov_b32 m0, s90
	s_nop 0
	global_load_lds_dwordx4 v154, s[42:43]
	s_mov_b32 m0, s51
	s_waitcnt vmcnt(8)
	s_waitcnt lgkmcnt(0)
	s_barrier
	s_setprio 1
	v_mfma_f32_16x16x32_bf16 v[124:127], v[146:149], v[184:187], v[124:127]
	v_mfma_f32_16x16x32_bf16 v[120:123], v[160:163], v[184:187], v[120:123]
	v_mfma_f32_16x16x32_bf16 v[116:119], v[146:149], v[192:195], v[116:119]
	v_mfma_f32_16x16x32_bf16 v[112:115], v[160:163], v[192:195], v[112:115]
	v_mfma_f32_16x16x32_bf16 v[108:111], v[146:149], v[200:203], v[108:111]
	v_mfma_f32_16x16x32_bf16 v[104:107], v[160:163], v[200:203], v[104:107]
	v_mfma_f32_16x16x32_bf16 v[100:103], v[146:149], v[208:211], v[100:103]
	v_mfma_f32_16x16x32_bf16 v[96:99], v[160:163], v[208:211], v[96:99]
	v_mfma_f32_16x16x32_bf16 v[124:127], v[150:153], v[188:191], v[124:127]
	v_mfma_f32_16x16x32_bf16 v[120:123], v[164:167], v[188:191], v[120:123]
	v_mfma_f32_16x16x32_bf16 v[116:119], v[150:153], v[196:199], v[116:119]
	v_mfma_f32_16x16x32_bf16 v[112:115], v[164:167], v[196:199], v[112:115]
	v_mfma_f32_16x16x32_bf16 v[108:111], v[150:153], v[204:207], v[108:111]
	v_mfma_f32_16x16x32_bf16 v[104:107], v[164:167], v[204:207], v[104:107]
	v_mfma_f32_16x16x32_bf16 v[100:103], v[150:153], v[212:215], v[100:103]
	v_mfma_f32_16x16x32_bf16 v[96:99], v[164:167], v[212:215], v[96:99]
	v_mfma_f32_16x16x32_bf16 v[92:95], v[168:171], v[184:187], v[92:95]
	v_mfma_f32_16x16x32_bf16 v[88:91], v[176:179], v[184:187], v[88:91]
	v_mfma_f32_16x16x32_bf16 v[84:87], v[168:171], v[192:195], v[84:87]
	v_mfma_f32_16x16x32_bf16 v[80:83], v[176:179], v[192:195], v[80:83]
	v_mfma_f32_16x16x32_bf16 v[76:79], v[168:171], v[200:203], v[76:79]
	v_mfma_f32_16x16x32_bf16 v[72:75], v[176:179], v[200:203], v[72:75]
	v_mfma_f32_16x16x32_bf16 v[68:71], v[168:171], v[208:211], v[68:71]
	v_mfma_f32_16x16x32_bf16 v[64:67], v[176:179], v[208:211], v[64:67]
	v_mfma_f32_16x16x32_bf16 v[92:95], v[172:175], v[188:191], v[92:95]
	v_mfma_f32_16x16x32_bf16 v[88:91], v[180:183], v[188:191], v[88:91]
	v_mfma_f32_16x16x32_bf16 v[84:87], v[172:175], v[196:199], v[84:87]
	v_mfma_f32_16x16x32_bf16 v[80:83], v[180:183], v[196:199], v[80:83]
	v_mfma_f32_16x16x32_bf16 v[76:79], v[172:175], v[204:207], v[76:79]
	v_mfma_f32_16x16x32_bf16 v[72:75], v[180:183], v[204:207], v[72:75]
	v_mfma_f32_16x16x32_bf16 v[68:71], v[172:175], v[212:215], v[68:71]
	v_mfma_f32_16x16x32_bf16 v[64:67], v[180:183], v[212:215], v[64:67]
	s_setprio 0
	s_barrier
	ds_read_b128 v[184:187], v158 offset:16384
	ds_read_b128 v[188:191], v158 offset:17408
	ds_read_b128 v[192:195], v158 offset:18432
	ds_read_b128 v[196:199], v158 offset:19456
	ds_read_b128 v[200:203], v158 offset:20480
	ds_read_b128 v[204:207], v158 offset:21504
	ds_read_b128 v[208:211], v158 offset:22528
	ds_read_b128 v[212:215], v158 offset:23552
	s_mov_b32 s42, m0
	s_mov_b32 m0, s17
	s_nop 0
	global_load_lds_dwordx4 v145, s[60:61]
	s_mov_b32 m0, s42
	s_nop 0
	s_mov_b32 s42, m0
	s_mov_b32 m0, s68
	s_nop 0
	global_load_lds_dwordx4 v155, s[60:61]
	s_mov_b32 m0, s42
	s_add_u32 s42, s60, 0x80000
	s_addc_u32 s43, s61, 0
	s_mov_b32 s51, m0
	s_mov_b32 m0, s69
	s_nop 0
	global_load_lds_dwordx4 v145, s[42:43]
	s_mov_b32 m0, s51
	s_nop 0
	s_mov_b32 s51, m0
	s_mov_b32 m0, s70
	s_nop 0
	global_load_lds_dwordx4 v155, s[42:43]
	s_mov_b32 m0, s51
	s_mov_b32 s42, m0
	s_mov_b32 m0, s15
	s_nop 0
	global_load_lds_dwordx4 v129, s[62:63]
	s_mov_b32 m0, s42
	s_nop 0
	s_mov_b32 s42, m0
	s_mov_b32 m0, s71
	s_nop 0
	global_load_lds_dwordx4 v154, s[62:63]
	s_mov_b32 m0, s42
	s_waitcnt vmcnt(8)
	s_waitcnt lgkmcnt(0)
	s_barrier
; #define PG8_STAGE(bufoff, gbase, voff) do { _Pragma("unroll") for (int _i = 0; _i < 2; ++_i) { unsigned keep_; \
;         asm volatile("s_mov_b32 %0, m0\n\ts_mov_b32 m0, %3\n\ts_nop 0\n\tglobal_load_lds_dwordx4 %1, %2\n\ts_mov_b32 m0, %0" : "=&s"(keep_) : "v"((voff)[_i]), "s"((const char*)(gbase)), "s"(ldsbase + (unsigned)((bufoff) + _i * 8192)) : "memory"); } } while (0)
; #define PG8_WAIT_V(n) asm volatile("s_waitcnt vmcnt(" #n ")" ::: "memory")
; #define PG8_WAIT_L(n) asm volatile("s_waitcnt lgkmcnt(" #n ")" ::: "memory")
; #define PG8_BAR __builtin_amdgcn_s_barrier()
; #define PG8_SCHED __builtin_amdgcn_sched_barrier(0)
; template <class Epi, class Sched, bool ALIGN_EPI, bool FP8 = false>
; DI void gemm_phase(LAS unsigned char* lds, const Gemm g, const Sched& S, const Epi& E) {
;     ...
;             PG8_WAIT_V(8); PG8_WAIT_L(0); PG8_BAR; PG8_MMA(1, 0, At, B0); PG8_MMA(1, 1, At, B1); PG8_BAR; PG8_SCHED;
;             PG8_LDB(B0, 1, 0); PG8_LDB(B1, 1, 1); PG8_SCHED; PG8_LDA(At, 1, 0); PG8_STAGE(PG8_SA(0, 1), a2 + hstepA, voffA);
;             PG8_WAIT_V(8); PG8_WAIT_L(0); PG8_BAR; PG8_MMA(0, 0, At, B0); PG8_MMA(0, 1, At, B1); PG8_BAR; PG8_SCHED;
	s_setprio 1
	v_mfma_f32_16x16x32_bf16 v[60:63], v[146:149], v[184:187], v[60:63]
	v_mfma_f32_16x16x32_bf16 v[56:59], v[160:163], v[184:187], v[56:59]
	v_mfma_f32_16x16x32_bf16 v[52:55], v[146:149], v[192:195], v[52:55]
	v_mfma_f32_16x16x32_bf16 v[48:51], v[160:163], v[192:195], v[48:51]
	v_mfma_f32_16x16x32_bf16 v[44:47], v[146:149], v[200:203], v[44:47]
	v_mfma_f32_16x16x32_bf16 v[40:43], v[160:163], v[200:203], v[40:43]
	v_mfma_f32_16x16x32_bf16 v[36:39], v[146:149], v[208:211], v[36:39]
	v_mfma_f32_16x16x32_bf16 v[32:35], v[160:163], v[208:211], v[32:35]
	v_mfma_f32_16x16x32_bf16 v[60:63], v[150:153], v[188:191], v[60:63]
	v_mfma_f32_16x16x32_bf16 v[56:59], v[164:167], v[188:191], v[56:59]
	v_mfma_f32_16x16x32_bf16 v[52:55], v[150:153], v[196:199], v[52:55]
	v_mfma_f32_16x16x32_bf16 v[48:51], v[164:167], v[196:199], v[48:51]
	v_mfma_f32_16x16x32_bf16 v[44:47], v[150:153], v[204:207], v[44:47]
	v_mfma_f32_16x16x32_bf16 v[40:43], v[164:167], v[204:207], v[40:43]
	v_mfma_f32_16x16x32_bf16 v[36:39], v[150:153], v[212:215], v[36:39]
	v_mfma_f32_16x16x32_bf16 v[32:35], v[164:167], v[212:215], v[32:35]
	v_mfma_f32_16x16x32_bf16 v[28:31], v[168:171], v[184:187], v[28:31]
	v_mfma_f32_16x16x32_bf16 v[24:27], v[176:179], v[184:187], v[24:27]
	v_mfma_f32_16x16x32_bf16 v[20:23], v[168:171], v[192:195], v[20:23]
	v_mfma_f32_16x16x32_bf16 v[16:19], v[176:179], v[192:195], v[16:19]
	v_mfma_f32_16x16x32_bf16 v[12:15], v[168:171], v[200:203], v[12:15]
	v_mfma_f32_16x16x32_bf16 v[8:11], v[176:179], v[200:203], v[8:11]
	v_mfma_f32_16x16x32_bf16 v[4:7], v[168:171], v[208:211], v[4:7]
	v_mfma_f32_16x16x32_bf16 v[0:3], v[176:179], v[208:211], v[0:3]
	v_mfma_f32_16x16x32_bf16 v[28:31], v[172:175], v[188:191], v[28:31]
	v_mfma_f32_16x16x32_bf16 v[24:27], v[180:183], v[188:191], v[24:27]
	v_mfma_f32_16x16x32_bf16 v[20:23], v[172:175], v[196:199], v[20:23]
	v_mfma_f32_16x16x32_bf16 v[16:19], v[180:183], v[196:199], v[16:19]
	v_mfma_f32_16x16x32_bf16 v[12:15], v[172:175], v[204:207], v[12:15]
	v_mfma_f32_16x16x32_bf16 v[8:11], v[180:183], v[204:207], v[8:11]
	v_mfma_f32_16x16x32_bf16 v[4:7], v[172:175], v[212:215], v[4:7]
	v_mfma_f32_16x16x32_bf16 v[0:3], v[180:183], v[212:215], v[0:3]
	s_setprio 0
	s_barrier
	v_add_u32_e32 v130, 0x18000, v157
	ds_read_b128 v[146:149], v130
	ds_read_b128 v[150:153], v130 offset:1024
	ds_read_b128 v[160:163], v130 offset:2048
	ds_read_b128 v[164:167], v130 offset:3072
	v_add_u32_e32 v130, 0x1c000, v157
	ds_read_b128 v[168:171], v130
	ds_read_b128 v[172:175], v130 offset:1024
	ds_read_b128 v[176:179], v130 offset:2048
	ds_read_b128 v[180:183], v130 offset:3072
	ds_read_b128 v[184:187], v158 offset:32768
	ds_read_b128 v[188:191], v158 offset:33792
	ds_read_b128 v[192:195], v158 offset:34816
	ds_read_b128 v[196:199], v158 offset:35840
	ds_read_b128 v[200:203], v158 offset:36864
	ds_read_b128 v[204:207], v158 offset:37888
	ds_read_b128 v[208:211], v158 offset:38912
	ds_read_b128 v[212:215], v158 offset:39936
	s_add_u32 s42, s62, 0x80000
	s_addc_u32 s43, s63, 0
	s_mov_b32 s51, m0
	s_mov_b32 m0, s72
	s_nop 0
	global_load_lds_dwordx4 v129, s[42:43]
	s_mov_b32 m0, s51
	s_nop 0
	s_mov_b32 s51, m0
	s_mov_b32 m0, s73
	s_nop 0
	global_load_lds_dwordx4 v154, s[42:43]
	s_mov_b32 m0, s51
	s_waitcnt vmcnt(8)
	s_waitcnt lgkmcnt(0)
	s_barrier
	s_setprio 1
	v_mfma_f32_16x16x32_bf16 v[124:127], v[146:149], v[184:187], v[124:127]
	v_mfma_f32_16x16x32_bf16 v[120:123], v[160:163], v[184:187], v[120:123]
	v_mfma_f32_16x16x32_bf16 v[116:119], v[146:149], v[192:195], v[116:119]
	v_mfma_f32_16x16x32_bf16 v[112:115], v[160:163], v[192:195], v[112:115]
	v_mfma_f32_16x16x32_bf16 v[108:111], v[146:149], v[200:203], v[108:111]
	v_mfma_f32_16x16x32_bf16 v[104:107], v[160:163], v[200:203], v[104:107]
	v_mfma_f32_16x16x32_bf16 v[100:103], v[146:149], v[208:211], v[100:103]
	v_mfma_f32_16x16x32_bf16 v[96:99], v[160:163], v[208:211], v[96:99]
	v_mfma_f32_16x16x32_bf16 v[124:127], v[150:153], v[188:191], v[124:127]
	v_mfma_f32_16x16x32_bf16 v[120:123], v[164:167], v[188:191], v[120:123]
	v_mfma_f32_16x16x32_bf16 v[116:119], v[150:153], v[196:199], v[116:119]
	v_mfma_f32_16x16x32_bf16 v[112:115], v[164:167], v[196:199], v[112:115]
	v_mfma_f32_16x16x32_bf16 v[108:111], v[150:153], v[204:207], v[108:111]
	v_mfma_f32_16x16x32_bf16 v[104:107], v[164:167], v[204:207], v[104:107]
	v_mfma_f32_16x16x32_bf16 v[100:103], v[150:153], v[212:215], v[100:103]
	v_mfma_f32_16x16x32_bf16 v[96:99], v[164:167], v[212:215], v[96:99]
	v_mfma_f32_16x16x32_bf16 v[92:95], v[168:171], v[184:187], v[92:95]
	v_mfma_f32_16x16x32_bf16 v[88:91], v[176:179], v[184:187], v[88:91]
	v_mfma_f32_16x16x32_bf16 v[84:87], v[168:171], v[192:195], v[84:87]
	v_mfma_f32_16x16x32_bf16 v[80:83], v[176:179], v[192:195], v[80:83]
	v_mfma_f32_16x16x32_bf16 v[76:79], v[168:171], v[200:203], v[76:79]
	v_mfma_f32_16x16x32_bf16 v[72:75], v[176:179], v[200:203], v[72:75]
	v_mfma_f32_16x16x32_bf16 v[68:71], v[168:171], v[208:211], v[68:71]
	v_mfma_f32_16x16x32_bf16 v[64:67], v[176:179], v[208:211], v[64:67]
	v_mfma_f32_16x16x32_bf16 v[92:95], v[172:175], v[188:191], v[92:95]
	v_mfma_f32_16x16x32_bf16 v[88:91], v[180:183], v[188:191], v[88:91]
	v_mfma_f32_16x16x32_bf16 v[84:87], v[172:175], v[196:199], v[84:87]
	v_mfma_f32_16x16x32_bf16 v[80:83], v[180:183], v[196:199], v[80:83]
	v_mfma_f32_16x16x32_bf16 v[76:79], v[172:175], v[204:207], v[76:79]
	v_mfma_f32_16x16x32_bf16 v[72:75], v[180:183], v[204:207], v[72:75]
	v_mfma_f32_16x16x32_bf16 v[68:71], v[172:175], v[212:215], v[68:71]
	v_mfma_f32_16x16x32_bf16 v[64:67], v[180:183], v[212:215], v[64:67]
	s_setprio 0
	s_barrier
; #define PG8_STAGE(bufoff, gbase, voff) do { _Pragma("unroll") for (int _i = 0; _i < 2; ++_i) { unsigned keep_; \
;         asm volatile("s_mov_b32 %0, m0\n\ts_mov_b32 m0, %3\n\ts_nop 0\n\tglobal_load_lds_dwordx4 %1, %2\n\ts_mov_b32 m0, %0" : "=&s"(keep_) : "v"((voff)[_i]), "s"((const char*)(gbase)), "s"(ldsbase + (unsigned)((bufoff) + _i * 8192)) : "memory"); } } while (0)
; #define PG8_WAIT_V(n) asm volatile("s_waitcnt vmcnt(" #n ")" ::: "memory")
; #define PG8_WAIT_L(n) asm volatile("s_waitcnt lgkmcnt(" #n ")" ::: "memory")
; #define PG8_BAR __builtin_amdgcn_s_barrier()
; #define PG8_SCHED __builtin_amdgcn_sched_barrier(0)
; template <class Epi, class Sched, bool ALIGN_EPI, bool FP8 = false>
; DI void gemm_phase(LAS unsigned char* lds, const Gemm g, const Sched& S, const Epi& E) {
;     ...
;             PG8_LDA(At, 1, 1); PG8_STAGE(PG8_SB(1, 0), b3, voffB); PG8_STAGE(PG8_SB(1, 1), b3 + hstepB, voffB); PG8_STAGE(PG8_SA(1, 0), a3, voffA);
;             PG8_WAIT_V(8); PG8_WAIT_L(0); PG8_BAR; PG8_MMA(1, 0, At, B0); PG8_MMA(1, 1, At, B1); PG8_BAR; PG8_SCHED;
;         }
;         if constexpr (ALIGN_EPI) { if (wr == 0) PG8_BAR; }
;         E(acc, cur, wr, wc, fr, fq);
;         if (!has_next) break;
	ds_read_b128 v[184:187], v158 offset:49152
	ds_read_b128 v[188:191], v158 offset:50176
	ds_read_b128 v[192:195], v158 offset:51200
	ds_read_b128 v[196:199], v158 offset:52224
	ds_read_b128 v[200:203], v158 offset:53248
	ds_read_b128 v[204:207], v158 offset:54272
	ds_read_b128 v[208:211], v158 offset:55296
	ds_read_b128 v[212:215], v158 offset:56320
	s_add_u32 s42, s60, 0x80
	s_addc_u32 s43, s61, 0
	s_mov_b32 s51, m0
	s_mov_b32 m0, s83
	s_nop 0
	global_load_lds_dwordx4 v145, s[42:43]
	s_mov_b32 m0, s51
	s_nop 0
	s_mov_b32 s51, m0
	s_mov_b32 m0, s84
	s_nop 0
	global_load_lds_dwordx4 v155, s[42:43]
	s_mov_b32 m0, s51
	s_add_u32 s42, s60, 0x80080
	s_addc_u32 s43, s61, 0
	s_mov_b32 s51, m0
	s_mov_b32 m0, s87
	s_nop 0
	global_load_lds_dwordx4 v145, s[42:43]
	s_mov_b32 m0, s51
	s_nop 0
	s_mov_b32 s51, m0
	s_mov_b32 m0, s88
	s_nop 0
	global_load_lds_dwordx4 v155, s[42:43]
	s_mov_b32 m0, s51
	s_mov_b32 s42, m0
	s_mov_b32 m0, s85
	s_nop 0
	global_load_lds_dwordx4 v129, s[58:59]
	s_mov_b32 m0, s42
	s_nop 0
	s_mov_b32 s42, m0
	s_mov_b32 m0, s86
	s_nop 0
	global_load_lds_dwordx4 v154, s[58:59]
	s_mov_b32 m0, s42
	s_waitcnt vmcnt(8)
	s_waitcnt lgkmcnt(0)
	s_barrier
	s_setprio 1
	v_mfma_f32_16x16x32_bf16 v[60:63], v[146:149], v[184:187], v[60:63]
	v_mfma_f32_16x16x32_bf16 v[56:59], v[160:163], v[184:187], v[56:59]
	v_mfma_f32_16x16x32_bf16 v[52:55], v[146:149], v[192:195], v[52:55]
	v_mfma_f32_16x16x32_bf16 v[48:51], v[160:163], v[192:195], v[48:51]
	v_mfma_f32_16x16x32_bf16 v[44:47], v[146:149], v[200:203], v[44:47]
	v_mfma_f32_16x16x32_bf16 v[40:43], v[160:163], v[200:203], v[40:43]
	v_mfma_f32_16x16x32_bf16 v[36:39], v[146:149], v[208:211], v[36:39]
	v_mfma_f32_16x16x32_bf16 v[32:35], v[160:163], v[208:211], v[32:35]
	v_mfma_f32_16x16x32_bf16 v[60:63], v[150:153], v[188:191], v[60:63]
	v_mfma_f32_16x16x32_bf16 v[56:59], v[164:167], v[188:191], v[56:59]
	v_mfma_f32_16x16x32_bf16 v[52:55], v[150:153], v[196:199], v[52:55]
	v_mfma_f32_16x16x32_bf16 v[48:51], v[164:167], v[196:199], v[48:51]
	v_mfma_f32_16x16x32_bf16 v[44:47], v[150:153], v[204:207], v[44:47]
	v_mfma_f32_16x16x32_bf16 v[40:43], v[164:167], v[204:207], v[40:43]
	v_mfma_f32_16x16x32_bf16 v[36:39], v[150:153], v[212:215], v[36:39]
	v_mfma_f32_16x16x32_bf16 v[32:35], v[164:167], v[212:215], v[32:35]
	v_mfma_f32_16x16x32_bf16 v[28:31], v[168:171], v[184:187], v[28:31]
	v_mfma_f32_16x16x32_bf16 v[24:27], v[176:179], v[184:187], v[24:27]
	v_mfma_f32_16x16x32_bf16 v[20:23], v[168:171], v[192:195], v[20:23]
	v_mfma_f32_16x16x32_bf16 v[16:19], v[176:179], v[192:195], v[16:19]
	v_mfma_f32_16x16x32_bf16 v[12:15], v[168:171], v[200:203], v[12:15]
	v_mfma_f32_16x16x32_bf16 v[8:11], v[176:179], v[200:203], v[8:11]
	v_mfma_f32_16x16x32_bf16 v[4:7], v[168:171], v[208:211], v[4:7]
	v_mfma_f32_16x16x32_bf16 v[0:3], v[176:179], v[208:211], v[0:3]
	v_mfma_f32_16x16x32_bf16 v[28:31], v[172:175], v[188:191], v[28:31]
	v_mfma_f32_16x16x32_bf16 v[24:27], v[180:183], v[188:191], v[24:27]
	v_mfma_f32_16x16x32_bf16 v[20:23], v[172:175], v[196:199], v[20:23]
	v_mfma_f32_16x16x32_bf16 v[16:19], v[180:183], v[196:199], v[16:19]
	v_mfma_f32_16x16x32_bf16 v[12:15], v[172:175], v[204:207], v[12:15]
	v_mfma_f32_16x16x32_bf16 v[8:11], v[180:183], v[204:207], v[8:11]
	v_mfma_f32_16x16x32_bf16 v[4:7], v[172:175], v[212:215], v[4:7]
	v_mfma_f32_16x16x32_bf16 v[0:3], v[180:183], v[212:215], v[0:3]
	s_setprio 0
	s_barrier
	s_add_u32 s56, s56, 0x100
	s_addc_u32 s57, s57, 0
	s_cmp_ge_u32 s53, s81
	s_mov_b32 s51, s53
	s_cbranch_scc0 .LBB0_991
	s_and_b64 vcc, exec, s[26:27]
	s_cbranch_vccnz .LBB0_1001
	s_bitcmp0_b32 s67, 1
	s_mov_b64 s[56:57], -1
	v_lshl_add_u32 v142, s14, 8, v156
	s_cbranch_scc0 .LBB0_1002

; #define PG8_STAGE(bufoff, gbase, voff) do { _Pragma("unroll") for (int _i = 0; _i < 2; ++_i) { unsigned keep_; \
;         asm volatile("s_mov_b32 %0, m0\n\ts_mov_b32 m0, %3\n\ts_nop 0\n\tglobal_load_lds_dwordx4 %1, %2\n\ts_mov_b32 m0, %0" : "=&s"(keep_) : "v"((voff)[_i]), "s"((const char*)(gbase)), "s"(ldsbase + (unsigned)((bufoff) + _i * 8192)) : "memory"); } } while (0)
; #define PG8_WAIT_V(n) asm volatile("s_waitcnt vmcnt(" #n ")" ::: "memory")
; #define PG8_WAIT_L(n) asm volatile("s_waitcnt lgkmcnt(" #n ")" ::: "memory")
; #define PG8_BAR __builtin_amdgcn_s_barrier()
; #define PG8_SCHED __builtin_amdgcn_sched_barrier(0)
; template <class Epi, class Sched, bool ALIGN_EPI, bool FP8 = false>
; DI void gemm_phase(LAS unsigned char* lds, const Gemm g, const Sched& S, const Epi& E) {
;     ...
;             PG8_LDB(B0, 0, 0); PG8_LDB(B1, 0, 1); PG8_SCHED; PG8_LDA(At, 0, 0); PG8_STAGE(PG8_SA(1, 1), a1 + hstepA, voffA);
;             PG8_WAIT_V(8); PG8_WAIT_L(0); PG8_BAR; PG8_MMA(0, 0, At, B0); PG8_MMA(0, 1, At, B1); PG8_BAR; PG8_SCHED;
;             PG8_LDA(At, 0, 1); PG8_STAGE(PG8_SB(0, 0), b2, voffB); PG8_STAGE(PG8_SB(0, 1), b2 + hstepB, voffB); PG8_STAGE(PG8_SA(0, 0), a2, voffA);
;             PG8_WAIT_V(8); PG8_WAIT_L(0); PG8_BAR; PG8_MMA(1, 0, At, B0); PG8_MMA(1, 1, At, B1); PG8_BAR; PG8_SCHED;
.LBB0_1608:
	ds_read_b128 v[144:147], v133
	ds_read_b128 v[148:151], v133 offset:16
	ds_read_b128 v[152:155], v133 offset:2048
	ds_read_b128 v[156:159], v133 offset:2064
	ds_read_b128 v[160:163], v133 offset:16384
	ds_read_b128 v[164:167], v133 offset:16400
	ds_read_b128 v[168:171], v133 offset:18432
	ds_read_b128 v[172:175], v133 offset:18448
	s_add_u32 s6, s26, 0x100
	s_addc_u32 s7, s27, 0
	s_cmp_eq_u32 s70, 12
	s_cselect_b32 s42, s17, s6
	s_cselect_b32 s43, s15, s7
	s_cselect_b32 s40, s18, s68
	s_cselect_b32 s41, s19, s69
	s_add_u32 s28, s42, 0x80
	s_addc_u32 s29, s43, 0
	ds_read_b128 v[176:179], v132
	ds_read_b128 v[180:183], v132 offset:16
	ds_read_b128 v[184:187], v132 offset:2048
	ds_read_b128 v[188:191], v132 offset:2064
	ds_read_b128 v[192:195], v132 offset:4096
	ds_read_b128 v[196:199], v132 offset:4112
	ds_read_b128 v[200:203], v132 offset:6144
	ds_read_b128 v[204:207], v132 offset:6160
	s_add_u32 s26, s26, 0x40080
	s_addc_u32 s27, s27, 0
	s_mov_b32 s71, m0
	s_mov_b32 m0, s62
	s_nop 0
	global_load_lds_dwordx4 v134, s[26:27]
	s_mov_b32 m0, s71
	s_nop 0
	s_mov_b32 s71, m0
	s_mov_b32 m0, s63
	s_nop 0
	global_load_lds_dwordx4 v136, s[26:27]
	s_mov_b32 m0, s71
	s_waitcnt vmcnt(8)
	s_waitcnt lgkmcnt(0)
	s_barrier
	s_setprio 1
	v_mfma_scale_f32_16x16x128_f8f6f4 v[124:127], v[144:151], v[176:183], v[124:127], v140, v140 op_sel_hi:[0,0,0]
	v_mfma_scale_f32_16x16x128_f8f6f4 v[120:123], v[152:159], v[176:183], v[120:123], v140, v140 op_sel_hi:[0,0,0]
	v_mfma_scale_f32_16x16x128_f8f6f4 v[108:111], v[144:151], v[184:191], v[108:111], v140, v140 op_sel_hi:[0,0,0]
	v_mfma_scale_f32_16x16x128_f8f6f4 v[104:107], v[152:159], v[184:191], v[104:107], v140, v140 op_sel_hi:[0,0,0]
	v_mfma_scale_f32_16x16x128_f8f6f4 v[208:211], v[144:151], v[192:199], v[92:95], v140, v140 op_sel_hi:[0,0,0]
	v_mfma_scale_f32_16x16x128_f8f6f4 v[212:215], v[152:159], v[192:199], v[88:91], v140, v140 op_sel_hi:[0,0,0]
	v_mfma_scale_f32_16x16x128_f8f6f4 v[216:219], v[144:151], v[200:207], v[76:79], v140, v140 op_sel_hi:[0,0,0]
	v_mfma_scale_f32_16x16x128_f8f6f4 v[220:223], v[152:159], v[200:207], v[72:75], v140, v140 op_sel_hi:[0,0,0]
	v_mfma_scale_f32_16x16x128_f8f6f4 v[116:119], v[160:167], v[176:183], v[116:119], v141, v140 op_sel_hi:[0,0,0]
	v_mfma_scale_f32_16x16x128_f8f6f4 v[112:115], v[168:175], v[176:183], v[112:115], v141, v140 op_sel_hi:[0,0,0]
	v_mfma_scale_f32_16x16x128_f8f6f4 v[100:103], v[160:167], v[184:191], v[100:103], v141, v140 op_sel_hi:[0,0,0]
	v_mfma_scale_f32_16x16x128_f8f6f4 v[96:99], v[168:175], v[184:191], v[96:99], v141, v140 op_sel_hi:[0,0,0]
	v_mfma_scale_f32_16x16x128_f8f6f4 v[176:179], v[160:167], v[192:199], v[84:87], v141, v140 op_sel_hi:[0,0,0]
	v_mfma_scale_f32_16x16x128_f8f6f4 v[180:183], v[168:175], v[192:199], v[80:83], v141, v140 op_sel_hi:[0,0,0]
	v_mfma_scale_f32_16x16x128_f8f6f4 v[184:187], v[160:167], v[200:207], v[68:71], v141, v140 op_sel_hi:[0,0,0]
	v_mfma_scale_f32_16x16x128_f8f6f4 v[188:191], v[168:175], v[200:207], v[64:67], v141, v140 op_sel_hi:[0,0,0]
	s_setprio 0
	s_barrier
	s_nop 4
	ds_read_b128 v[64:67], v132 offset:16384
	ds_read_b128 v[68:71], v132 offset:16400
	ds_read_b128 v[72:75], v132 offset:18432
	ds_read_b128 v[76:79], v132 offset:18448
	ds_read_b128 v[80:83], v132 offset:20480
	ds_read_b128 v[84:87], v132 offset:20496
	ds_read_b128 v[88:91], v132 offset:22528
	ds_read_b128 v[92:95], v132 offset:22544
	s_mov_b32 s26, m0
	s_mov_b32 m0, s23
	s_nop 0
	global_load_lds_dwordx4 v135, s[40:41]
	s_mov_b32 m0, s26
	s_nop 0
	s_mov_b32 s26, m0
	s_mov_b32 m0, s25
	s_nop 0
	global_load_lds_dwordx4 v137, s[40:41]
	s_mov_b32 m0, s26
	s_add_u32 s26, s40, 0x40000
	s_addc_u32 s27, s41, 0
	s_mov_b32 s71, m0
	s_mov_b32 m0, s48
	s_nop 0
	global_load_lds_dwordx4 v135, s[26:27]
	s_mov_b32 m0, s71
	s_nop 0
	s_mov_b32 s71, m0
	s_mov_b32 m0, s49
	s_nop 0
	global_load_lds_dwordx4 v137, s[26:27]
	s_mov_b32 m0, s71
	s_mov_b32 s26, m0
	s_mov_b32 m0, s44
	s_nop 0
	global_load_lds_dwordx4 v134, s[42:43]
	s_mov_b32 m0, s26
	s_nop 0
	s_mov_b32 s26, m0
	s_mov_b32 m0, s50
	s_nop 0
	global_load_lds_dwordx4 v136, s[42:43]
	s_mov_b32 m0, s26
	s_waitcnt vmcnt(8)
	s_waitcnt lgkmcnt(0)
	s_barrier
	s_setprio 1
	v_mfma_scale_f32_16x16x128_f8f6f4 v[60:63], v[144:151], v[64:71], v[60:63], v140, v140 op_sel_hi:[0,0,0]
	v_mfma_scale_f32_16x16x128_f8f6f4 v[56:59], v[152:159], v[64:71], v[56:59], v140, v140 op_sel_hi:[0,0,0]
	v_mfma_scale_f32_16x16x128_f8f6f4 v[192:195], v[144:151], v[72:79], v[44:47], v140, v140 op_sel_hi:[0,0,0]
	v_mfma_scale_f32_16x16x128_f8f6f4 v[196:199], v[152:159], v[72:79], v[40:43], v140, v140 op_sel_hi:[0,0,0]
	v_mfma_scale_f32_16x16x128_f8f6f4 v[200:203], v[144:151], v[80:87], v[28:31], v140, v140 op_sel_hi:[0,0,0]
	v_mfma_scale_f32_16x16x128_f8f6f4 v[204:207], v[152:159], v[80:87], v[24:27], v140, v140 op_sel_hi:[0,0,0]
	v_mfma_scale_f32_16x16x128_f8f6f4 v[224:227], v[144:151], v[88:95], v[12:15], v140, v140 op_sel_hi:[0,0,0]
	v_mfma_scale_f32_16x16x128_f8f6f4 v[228:231], v[152:159], v[88:95], v[8:11], v140, v140 op_sel_hi:[0,0,0]
	v_mfma_scale_f32_16x16x128_f8f6f4 v[52:55], v[160:167], v[64:71], v[52:55], v141, v140 op_sel_hi:[0,0,0]
	v_mfma_scale_f32_16x16x128_f8f6f4 v[48:51], v[168:175], v[64:71], v[48:51], v141, v140 op_sel_hi:[0,0,0]
	v_mfma_scale_f32_16x16x128_f8f6f4 v[232:235], v[160:167], v[72:79], v[36:39], v141, v140 op_sel_hi:[0,0,0]
	v_mfma_scale_f32_16x16x128_f8f6f4 v[236:239], v[168:175], v[72:79], v[32:35], v141, v140 op_sel_hi:[0,0,0]
	v_mfma_scale_f32_16x16x128_f8f6f4 v[240:243], v[160:167], v[80:87], v[20:23], v141, v140 op_sel_hi:[0,0,0]
	v_mfma_scale_f32_16x16x128_f8f6f4 v[244:247], v[168:175], v[80:87], v[16:19], v141, v140 op_sel_hi:[0,0,0]
	v_mfma_scale_f32_16x16x128_f8f6f4 v[248:251], v[160:167], v[88:95], v[4:7], v141, v140 op_sel_hi:[0,0,0]
	v_mfma_scale_f32_16x16x128_f8f6f4 v[128:131], v[168:175], v[88:95], v[0:3], v141, v140 op_sel_hi:[0,0,0]
	s_setprio 0
	s_barrier
; #define PG8_STAGE(bufoff, gbase, voff) do { _Pragma("unroll") for (int _i = 0; _i < 2; ++_i) { unsigned keep_; \
;         asm volatile("s_mov_b32 %0, m0\n\ts_mov_b32 m0, %3\n\ts_nop 0\n\tglobal_load_lds_dwordx4 %1, %2\n\ts_mov_b32 m0, %0" : "=&s"(keep_) : "v"((voff)[_i]), "s"((const char*)(gbase)), "s"(ldsbase + (unsigned)((bufoff) + _i * 8192)) : "memory"); } } while (0)
; #define PG8_WAIT_V(n) asm volatile("s_waitcnt vmcnt(" #n ")" ::: "memory")
; #define PG8_WAIT_L(n) asm volatile("s_waitcnt lgkmcnt(" #n ")" ::: "memory")
; #define PG8_BAR __builtin_amdgcn_s_barrier()
; #define PG8_SCHED __builtin_amdgcn_sched_barrier(0)
; template <class Epi, class Sched, bool ALIGN_EPI, bool FP8 = false>
; DI void gemm_phase(LAS unsigned char* lds, const Gemm g, const Sched& S, const Epi& E) {
;     ...
;             PG8_LDB(B0, 1, 0); PG8_LDB(B1, 1, 1); PG8_SCHED; PG8_LDA(At, 1, 0); PG8_STAGE(PG8_SA(0, 1), a2 + hstepA, voffA);
;             PG8_WAIT_V(8); PG8_WAIT_L(0); PG8_BAR; PG8_MMA(0, 0, At, B0); PG8_MMA(0, 1, At, B1); PG8_BAR; PG8_SCHED;
;             PG8_LDA(At, 1, 1); PG8_STAGE(PG8_SB(1, 0), b3, voffB); PG8_STAGE(PG8_SB(1, 1), b3 + hstepB, voffB); PG8_STAGE(PG8_SA(1, 0), a3, voffA);
;             PG8_WAIT_V(8); PG8_WAIT_L(0); PG8_BAR; PG8_MMA(1, 0, At, B0); PG8_MMA(1, 1, At, B1); PG8_BAR; PG8_SCHED;
;         }
;         if constexpr (ALIGN_EPI) { if (wr == 0) PG8_BAR; }
;         E(acc, cur, wr, wc, fr, fq);
;         if (!has_next) break;
	s_nop 4
	ds_read_b128 v[0:3], v133 offset:32768
	ds_read_b128 v[4:7], v133 offset:32784
	ds_read_b128 v[16:19], v133 offset:34816
	ds_read_b128 v[20:23], v133 offset:34832
	ds_read_b128 v[144:147], v133 offset:49152
	ds_read_b128 v[148:151], v133 offset:49168
	ds_read_b128 v[152:155], v133 offset:51200
	ds_read_b128 v[156:159], v133 offset:51216
	ds_read_b128 v[8:11], v132 offset:32768
	ds_read_b128 v[12:15], v132 offset:32784
	ds_read_b128 v[24:27], v132 offset:34816
	ds_read_b128 v[28:31], v132 offset:34832
	ds_read_b128 v[32:35], v132 offset:36864
	ds_read_b128 v[36:39], v132 offset:36880
	ds_read_b128 v[40:43], v132 offset:38912
	ds_read_b128 v[44:47], v132 offset:38928
	s_add_u32 s26, s42, 0x40000
	s_addc_u32 s27, s43, 0
	s_mov_b32 s42, m0
	s_mov_b32 m0, s51
	s_nop 0
	global_load_lds_dwordx4 v134, s[26:27]
	s_mov_b32 m0, s42
	s_nop 0
	s_mov_b32 s42, m0
	s_mov_b32 m0, s52
	s_nop 0
	global_load_lds_dwordx4 v136, s[26:27]
	s_mov_b32 m0, s42
	s_waitcnt vmcnt(8)
	s_waitcnt lgkmcnt(0)
	s_barrier
	s_setprio 1
	v_mfma_scale_f32_16x16x128_f8f6f4 v[124:127], v[0:7], v[8:15], v[124:127], v140, v140 op_sel_hi:[0,0,0]
	v_mfma_scale_f32_16x16x128_f8f6f4 v[120:123], v[16:23], v[8:15], v[120:123], v140, v140 op_sel_hi:[0,0,0]
	v_mfma_scale_f32_16x16x128_f8f6f4 v[108:111], v[0:7], v[24:31], v[108:111], v140, v140 op_sel_hi:[0,0,0]
	v_mfma_scale_f32_16x16x128_f8f6f4 v[104:107], v[16:23], v[24:31], v[104:107], v140, v140 op_sel_hi:[0,0,0]
	v_mfma_scale_f32_16x16x128_f8f6f4 v[92:95], v[0:7], v[32:39], v[208:211], v140, v140 op_sel_hi:[0,0,0]
	v_mfma_scale_f32_16x16x128_f8f6f4 v[88:91], v[16:23], v[32:39], v[212:215], v140, v140 op_sel_hi:[0,0,0]
	v_mfma_scale_f32_16x16x128_f8f6f4 v[76:79], v[0:7], v[40:47], v[216:219], v140, v140 op_sel_hi:[0,0,0]
	v_mfma_scale_f32_16x16x128_f8f6f4 v[72:75], v[16:23], v[40:47], v[220:223], v140, v140 op_sel_hi:[0,0,0]
	v_mfma_scale_f32_16x16x128_f8f6f4 v[116:119], v[144:151], v[8:15], v[116:119], v141, v140 op_sel_hi:[0,0,0]
	v_mfma_scale_f32_16x16x128_f8f6f4 v[112:115], v[152:159], v[8:15], v[112:115], v141, v140 op_sel_hi:[0,0,0]
	v_mfma_scale_f32_16x16x128_f8f6f4 v[100:103], v[144:151], v[24:31], v[100:103], v141, v140 op_sel_hi:[0,0,0]
	v_mfma_scale_f32_16x16x128_f8f6f4 v[96:99], v[152:159], v[24:31], v[96:99], v141, v140 op_sel_hi:[0,0,0]
	v_mfma_scale_f32_16x16x128_f8f6f4 v[84:87], v[144:151], v[32:39], v[176:179], v141, v140 op_sel_hi:[0,0,0]
	v_mfma_scale_f32_16x16x128_f8f6f4 v[80:83], v[152:159], v[32:39], v[180:183], v141, v140 op_sel_hi:[0,0,0]
	v_mfma_scale_f32_16x16x128_f8f6f4 v[68:71], v[144:151], v[40:47], v[184:187], v141, v140 op_sel_hi:[0,0,0]
	v_mfma_scale_f32_16x16x128_f8f6f4 v[64:67], v[152:159], v[40:47], v[188:191], v141, v140 op_sel_hi:[0,0,0]
	s_setprio 0
	s_barrier
	ds_read_b128 v[32:35], v132 offset:49152
	ds_read_b128 v[36:39], v132 offset:49168
	ds_read_b128 v[160:163], v132 offset:51200
	ds_read_b128 v[164:167], v132 offset:51216
	ds_read_b128 v[168:171], v132 offset:53248
	ds_read_b128 v[172:175], v132 offset:53264
	ds_read_b128 v[176:179], v132 offset:55296
	ds_read_b128 v[180:183], v132 offset:55312
	s_add_u32 s26, s40, 0x80
	s_addc_u32 s27, s41, 0
	s_mov_b32 s42, m0
	s_mov_b32 m0, s56
	s_nop 0
	global_load_lds_dwordx4 v135, s[26:27]
	s_mov_b32 m0, s42
	s_nop 0
	s_mov_b32 s42, m0
	s_mov_b32 m0, s57
	s_nop 0
	global_load_lds_dwordx4 v137, s[26:27]
	s_mov_b32 m0, s42
	s_add_u32 s26, s40, 0x40080
	s_addc_u32 s27, s41, 0
	s_mov_b32 s40, m0
	s_mov_b32 m0, s60
	s_nop 0
	global_load_lds_dwordx4 v135, s[26:27]
	s_mov_b32 m0, s40
	s_nop 0
	s_mov_b32 s40, m0
	s_mov_b32 m0, s61
	s_nop 0
	global_load_lds_dwordx4 v137, s[26:27]
	s_mov_b32 m0, s40
	s_mov_b32 s26, m0
	s_mov_b32 m0, s58
	s_nop 0
	global_load_lds_dwordx4 v134, s[28:29]
	s_mov_b32 m0, s26
	s_nop 0
	s_mov_b32 s26, m0
	s_mov_b32 m0, s59
	s_nop 0
	global_load_lds_dwordx4 v136, s[28:29]
	s_mov_b32 m0, s26
	s_waitcnt vmcnt(8)
	s_waitcnt lgkmcnt(0)
	s_barrier
	s_setprio 1
	v_mfma_scale_f32_16x16x128_f8f6f4 v[60:63], v[0:7], v[32:39], v[60:63], v140, v140 op_sel_hi:[0,0,0]
	v_mfma_scale_f32_16x16x128_f8f6f4 v[56:59], v[16:23], v[32:39], v[56:59], v140, v140 op_sel_hi:[0,0,0]
	v_mfma_scale_f32_16x16x128_f8f6f4 v[44:47], v[0:7], v[160:167], v[192:195], v140, v140 op_sel_hi:[0,0,0]
	v_mfma_scale_f32_16x16x128_f8f6f4 v[40:43], v[16:23], v[160:167], v[196:199], v140, v140 op_sel_hi:[0,0,0]
	v_mfma_scale_f32_16x16x128_f8f6f4 v[28:31], v[0:7], v[168:175], v[200:203], v140, v140 op_sel_hi:[0,0,0]
	v_mfma_scale_f32_16x16x128_f8f6f4 v[24:27], v[16:23], v[168:175], v[204:207], v140, v140 op_sel_hi:[0,0,0]
	v_mfma_scale_f32_16x16x128_f8f6f4 v[12:15], v[0:7], v[176:183], v[224:227], v140, v140 op_sel_hi:[0,0,0]
	v_mfma_scale_f32_16x16x128_f8f6f4 v[8:11], v[16:23], v[176:183], v[228:231], v140, v140 op_sel_hi:[0,0,0]
	v_mfma_scale_f32_16x16x128_f8f6f4 v[52:55], v[144:151], v[32:39], v[52:55], v141, v140 op_sel_hi:[0,0,0]
	v_mfma_scale_f32_16x16x128_f8f6f4 v[48:51], v[152:159], v[32:39], v[48:51], v141, v140 op_sel_hi:[0,0,0]
	v_mfma_scale_f32_16x16x128_f8f6f4 v[36:39], v[144:151], v[160:167], v[232:235], v141, v140 op_sel_hi:[0,0,0]
	v_mfma_scale_f32_16x16x128_f8f6f4 v[32:35], v[152:159], v[160:167], v[236:239], v141, v140 op_sel_hi:[0,0,0]
	v_mfma_scale_f32_16x16x128_f8f6f4 v[20:23], v[144:151], v[168:175], v[240:243], v141, v140 op_sel_hi:[0,0,0]
	v_mfma_scale_f32_16x16x128_f8f6f4 v[16:19], v[152:159], v[168:175], v[244:247], v141, v140 op_sel_hi:[0,0,0]
	v_mfma_scale_f32_16x16x128_f8f6f4 v[4:7], v[144:151], v[176:183], v[248:251], v141, v140 op_sel_hi:[0,0,0]
	v_mfma_scale_f32_16x16x128_f8f6f4 v[0:3], v[152:159], v[176:183], v[128:131], v141, v140 op_sel_hi:[0,0,0]
	s_setprio 0
	s_barrier
	s_add_i32 s70, s70, 2
	s_add_u32 s68, s68, 0x100
	s_addc_u32 s69, s69, 0
	s_cmp_gt_u32 s70, 13
	s_mov_b64 s[26:27], s[6:7]
	s_cbranch_scc0 .LBB0_1608
	s_and_b64 vcc, exec, s[12:13]
	s_cbranch_vccz .LBB0_1611
	s_barrier

; #define PG8_STAGE(bufoff, gbase, voff) do { _Pragma("unroll") for (int _i = 0; _i < 2; ++_i) { unsigned keep_; \
;         asm volatile("s_mov_b32 %0, m0\n\ts_mov_b32 m0, %3\n\ts_nop 0\n\tglobal_load_lds_dwordx4 %1, %2\n\ts_mov_b32 m0, %0" : "=&s"(keep_) : "v"((voff)[_i]), "s"((const char*)(gbase)), "s"(ldsbase + (unsigned)((bufoff) + _i * 8192)) : "memory"); } } while (0)
; #define PG8_WAIT_V(n) asm volatile("s_waitcnt vmcnt(" #n ")" ::: "memory")
; #define PG8_WAIT_L(n) asm volatile("s_waitcnt lgkmcnt(" #n ")" ::: "memory")
; #define PG8_BAR __builtin_amdgcn_s_barrier()
; #define PG8_SCHED __builtin_amdgcn_sched_barrier(0)
;     DI int nt(const Unit& u) const { return (u.aux & 8) ? PLED / 64 : ((u.aux & 4) ? (D_ / 2) / 64 : D_ / 64); }
; template <class Epi, class Sched, bool ALIGN_EPI, bool FP8 = false>
; DI void gemm_phase(LAS unsigned char* lds, const Gemm g, const Sched& S, const Epi& E) {
;     ...
;         for (int t = 0; t < nt; t += 2) {
;             if constexpr (Epi::MID) { if (t == (nt >> 1)) E.mid(acc, cur, wr, wc, fr, fq); }
;             const bool last = (t == nt - 2);
;             const char* a1 = cA + (size_t)(t + 1) * kstep;
;             const char* a2 = last ? nA : cA + (size_t)(t + 2) * kstep; const char* b2 = last ? nB : cB + (size_t)(t + 2) * kstep;
;             const char* a3 = a2 + kstep; const char* b3 = b2 + kstep;
;             PG8_LDB(B0, 0, 0); PG8_LDB(B1, 0, 1); PG8_SCHED; PG8_LDA(At, 0, 0); PG8_STAGE(PG8_SA(1, 1), a1 + hstepA, voffA);
;             PG8_WAIT_V(8); PG8_WAIT_L(0); PG8_BAR; PG8_MMA(0, 0, At, B0); PG8_MMA(0, 1, At, B1); PG8_BAR; PG8_SCHED;
;             PG8_LDA(At, 0, 1); PG8_STAGE(PG8_SB(0, 0), b2, voffB); PG8_STAGE(PG8_SB(0, 1), b2 + hstepB, voffB); PG8_STAGE(PG8_SA(0, 0), a2, voffA);
;             PG8_WAIT_V(8); PG8_WAIT_L(0); PG8_BAR; PG8_MMA(1, 0, At, B0); PG8_MMA(1, 1, At, B1); PG8_BAR; PG8_SCHED;
.LBB0_1685:
	ds_read_b128 v[140:143], v131
	ds_read_b128 v[144:147], v131 offset:16
	ds_read_b128 v[148:151], v131 offset:2048
	ds_read_b128 v[152:155], v131 offset:2064
	ds_read_b128 v[156:159], v131 offset:16384
	ds_read_b128 v[160:163], v131 offset:16400
	ds_read_b128 v[164:167], v131 offset:18432
	ds_read_b128 v[168:171], v131 offset:18448
	s_add_u32 s46, s44, 0x100
	s_addc_u32 s47, s45, 0
	s_cmp_eq_u32 s92, 52
	s_cselect_b32 s52, s6, s46
	s_cselect_b32 s53, s7, s47
	s_cselect_b32 s50, s42, s90
	s_cselect_b32 s51, s43, s91
	s_add_u32 s48, s52, 0x80
	s_addc_u32 s49, s53, 0
	ds_read_b128 v[172:175], v130
	ds_read_b128 v[176:179], v130 offset:16
	ds_read_b128 v[180:183], v130 offset:2048
	ds_read_b128 v[184:187], v130 offset:2064
	ds_read_b128 v[188:191], v130 offset:4096
	ds_read_b128 v[192:195], v130 offset:4112
	ds_read_b128 v[196:199], v130 offset:6144
	ds_read_b128 v[200:203], v130 offset:6160
	s_add_u32 s44, s44, 0xe0080
	s_addc_u32 s45, s45, 0
	s_mov_b32 s93, m0
	s_mov_b32 m0, s73
	s_nop 0
	global_load_lds_dwordx4 v132, s[44:45]
	s_mov_b32 m0, s93
	s_nop 0
	s_mov_b32 s93, m0
	s_mov_b32 m0, s74
	s_nop 0
	global_load_lds_dwordx4 v134, s[44:45]
	s_mov_b32 m0, s93
	s_waitcnt vmcnt(8)
	s_waitcnt lgkmcnt(0)
	s_barrier
	s_setprio 1
	v_mfma_scale_f32_16x16x128_f8f6f4 v[124:127], v[140:147], v[172:179], v[124:127], v138, v138 op_sel_hi:[0,0,0]
	v_mfma_scale_f32_16x16x128_f8f6f4 v[120:123], v[148:155], v[172:179], v[120:123], v138, v138 op_sel_hi:[0,0,0]
	v_mfma_scale_f32_16x16x128_f8f6f4 v[116:119], v[140:147], v[180:187], v[116:119], v138, v138 op_sel_hi:[0,0,0]
	v_mfma_scale_f32_16x16x128_f8f6f4 v[112:115], v[148:155], v[180:187], v[112:115], v138, v138 op_sel_hi:[0,0,0]
	v_mfma_scale_f32_16x16x128_f8f6f4 v[100:103], v[140:147], v[188:195], v[100:103], v138, v138 op_sel_hi:[0,0,0]
	v_mfma_scale_f32_16x16x128_f8f6f4 v[96:99], v[148:155], v[188:195], v[96:99], v138, v138 op_sel_hi:[0,0,0]
	v_mfma_scale_f32_16x16x128_f8f6f4 v[204:207], v[140:147], v[196:203], v[84:87], v138, v138 op_sel_hi:[0,0,0]
	v_mfma_scale_f32_16x16x128_f8f6f4 v[208:211], v[148:155], v[196:203], v[80:83], v138, v138 op_sel_hi:[0,0,0]
	v_mfma_scale_f32_16x16x128_f8f6f4 v[108:111], v[156:163], v[172:179], v[108:111], v138, v138 op_sel_hi:[0,0,0]
	v_mfma_scale_f32_16x16x128_f8f6f4 v[104:107], v[164:171], v[172:179], v[104:107], v138, v138 op_sel_hi:[0,0,0]
	v_mfma_scale_f32_16x16x128_f8f6f4 v[172:175], v[156:163], v[180:187], v[92:95], v138, v138 op_sel_hi:[0,0,0]
	v_mfma_scale_f32_16x16x128_f8f6f4 v[176:179], v[164:171], v[180:187], v[88:91], v138, v138 op_sel_hi:[0,0,0]
	v_mfma_scale_f32_16x16x128_f8f6f4 v[180:183], v[156:163], v[188:195], v[76:79], v138, v138 op_sel_hi:[0,0,0]
	v_mfma_scale_f32_16x16x128_f8f6f4 v[184:187], v[164:171], v[188:195], v[72:75], v138, v138 op_sel_hi:[0,0,0]
	v_mfma_scale_f32_16x16x128_f8f6f4 v[188:191], v[156:163], v[196:203], v[68:71], v138, v138 op_sel_hi:[0,0,0]
	v_mfma_scale_f32_16x16x128_f8f6f4 v[192:195], v[164:171], v[196:203], v[64:67], v138, v138 op_sel_hi:[0,0,0]
	s_setprio 0
	s_barrier
	s_nop 4
	ds_read_b128 v[64:67], v130 offset:16384
	ds_read_b128 v[68:71], v130 offset:16400
	ds_read_b128 v[72:75], v130 offset:18432
	ds_read_b128 v[76:79], v130 offset:18448
	ds_read_b128 v[80:83], v130 offset:20480
	ds_read_b128 v[84:87], v130 offset:20496
	ds_read_b128 v[88:91], v130 offset:22528
	ds_read_b128 v[92:95], v130 offset:22544
	s_mov_b32 s44, m0
	s_mov_b32 m0, s57
	s_nop 0
	global_load_lds_dwordx4 v133, s[50:51]
	s_mov_b32 m0, s44
	s_nop 0
	s_mov_b32 s44, m0
	s_mov_b32 m0, s58
	s_nop 0
	global_load_lds_dwordx4 v135, s[50:51]
	s_mov_b32 m0, s44
	s_add_u32 s44, s50, 0xe0000
	s_addc_u32 s45, s51, 0
	s_mov_b32 s93, m0
	s_mov_b32 m0, s59
	s_nop 0
	global_load_lds_dwordx4 v133, s[44:45]
	s_mov_b32 m0, s93
	s_nop 0
	s_mov_b32 s93, m0
	s_mov_b32 m0, s60
	s_nop 0
	global_load_lds_dwordx4 v135, s[44:45]
	s_mov_b32 m0, s93
	s_mov_b32 s44, m0
	s_mov_b32 m0, s54
	s_nop 0
	global_load_lds_dwordx4 v132, s[52:53]
	s_mov_b32 m0, s44
	s_nop 0
	s_mov_b32 s44, m0
	s_mov_b32 m0, s61
	s_nop 0
	global_load_lds_dwordx4 v134, s[52:53]
	s_mov_b32 m0, s44
	s_waitcnt vmcnt(8)
	s_waitcnt lgkmcnt(0)
	s_barrier
	s_setprio 1
	v_mfma_scale_f32_16x16x128_f8f6f4 v[60:63], v[140:147], v[64:71], v[60:63], v138, v138 op_sel_hi:[0,0,0]
	v_mfma_scale_f32_16x16x128_f8f6f4 v[56:59], v[148:155], v[64:71], v[56:59], v138, v138 op_sel_hi:[0,0,0]
	v_mfma_scale_f32_16x16x128_f8f6f4 v[52:55], v[140:147], v[72:79], v[52:55], v138, v138 op_sel_hi:[0,0,0]
	v_mfma_scale_f32_16x16x128_f8f6f4 v[48:51], v[148:155], v[72:79], v[48:51], v138, v138 op_sel_hi:[0,0,0]
	v_mfma_scale_f32_16x16x128_f8f6f4 v[196:199], v[140:147], v[80:87], v[36:39], v138, v138 op_sel_hi:[0,0,0]
	v_mfma_scale_f32_16x16x128_f8f6f4 v[200:203], v[148:155], v[80:87], v[32:35], v138, v138 op_sel_hi:[0,0,0]
	v_mfma_scale_f32_16x16x128_f8f6f4 v[212:215], v[140:147], v[88:95], v[20:23], v138, v138 op_sel_hi:[0,0,0]
	v_mfma_scale_f32_16x16x128_f8f6f4 v[216:219], v[148:155], v[88:95], v[16:19], v138, v138 op_sel_hi:[0,0,0]
	v_mfma_scale_f32_16x16x128_f8f6f4 v[220:223], v[156:163], v[64:71], v[44:47], v138, v138 op_sel_hi:[0,0,0]
	v_mfma_scale_f32_16x16x128_f8f6f4 v[224:227], v[164:171], v[64:71], v[40:43], v138, v138 op_sel_hi:[0,0,0]
	v_mfma_scale_f32_16x16x128_f8f6f4 v[228:231], v[156:163], v[72:79], v[28:31], v138, v138 op_sel_hi:[0,0,0]
	v_mfma_scale_f32_16x16x128_f8f6f4 v[232:235], v[164:171], v[72:79], v[24:27], v138, v138 op_sel_hi:[0,0,0]
	v_mfma_scale_f32_16x16x128_f8f6f4 v[236:239], v[156:163], v[80:87], v[12:15], v138, v138 op_sel_hi:[0,0,0]
	v_mfma_scale_f32_16x16x128_f8f6f4 v[240:243], v[164:171], v[80:87], v[8:11], v138, v138 op_sel_hi:[0,0,0]
	v_mfma_scale_f32_16x16x128_f8f6f4 v[244:247], v[156:163], v[88:95], v[4:7], v138, v138 op_sel_hi:[0,0,0]
	v_mfma_scale_f32_16x16x128_f8f6f4 v[248:251], v[164:171], v[88:95], v[0:3], v138, v138 op_sel_hi:[0,0,0]
	s_setprio 0
	s_barrier
; #define PG8_STAGE(bufoff, gbase, voff) do { _Pragma("unroll") for (int _i = 0; _i < 2; ++_i) { unsigned keep_; \
;         asm volatile("s_mov_b32 %0, m0\n\ts_mov_b32 m0, %3\n\ts_nop 0\n\tglobal_load_lds_dwordx4 %1, %2\n\ts_mov_b32 m0, %0" : "=&s"(keep_) : "v"((voff)[_i]), "s"((const char*)(gbase)), "s"(ldsbase + (unsigned)((bufoff) + _i * 8192)) : "memory"); } } while (0)
; #define PG8_WAIT_V(n) asm volatile("s_waitcnt vmcnt(" #n ")" ::: "memory")
; #define PG8_WAIT_L(n) asm volatile("s_waitcnt lgkmcnt(" #n ")" ::: "memory")
; #define PG8_BAR __builtin_amdgcn_s_barrier()
; #define PG8_SCHED __builtin_amdgcn_sched_barrier(0)
; template <class Epi, class Sched, bool ALIGN_EPI, bool FP8 = false>
; DI void gemm_phase(LAS unsigned char* lds, const Gemm g, const Sched& S, const Epi& E) {
;     ...
;             PG8_LDB(B0, 1, 0); PG8_LDB(B1, 1, 1); PG8_SCHED; PG8_LDA(At, 1, 0); PG8_STAGE(PG8_SA(0, 1), a2 + hstepA, voffA);
;             PG8_WAIT_V(8); PG8_WAIT_L(0); PG8_BAR; PG8_MMA(0, 0, At, B0); PG8_MMA(0, 1, At, B1); PG8_BAR; PG8_SCHED;
;             PG8_LDA(At, 1, 1); PG8_STAGE(PG8_SB(1, 0), b3, voffB); PG8_STAGE(PG8_SB(1, 1), b3 + hstepB, voffB); PG8_STAGE(PG8_SA(1, 0), a3, voffA);
;             PG8_WAIT_V(8); PG8_WAIT_L(0); PG8_BAR; PG8_MMA(1, 0, At, B0); PG8_MMA(1, 1, At, B1); PG8_BAR; PG8_SCHED;
;         }
	s_nop 4
	ds_read_b128 v[0:3], v131 offset:32768
	ds_read_b128 v[4:7], v131 offset:32784
	ds_read_b128 v[8:11], v131 offset:34816
	ds_read_b128 v[12:15], v131 offset:34832
	ds_read_b128 v[140:143], v131 offset:49152
	ds_read_b128 v[144:147], v131 offset:49168
	ds_read_b128 v[148:151], v131 offset:51200
	ds_read_b128 v[152:155], v131 offset:51216
	ds_read_b128 v[16:19], v130 offset:32768
	ds_read_b128 v[20:23], v130 offset:32784
	ds_read_b128 v[24:27], v130 offset:34816
	ds_read_b128 v[28:31], v130 offset:34832
	ds_read_b128 v[32:35], v130 offset:36864
	ds_read_b128 v[36:39], v130 offset:36880
	ds_read_b128 v[40:43], v130 offset:38912
	ds_read_b128 v[44:47], v130 offset:38928
	s_add_u32 s44, s52, 0xe0000
	s_addc_u32 s45, s53, 0
	s_mov_b32 s52, m0
	s_mov_b32 m0, s62
	s_nop 0
	global_load_lds_dwordx4 v132, s[44:45]
	s_mov_b32 m0, s52
	s_nop 0
	s_mov_b32 s52, m0
	s_mov_b32 m0, s63
	s_nop 0
	global_load_lds_dwordx4 v134, s[44:45]
	s_mov_b32 m0, s52
	s_waitcnt vmcnt(8)
	s_waitcnt lgkmcnt(0)
	s_barrier
	s_setprio 1
	v_mfma_scale_f32_16x16x128_f8f6f4 v[124:127], v[0:7], v[16:23], v[124:127], v138, v138 op_sel_hi:[0,0,0]
	v_mfma_scale_f32_16x16x128_f8f6f4 v[120:123], v[8:15], v[16:23], v[120:123], v138, v138 op_sel_hi:[0,0,0]
	v_mfma_scale_f32_16x16x128_f8f6f4 v[116:119], v[0:7], v[24:31], v[116:119], v138, v138 op_sel_hi:[0,0,0]
	v_mfma_scale_f32_16x16x128_f8f6f4 v[112:115], v[8:15], v[24:31], v[112:115], v138, v138 op_sel_hi:[0,0,0]
	v_mfma_scale_f32_16x16x128_f8f6f4 v[100:103], v[0:7], v[32:39], v[100:103], v138, v138 op_sel_hi:[0,0,0]
	v_mfma_scale_f32_16x16x128_f8f6f4 v[96:99], v[8:15], v[32:39], v[96:99], v138, v138 op_sel_hi:[0,0,0]
	v_mfma_scale_f32_16x16x128_f8f6f4 v[84:87], v[0:7], v[40:47], v[204:207], v138, v138 op_sel_hi:[0,0,0]
	v_mfma_scale_f32_16x16x128_f8f6f4 v[80:83], v[8:15], v[40:47], v[208:211], v138, v138 op_sel_hi:[0,0,0]
	v_mfma_scale_f32_16x16x128_f8f6f4 v[108:111], v[140:147], v[16:23], v[108:111], v138, v138 op_sel_hi:[0,0,0]
	v_mfma_scale_f32_16x16x128_f8f6f4 v[104:107], v[148:155], v[16:23], v[104:107], v138, v138 op_sel_hi:[0,0,0]
	v_mfma_scale_f32_16x16x128_f8f6f4 v[92:95], v[140:147], v[24:31], v[172:175], v138, v138 op_sel_hi:[0,0,0]
	v_mfma_scale_f32_16x16x128_f8f6f4 v[88:91], v[148:155], v[24:31], v[176:179], v138, v138 op_sel_hi:[0,0,0]
	v_mfma_scale_f32_16x16x128_f8f6f4 v[76:79], v[140:147], v[32:39], v[180:183], v138, v138 op_sel_hi:[0,0,0]
	v_mfma_scale_f32_16x16x128_f8f6f4 v[72:75], v[148:155], v[32:39], v[184:187], v138, v138 op_sel_hi:[0,0,0]
	v_mfma_scale_f32_16x16x128_f8f6f4 v[68:71], v[140:147], v[40:47], v[188:191], v138, v138 op_sel_hi:[0,0,0]
	v_mfma_scale_f32_16x16x128_f8f6f4 v[64:67], v[148:155], v[40:47], v[192:195], v138, v138 op_sel_hi:[0,0,0]
	s_setprio 0
	s_barrier
	ds_read_b128 v[24:27], v130 offset:49152
	ds_read_b128 v[28:31], v130 offset:49168
	ds_read_b128 v[156:159], v130 offset:51200
	ds_read_b128 v[160:163], v130 offset:51216
	ds_read_b128 v[164:167], v130 offset:53248
	ds_read_b128 v[168:171], v130 offset:53264
	ds_read_b128 v[172:175], v130 offset:55296
	ds_read_b128 v[176:179], v130 offset:55312
	s_add_u32 s44, s50, 0x80
	s_addc_u32 s45, s51, 0
	s_mov_b32 s52, m0
	s_mov_b32 m0, s67
	s_nop 0
	global_load_lds_dwordx4 v133, s[44:45]
	s_mov_b32 m0, s52
	s_nop 0
	s_mov_b32 s52, m0
	s_mov_b32 m0, s68
	s_nop 0
	global_load_lds_dwordx4 v135, s[44:45]
	s_mov_b32 m0, s52
	s_add_u32 s44, s50, 0xe0080
	s_addc_u32 s45, s51, 0
	s_mov_b32 s50, m0
	s_mov_b32 m0, s71
	s_nop 0
	global_load_lds_dwordx4 v133, s[44:45]
	s_mov_b32 m0, s50
	s_nop 0
	s_mov_b32 s50, m0
	s_mov_b32 m0, s72
	s_nop 0
	global_load_lds_dwordx4 v135, s[44:45]
	s_mov_b32 m0, s50
	s_mov_b32 s44, m0
	s_mov_b32 m0, s69
	s_nop 0
	global_load_lds_dwordx4 v132, s[48:49]
	s_mov_b32 m0, s44
	s_nop 0
	s_mov_b32 s44, m0
	s_mov_b32 m0, s70
	s_nop 0
	global_load_lds_dwordx4 v134, s[48:49]
	s_mov_b32 m0, s44
	s_waitcnt vmcnt(8)
	s_waitcnt lgkmcnt(0)
	s_barrier
	s_setprio 1
	v_mfma_scale_f32_16x16x128_f8f6f4 v[60:63], v[0:7], v[24:31], v[60:63], v138, v138 op_sel_hi:[0,0,0]
	v_mfma_scale_f32_16x16x128_f8f6f4 v[56:59], v[8:15], v[24:31], v[56:59], v138, v138 op_sel_hi:[0,0,0]
	v_mfma_scale_f32_16x16x128_f8f6f4 v[52:55], v[0:7], v[156:163], v[52:55], v138, v138 op_sel_hi:[0,0,0]
	v_mfma_scale_f32_16x16x128_f8f6f4 v[48:51], v[8:15], v[156:163], v[48:51], v138, v138 op_sel_hi:[0,0,0]
	v_mfma_scale_f32_16x16x128_f8f6f4 v[36:39], v[0:7], v[164:171], v[196:199], v138, v138 op_sel_hi:[0,0,0]
	v_mfma_scale_f32_16x16x128_f8f6f4 v[32:35], v[8:15], v[164:171], v[200:203], v138, v138 op_sel_hi:[0,0,0]
	v_mfma_scale_f32_16x16x128_f8f6f4 v[20:23], v[0:7], v[172:179], v[212:215], v138, v138 op_sel_hi:[0,0,0]
	v_mfma_scale_f32_16x16x128_f8f6f4 v[16:19], v[8:15], v[172:179], v[216:219], v138, v138 op_sel_hi:[0,0,0]
	v_mfma_scale_f32_16x16x128_f8f6f4 v[44:47], v[140:147], v[24:31], v[220:223], v138, v138 op_sel_hi:[0,0,0]
	v_mfma_scale_f32_16x16x128_f8f6f4 v[40:43], v[148:155], v[24:31], v[224:227], v138, v138 op_sel_hi:[0,0,0]
	v_mfma_scale_f32_16x16x128_f8f6f4 v[28:31], v[140:147], v[156:163], v[228:231], v138, v138 op_sel_hi:[0,0,0]
	v_mfma_scale_f32_16x16x128_f8f6f4 v[24:27], v[148:155], v[156:163], v[232:235], v138, v138 op_sel_hi:[0,0,0]
	v_mfma_scale_f32_16x16x128_f8f6f4 v[12:15], v[140:147], v[164:171], v[236:239], v138, v138 op_sel_hi:[0,0,0]
	v_mfma_scale_f32_16x16x128_f8f6f4 v[8:11], v[148:155], v[164:171], v[240:243], v138, v138 op_sel_hi:[0,0,0]
	v_mfma_scale_f32_16x16x128_f8f6f4 v[4:7], v[140:147], v[172:179], v[244:247], v138, v138 op_sel_hi:[0,0,0]
	v_mfma_scale_f32_16x16x128_f8f6f4 v[0:3], v[148:155], v[172:179], v[248:251], v138, v138 op_sel_hi:[0,0,0]
	s_setprio 0
	s_barrier
	s_add_i32 s92, s92, 2
	s_add_u32 s90, s90, 0x100
	s_addc_u32 s91, s91, 0
	s_cmp_gt_u32 s92, 53
	s_mov_b64 s[44:45], s[46:47]
	s_cbranch_scc0 .LBB0_1685
	s_and_b64 vcc, exec, s[16:17]
	s_cbranch_vccz .LBB0_1688
	s_barrier

; #define PG8_STAGE(bufoff, gbase, voff) do { _Pragma("unroll") for (int _i = 0; _i < 2; ++_i) { unsigned keep_; \
;         asm volatile("s_mov_b32 %0, m0\n\ts_mov_b32 m0, %3\n\ts_nop 0\n\tglobal_load_lds_dwordx4 %1, %2\n\ts_mov_b32 m0, %0" : "=&s"(keep_) : "v"((voff)[_i]), "s"((const char*)(gbase)), "s"(ldsbase + (unsigned)((bufoff) + _i * 8192)) : "memory"); } } while (0)
; #define PG8_WAIT_V(n) asm volatile("s_waitcnt vmcnt(" #n ")" ::: "memory")
; #define PG8_WAIT_L(n) asm volatile("s_waitcnt lgkmcnt(" #n ")" ::: "memory")
; #define PG8_BAR __builtin_amdgcn_s_barrier()
; #define PG8_SCHED __builtin_amdgcn_sched_barrier(0)
;     DI int nt(const Unit& u) const { return (u.aux & 8) ? PLED / 64 : ((u.aux & 4) ? (D_ / 2) / 64 : D_ / 64); }
; template <class Epi, class Sched, bool ALIGN_EPI, bool FP8 = false>
; DI void gemm_phase(LAS unsigned char* lds, const Gemm g, const Sched& S, const Epi& E) {
;     ...
;         for (int t = 0; t < nt; t += 2) {
;             if constexpr (Epi::MID) { if (t == (nt >> 1)) E.mid(acc, cur, wr, wc, fr, fq); }
;             const bool last = (t == nt - 2);
;             const char* a1 = cA + (size_t)(t + 1) * kstep;
;             const char* a2 = last ? nA : cA + (size_t)(t + 2) * kstep; const char* b2 = last ? nB : cB + (size_t)(t + 2) * kstep;
;             const char* a3 = a2 + kstep; const char* b3 = b2 + kstep;
;             PG8_LDB(B0, 0, 0); PG8_LDB(B1, 0, 1); PG8_SCHED; PG8_LDA(At, 0, 0); PG8_STAGE(PG8_SA(1, 1), a1 + hstepA, voffA);
;             PG8_WAIT_V(8); PG8_WAIT_L(0); PG8_BAR; PG8_MMA(0, 0, At, B0); PG8_MMA(0, 1, At, B1); PG8_BAR; PG8_SCHED;
;             PG8_LDA(At, 0, 1); PG8_STAGE(PG8_SB(0, 0), b2, voffB); PG8_STAGE(PG8_SB(0, 1), b2 + hstepB, voffB); PG8_STAGE(PG8_SA(0, 0), a2, voffA);
.LBB0_1710:
	ds_read_b128 v[146:149], v140
	ds_read_b128 v[150:153], v140 offset:1024
	ds_read_b128 v[154:157], v140 offset:2048
	ds_read_b128 v[158:161], v140 offset:3072
	ds_read_b128 v[162:165], v141
	ds_read_b128 v[166:169], v141 offset:1024
	ds_read_b128 v[170:173], v141 offset:2048
	ds_read_b128 v[174:177], v141 offset:3072
	s_add_u32 s64, s62, 0x100
	s_addc_u32 s65, s63, 0
	s_cmp_eq_u32 vcc_lo, 28
	s_cselect_b32 s70, s94, s64
	s_cselect_b32 s71, s55, s65
	s_cselect_b32 s68, s95, s96
	s_cselect_b32 s69, s53, s97
	s_add_u32 s66, s70, 0x80
	s_addc_u32 s67, s71, 0
	ds_read_b128 v[178:181], v142
	ds_read_b128 v[182:185], v142 offset:1024
	ds_read_b128 v[186:189], v142 offset:2048
	ds_read_b128 v[190:193], v142 offset:3072
	ds_read_b128 v[194:197], v142 offset:4096
	ds_read_b128 v[198:201], v142 offset:5120
	ds_read_b128 v[202:205], v142 offset:6144
	ds_read_b128 v[206:209], v142 offset:7168
	s_add_u32 s62, s62, 0x80080
	s_addc_u32 s63, s63, 0
	s_mov_b32 vcc_hi, m0
	s_mov_b32 m0, s89
	s_nop 0
	global_load_lds_dwordx4 v134, s[62:63]
	s_mov_b32 m0, vcc_hi
	s_nop 0
	s_mov_b32 vcc_hi, m0
	s_mov_b32 m0, s90
	s_nop 0
	global_load_lds_dwordx4 v136, s[62:63]
	s_mov_b32 m0, vcc_hi
	s_waitcnt vmcnt(8)
	s_waitcnt lgkmcnt(0)
	s_barrier
	s_setprio 1
	v_mfma_f32_16x16x32_bf16 v[124:127], v[146:149], v[178:181], v[124:127]
	v_mfma_f32_16x16x32_bf16 v[120:123], v[154:157], v[178:181], v[120:123]
	v_mfma_f32_16x16x32_bf16 v[108:111], v[146:149], v[186:189], v[108:111]
	v_mfma_f32_16x16x32_bf16 v[104:107], v[154:157], v[186:189], v[104:107]
	v_mfma_f32_16x16x32_bf16 v[92:95], v[146:149], v[194:197], v[92:95]
	v_mfma_f32_16x16x32_bf16 v[88:91], v[154:157], v[194:197], v[88:91]
	v_mfma_f32_16x16x32_bf16 v[76:79], v[146:149], v[202:205], v[76:79]
	v_mfma_f32_16x16x32_bf16 v[72:75], v[154:157], v[202:205], v[72:75]
	v_mfma_f32_16x16x32_bf16 v[124:127], v[150:153], v[182:185], v[124:127]
	v_mfma_f32_16x16x32_bf16 v[120:123], v[158:161], v[182:185], v[120:123]
	v_mfma_f32_16x16x32_bf16 v[108:111], v[150:153], v[190:193], v[108:111]
	v_mfma_f32_16x16x32_bf16 v[104:107], v[158:161], v[190:193], v[104:107]
	v_mfma_f32_16x16x32_bf16 v[92:95], v[150:153], v[198:201], v[92:95]
	v_mfma_f32_16x16x32_bf16 v[88:91], v[158:161], v[198:201], v[88:91]
	v_mfma_f32_16x16x32_bf16 v[76:79], v[150:153], v[206:209], v[76:79]
	v_mfma_f32_16x16x32_bf16 v[72:75], v[158:161], v[206:209], v[72:75]
	v_mfma_f32_16x16x32_bf16 v[116:119], v[162:165], v[178:181], v[116:119]
	v_mfma_f32_16x16x32_bf16 v[112:115], v[170:173], v[178:181], v[112:115]
	v_mfma_f32_16x16x32_bf16 v[100:103], v[162:165], v[186:189], v[100:103]
	v_mfma_f32_16x16x32_bf16 v[96:99], v[170:173], v[186:189], v[96:99]
	v_mfma_f32_16x16x32_bf16 v[84:87], v[162:165], v[194:197], v[84:87]
	v_mfma_f32_16x16x32_bf16 v[80:83], v[170:173], v[194:197], v[80:83]
	v_mfma_f32_16x16x32_bf16 v[68:71], v[162:165], v[202:205], v[68:71]
	v_mfma_f32_16x16x32_bf16 v[64:67], v[170:173], v[202:205], v[64:67]
	v_mfma_f32_16x16x32_bf16 v[116:119], v[166:169], v[182:185], v[116:119]
	v_mfma_f32_16x16x32_bf16 v[112:115], v[174:177], v[182:185], v[112:115]
	v_mfma_f32_16x16x32_bf16 v[100:103], v[166:169], v[190:193], v[100:103]
	v_mfma_f32_16x16x32_bf16 v[96:99], v[174:177], v[190:193], v[96:99]
	v_mfma_f32_16x16x32_bf16 v[84:87], v[166:169], v[198:201], v[84:87]
	v_mfma_f32_16x16x32_bf16 v[80:83], v[174:177], v[198:201], v[80:83]
	v_mfma_f32_16x16x32_bf16 v[68:71], v[166:169], v[206:209], v[68:71]
	v_mfma_f32_16x16x32_bf16 v[64:67], v[174:177], v[206:209], v[64:67]
	s_setprio 0
	s_barrier
	ds_read_b128 v[178:181], v142 offset:16384
	ds_read_b128 v[182:185], v142 offset:17408
	ds_read_b128 v[186:189], v142 offset:18432
	ds_read_b128 v[190:193], v142 offset:19456
	ds_read_b128 v[194:197], v142 offset:20480
	ds_read_b128 v[198:201], v142 offset:21504
	ds_read_b128 v[202:205], v142 offset:22528
	ds_read_b128 v[206:209], v142 offset:23552
	s_mov_b32 s62, m0
	s_mov_b32 m0, s61
	s_nop 0
	global_load_lds_dwordx4 v135, s[68:69]
	s_mov_b32 m0, s62
	s_nop 0
	s_mov_b32 s62, m0
	s_mov_b32 m0, s75
	s_nop 0
	global_load_lds_dwordx4 v137, s[68:69]
	s_mov_b32 m0, s62
	s_add_u32 s62, s68, 0x80000
	s_addc_u32 s63, s69, 0
	s_mov_b32 vcc_hi, m0
	s_mov_b32 m0, s77
	s_nop 0
	global_load_lds_dwordx4 v135, s[62:63]
	s_mov_b32 m0, vcc_hi
	s_nop 0
	s_mov_b32 vcc_hi, m0
	s_mov_b32 m0, s79
	s_nop 0
	global_load_lds_dwordx4 v137, s[62:63]
	s_mov_b32 m0, vcc_hi
	s_mov_b32 s62, m0
	s_mov_b32 m0, s74
	s_nop 0
	global_load_lds_dwordx4 v134, s[70:71]
	s_mov_b32 m0, s62
	s_nop 0
	s_mov_b32 s62, m0
	s_mov_b32 m0, s80
	s_nop 0
	global_load_lds_dwordx4 v136, s[70:71]
	s_mov_b32 m0, s62
	s_waitcnt vmcnt(8)
	s_waitcnt lgkmcnt(0)
	s_barrier
; #define PG8_STAGE(bufoff, gbase, voff) do { _Pragma("unroll") for (int _i = 0; _i < 2; ++_i) { unsigned keep_; \
;         asm volatile("s_mov_b32 %0, m0\n\ts_mov_b32 m0, %3\n\ts_nop 0\n\tglobal_load_lds_dwordx4 %1, %2\n\ts_mov_b32 m0, %0" : "=&s"(keep_) : "v"((voff)[_i]), "s"((const char*)(gbase)), "s"(ldsbase + (unsigned)((bufoff) + _i * 8192)) : "memory"); } } while (0)
; #define PG8_WAIT_V(n) asm volatile("s_waitcnt vmcnt(" #n ")" ::: "memory")
; #define PG8_WAIT_L(n) asm volatile("s_waitcnt lgkmcnt(" #n ")" ::: "memory")
; #define PG8_BAR __builtin_amdgcn_s_barrier()
; #define PG8_SCHED __builtin_amdgcn_sched_barrier(0)
; template <class Epi, class Sched, bool ALIGN_EPI, bool FP8 = false>
; DI void gemm_phase(LAS unsigned char* lds, const Gemm g, const Sched& S, const Epi& E) {
;     ...
;             PG8_WAIT_V(8); PG8_WAIT_L(0); PG8_BAR; PG8_MMA(1, 0, At, B0); PG8_MMA(1, 1, At, B1); PG8_BAR; PG8_SCHED;
;             PG8_LDB(B0, 1, 0); PG8_LDB(B1, 1, 1); PG8_SCHED; PG8_LDA(At, 1, 0); PG8_STAGE(PG8_SA(0, 1), a2 + hstepA, voffA);
;             PG8_WAIT_V(8); PG8_WAIT_L(0); PG8_BAR; PG8_MMA(0, 0, At, B0); PG8_MMA(0, 1, At, B1); PG8_BAR; PG8_SCHED;
;             PG8_LDA(At, 1, 1); PG8_STAGE(PG8_SB(1, 0), b3, voffB); PG8_STAGE(PG8_SB(1, 1), b3 + hstepB, voffB); PG8_STAGE(PG8_SA(1, 0), a3, voffA);
	s_setprio 1
	v_mfma_f32_16x16x32_bf16 v[60:63], v[146:149], v[178:181], v[60:63]
	v_mfma_f32_16x16x32_bf16 v[56:59], v[154:157], v[178:181], v[56:59]
	v_mfma_f32_16x16x32_bf16 v[44:47], v[146:149], v[186:189], v[44:47]
	v_mfma_f32_16x16x32_bf16 v[40:43], v[154:157], v[186:189], v[40:43]
	v_mfma_f32_16x16x32_bf16 v[28:31], v[146:149], v[194:197], v[28:31]
	v_mfma_f32_16x16x32_bf16 v[24:27], v[154:157], v[194:197], v[24:27]
	v_mfma_f32_16x16x32_bf16 v[12:15], v[146:149], v[202:205], v[12:15]
	v_mfma_f32_16x16x32_bf16 v[8:11], v[154:157], v[202:205], v[8:11]
	v_mfma_f32_16x16x32_bf16 v[60:63], v[150:153], v[182:185], v[60:63]
	v_mfma_f32_16x16x32_bf16 v[56:59], v[158:161], v[182:185], v[56:59]
	v_mfma_f32_16x16x32_bf16 v[44:47], v[150:153], v[190:193], v[44:47]
	v_mfma_f32_16x16x32_bf16 v[40:43], v[158:161], v[190:193], v[40:43]
	v_mfma_f32_16x16x32_bf16 v[28:31], v[150:153], v[198:201], v[28:31]
	v_mfma_f32_16x16x32_bf16 v[24:27], v[158:161], v[198:201], v[24:27]
	v_mfma_f32_16x16x32_bf16 v[12:15], v[150:153], v[206:209], v[12:15]
	v_mfma_f32_16x16x32_bf16 v[8:11], v[158:161], v[206:209], v[8:11]
	v_mfma_f32_16x16x32_bf16 v[52:55], v[162:165], v[178:181], v[52:55]
	v_mfma_f32_16x16x32_bf16 v[48:51], v[170:173], v[178:181], v[48:51]
	v_mfma_f32_16x16x32_bf16 v[36:39], v[162:165], v[186:189], v[36:39]
	v_mfma_f32_16x16x32_bf16 v[32:35], v[170:173], v[186:189], v[32:35]
	v_mfma_f32_16x16x32_bf16 v[20:23], v[162:165], v[194:197], v[20:23]
	v_mfma_f32_16x16x32_bf16 v[16:19], v[170:173], v[194:197], v[16:19]
	v_mfma_f32_16x16x32_bf16 v[4:7], v[162:165], v[202:205], v[4:7]
	v_mfma_f32_16x16x32_bf16 v[0:3], v[170:173], v[202:205], v[0:3]
	v_mfma_f32_16x16x32_bf16 v[52:55], v[166:169], v[182:185], v[52:55]
	v_mfma_f32_16x16x32_bf16 v[48:51], v[174:177], v[182:185], v[48:51]
	v_mfma_f32_16x16x32_bf16 v[36:39], v[166:169], v[190:193], v[36:39]
	v_mfma_f32_16x16x32_bf16 v[32:35], v[174:177], v[190:193], v[32:35]
	v_mfma_f32_16x16x32_bf16 v[20:23], v[166:169], v[198:201], v[20:23]
	v_mfma_f32_16x16x32_bf16 v[16:19], v[174:177], v[198:201], v[16:19]
	v_mfma_f32_16x16x32_bf16 v[4:7], v[166:169], v[206:209], v[4:7]
	v_mfma_f32_16x16x32_bf16 v[0:3], v[174:177], v[206:209], v[0:3]
	s_setprio 0
	s_barrier
	ds_read_b128 v[146:149], v143
	ds_read_b128 v[150:153], v143 offset:1024
	ds_read_b128 v[154:157], v143 offset:2048
	ds_read_b128 v[158:161], v143 offset:3072
	ds_read_b128 v[162:165], v144
	ds_read_b128 v[166:169], v144 offset:1024
	ds_read_b128 v[170:173], v144 offset:2048
	ds_read_b128 v[174:177], v144 offset:3072
	ds_read_b128 v[178:181], v142 offset:32768
	ds_read_b128 v[182:185], v142 offset:33792
	ds_read_b128 v[186:189], v142 offset:34816
	ds_read_b128 v[190:193], v142 offset:35840
	ds_read_b128 v[194:197], v142 offset:36864
	ds_read_b128 v[198:201], v142 offset:37888
	ds_read_b128 v[202:205], v142 offset:38912
	ds_read_b128 v[206:209], v142 offset:39936
	s_add_u32 s62, s70, 0x80000
	s_addc_u32 s63, s71, 0
	s_mov_b32 s70, m0
	s_mov_b32 m0, s81
	s_nop 0
	global_load_lds_dwordx4 v134, s[62:63]
	s_mov_b32 m0, s70
	s_nop 0
	s_mov_b32 s70, m0
	s_mov_b32 m0, s82
	s_nop 0
	global_load_lds_dwordx4 v136, s[62:63]
	s_mov_b32 m0, s70
	s_waitcnt vmcnt(8)
	s_waitcnt lgkmcnt(0)
	s_barrier
	s_setprio 1
	v_mfma_f32_16x16x32_bf16 v[124:127], v[146:149], v[178:181], v[124:127]
	v_mfma_f32_16x16x32_bf16 v[120:123], v[154:157], v[178:181], v[120:123]
	v_mfma_f32_16x16x32_bf16 v[108:111], v[146:149], v[186:189], v[108:111]
	v_mfma_f32_16x16x32_bf16 v[104:107], v[154:157], v[186:189], v[104:107]
	v_mfma_f32_16x16x32_bf16 v[92:95], v[146:149], v[194:197], v[92:95]
	v_mfma_f32_16x16x32_bf16 v[88:91], v[154:157], v[194:197], v[88:91]
	v_mfma_f32_16x16x32_bf16 v[76:79], v[146:149], v[202:205], v[76:79]
	v_mfma_f32_16x16x32_bf16 v[72:75], v[154:157], v[202:205], v[72:75]
	v_mfma_f32_16x16x32_bf16 v[124:127], v[150:153], v[182:185], v[124:127]
	v_mfma_f32_16x16x32_bf16 v[120:123], v[158:161], v[182:185], v[120:123]
	v_mfma_f32_16x16x32_bf16 v[108:111], v[150:153], v[190:193], v[108:111]
	v_mfma_f32_16x16x32_bf16 v[104:107], v[158:161], v[190:193], v[104:107]
	v_mfma_f32_16x16x32_bf16 v[92:95], v[150:153], v[198:201], v[92:95]
	v_mfma_f32_16x16x32_bf16 v[88:91], v[158:161], v[198:201], v[88:91]
	v_mfma_f32_16x16x32_bf16 v[76:79], v[150:153], v[206:209], v[76:79]
	v_mfma_f32_16x16x32_bf16 v[72:75], v[158:161], v[206:209], v[72:75]
	v_mfma_f32_16x16x32_bf16 v[116:119], v[162:165], v[178:181], v[116:119]
	v_mfma_f32_16x16x32_bf16 v[112:115], v[170:173], v[178:181], v[112:115]
	v_mfma_f32_16x16x32_bf16 v[100:103], v[162:165], v[186:189], v[100:103]
	v_mfma_f32_16x16x32_bf16 v[96:99], v[170:173], v[186:189], v[96:99]
	v_mfma_f32_16x16x32_bf16 v[84:87], v[162:165], v[194:197], v[84:87]
	v_mfma_f32_16x16x32_bf16 v[80:83], v[170:173], v[194:197], v[80:83]
	v_mfma_f32_16x16x32_bf16 v[68:71], v[162:165], v[202:205], v[68:71]
	v_mfma_f32_16x16x32_bf16 v[64:67], v[170:173], v[202:205], v[64:67]
	v_mfma_f32_16x16x32_bf16 v[116:119], v[166:169], v[182:185], v[116:119]
	v_mfma_f32_16x16x32_bf16 v[112:115], v[174:177], v[182:185], v[112:115]
	v_mfma_f32_16x16x32_bf16 v[100:103], v[166:169], v[190:193], v[100:103]
	v_mfma_f32_16x16x32_bf16 v[96:99], v[174:177], v[190:193], v[96:99]
	v_mfma_f32_16x16x32_bf16 v[84:87], v[166:169], v[198:201], v[84:87]
	v_mfma_f32_16x16x32_bf16 v[80:83], v[174:177], v[198:201], v[80:83]
	v_mfma_f32_16x16x32_bf16 v[68:71], v[166:169], v[206:209], v[68:71]
	v_mfma_f32_16x16x32_bf16 v[64:67], v[174:177], v[206:209], v[64:67]
	s_setprio 0
	s_barrier
; #define PG8_STAGE(bufoff, gbase, voff) do { _Pragma("unroll") for (int _i = 0; _i < 2; ++_i) { unsigned keep_; \
;         asm volatile("s_mov_b32 %0, m0\n\ts_mov_b32 m0, %3\n\ts_nop 0\n\tglobal_load_lds_dwordx4 %1, %2\n\ts_mov_b32 m0, %0" : "=&s"(keep_) : "v"((voff)[_i]), "s"((const char*)(gbase)), "s"(ldsbase + (unsigned)((bufoff) + _i * 8192)) : "memory"); } } while (0)
; #define PG8_WAIT_V(n) asm volatile("s_waitcnt vmcnt(" #n ")" ::: "memory")
; #define PG8_WAIT_L(n) asm volatile("s_waitcnt lgkmcnt(" #n ")" ::: "memory")
; #define PG8_BAR __builtin_amdgcn_s_barrier()
; #define PG8_SCHED __builtin_amdgcn_sched_barrier(0)
; template <class Epi, class Sched, bool ALIGN_EPI, bool FP8 = false>
; DI void gemm_phase(LAS unsigned char* lds, const Gemm g, const Sched& S, const Epi& E) {
;     ...
;             PG8_LDA(At, 1, 1); PG8_STAGE(PG8_SB(1, 0), b3, voffB); PG8_STAGE(PG8_SB(1, 1), b3 + hstepB, voffB); PG8_STAGE(PG8_SA(1, 0), a3, voffA);
;             PG8_WAIT_V(8); PG8_WAIT_L(0); PG8_BAR; PG8_MMA(1, 0, At, B0); PG8_MMA(1, 1, At, B1); PG8_BAR; PG8_SCHED;
;         }
	ds_read_b128 v[178:181], v142 offset:49152
	ds_read_b128 v[182:185], v142 offset:50176
	ds_read_b128 v[186:189], v142 offset:51200
	ds_read_b128 v[190:193], v142 offset:52224
	ds_read_b128 v[194:197], v142 offset:53248
	ds_read_b128 v[198:201], v142 offset:54272
	ds_read_b128 v[202:205], v142 offset:55296
	ds_read_b128 v[206:209], v142 offset:56320
	s_add_u32 s62, s68, 0x80
	s_addc_u32 s63, s69, 0
	s_mov_b32 s70, m0
	s_mov_b32 m0, s83
	s_nop 0
	global_load_lds_dwordx4 v135, s[62:63]
	s_mov_b32 m0, s70
	s_nop 0
	s_mov_b32 s70, m0
	s_mov_b32 m0, s84
	s_nop 0
	global_load_lds_dwordx4 v137, s[62:63]
	s_mov_b32 m0, s70
	s_add_u32 s62, s68, 0x80080
	s_addc_u32 s63, s69, 0
	s_mov_b32 s68, m0
	s_mov_b32 m0, s87
	s_nop 0
	global_load_lds_dwordx4 v135, s[62:63]
	s_mov_b32 m0, s68
	s_nop 0
	s_mov_b32 s68, m0
	s_mov_b32 m0, s88
	s_nop 0
	global_load_lds_dwordx4 v137, s[62:63]
	s_mov_b32 m0, s68
	s_mov_b32 s62, m0
	s_mov_b32 m0, s85
	s_nop 0
	global_load_lds_dwordx4 v134, s[66:67]
	s_mov_b32 m0, s62
	s_nop 0
	s_mov_b32 s62, m0
	s_mov_b32 m0, s86
	s_nop 0
	global_load_lds_dwordx4 v136, s[66:67]
	s_mov_b32 m0, s62
	s_waitcnt vmcnt(8)
	s_waitcnt lgkmcnt(0)
	s_barrier
	s_setprio 1
	v_mfma_f32_16x16x32_bf16 v[60:63], v[146:149], v[178:181], v[60:63]
	v_mfma_f32_16x16x32_bf16 v[56:59], v[154:157], v[178:181], v[56:59]
	v_mfma_f32_16x16x32_bf16 v[44:47], v[146:149], v[186:189], v[44:47]
	v_mfma_f32_16x16x32_bf16 v[40:43], v[154:157], v[186:189], v[40:43]
	v_mfma_f32_16x16x32_bf16 v[28:31], v[146:149], v[194:197], v[28:31]
	v_mfma_f32_16x16x32_bf16 v[24:27], v[154:157], v[194:197], v[24:27]
	v_mfma_f32_16x16x32_bf16 v[12:15], v[146:149], v[202:205], v[12:15]
	v_mfma_f32_16x16x32_bf16 v[8:11], v[154:157], v[202:205], v[8:11]
	v_mfma_f32_16x16x32_bf16 v[60:63], v[150:153], v[182:185], v[60:63]
	v_mfma_f32_16x16x32_bf16 v[56:59], v[158:161], v[182:185], v[56:59]
	v_mfma_f32_16x16x32_bf16 v[44:47], v[150:153], v[190:193], v[44:47]
	v_mfma_f32_16x16x32_bf16 v[40:43], v[158:161], v[190:193], v[40:43]
	v_mfma_f32_16x16x32_bf16 v[28:31], v[150:153], v[198:201], v[28:31]
	v_mfma_f32_16x16x32_bf16 v[24:27], v[158:161], v[198:201], v[24:27]
	v_mfma_f32_16x16x32_bf16 v[12:15], v[150:153], v[206:209], v[12:15]
	v_mfma_f32_16x16x32_bf16 v[8:11], v[158:161], v[206:209], v[8:11]
	v_mfma_f32_16x16x32_bf16 v[52:55], v[162:165], v[178:181], v[52:55]
	v_mfma_f32_16x16x32_bf16 v[48:51], v[170:173], v[178:181], v[48:51]
	v_mfma_f32_16x16x32_bf16 v[36:39], v[162:165], v[186:189], v[36:39]
	v_mfma_f32_16x16x32_bf16 v[32:35], v[170:173], v[186:189], v[32:35]
	v_mfma_f32_16x16x32_bf16 v[20:23], v[162:165], v[194:197], v[20:23]
	v_mfma_f32_16x16x32_bf16 v[16:19], v[170:173], v[194:197], v[16:19]
	v_mfma_f32_16x16x32_bf16 v[4:7], v[162:165], v[202:205], v[4:7]
	v_mfma_f32_16x16x32_bf16 v[0:3], v[170:173], v[202:205], v[0:3]
	v_mfma_f32_16x16x32_bf16 v[52:55], v[166:169], v[182:185], v[52:55]
	v_mfma_f32_16x16x32_bf16 v[48:51], v[174:177], v[182:185], v[48:51]
	v_mfma_f32_16x16x32_bf16 v[36:39], v[166:169], v[190:193], v[36:39]
	v_mfma_f32_16x16x32_bf16 v[32:35], v[174:177], v[190:193], v[32:35]
	v_mfma_f32_16x16x32_bf16 v[20:23], v[166:169], v[198:201], v[20:23]
	v_mfma_f32_16x16x32_bf16 v[16:19], v[174:177], v[198:201], v[16:19]
	v_mfma_f32_16x16x32_bf16 v[4:7], v[166:169], v[206:209], v[4:7]
	v_mfma_f32_16x16x32_bf16 v[0:3], v[174:177], v[206:209], v[0:3]
	s_setprio 0
	s_barrier
	s_add_i32 vcc_lo, vcc_lo, 2
	s_add_u32 s96, s96, 0x100
	s_addc_u32 s97, s97, 0
	s_cmp_gt_u32 vcc_lo, 29
	s_mov_b64 s[62:63], s[64:65]
	s_cbranch_scc0 .LBB0_1710
	s_and_b64 vcc, exec, s[14:15]
	s_cbranch_vccz .LBB0_1713
	s_barrier
